# E2: the six pooling-row staging loads issued back to back (exec-masked) and drained with counted waits instead of load->wait->ds_write chains
# speedup vs baseline: 1.0252x; 1.0033x over previous
; #define LAS __attribute__((address_space(3)))
; __device__ __forceinline__ void phase_even_mix(CArgs a, LAS unsigned char* lds, int i2, int wv, int xw  ) {
;     ...
;             const float* lg = a->in[I_CLNG] + i2 * 512 + lane * 8; const float* lb = a->in[I_CLNB] + i2 * 512 + lane * 8;
;             const f32x4 g0 = *(const f32x4*)lg, g1 = *(const f32x4*)(lg + 4), b0 = *(const f32x4*)lb, b1 = *(const f32x4*)(lb + 4);
; #pragma unroll
;             for (int tt = 0; tt < 4; ++tt) { const int t = wave * 4 + tt;
;                 f32x4 v0 = *(const LAS f32x4*)(ybuf + t * 512 + lane * 8), v1 = *(const LAS f32x4*)(ybuf + t * 512 + lane * 8 + 4);
;                 const float mean = wave_sum((v0.x + v0.y) + (v0.z + v0.w) + (v1.x + v1.y) + (v1.z + v1.w), lane) * (1.f / 512.f);
;                 v0 = v0 - mean; v1 = v1 - mean;
;                 const float var = wave_sum((v0.x * v0.x + v0.y * v0.y) + (v0.z * v0.z + v0.w * v0.w) + (v1.x * v1.x + v1.y * v1.y) + (v1.z * v1.z + v1.w * v1.w), lane) * (1.f / 512.f);
;                 const float rstd = 1.0f / sqrtf(var + LN_EPS);
.LBB0_460:
	s_or_b64 exec, exec, s[16:17]
	s_xor_b64 s[68:69], s[12:13], -1
	v_readlane_b32 s12, v254, 29
	s_waitcnt vmcnt(0)
	s_or_b32 s12, s18, s12
	s_load_dwordx4 s[16:19], s[88:89], 0x20
	s_load_dwordx4 s[64:67], s[88:89], 0x40
	s_ashr_i32 s13, s12, 31
	s_lshl_b64 s[22:23], s[12:13], 5
	s_waitcnt lgkmcnt(0)
	s_add_u32 s12, s64, s86
	s_addc_u32 s13, s65, s87
	s_add_u32 s64, s66, s86
	s_addc_u32 s65, s67, s87
	global_load_dwordx4 v[8:11], v143, s[12:13] offset:16
	global_load_dwordx4 v[12:15], v143, s[12:13]
	global_load_dwordx4 v[0:3], v143, s[64:65] offset:16
	global_load_dwordx4 v[4:7], v143, s[64:65]
	global_load_dwordx4 v[200:203], v[36:37], off
	global_load_dwordx4 v[204:207], v[38:39], off
	global_load_dwordx4 v[208:211], v[40:41], off
	global_load_dwordx4 v[212:215], v[42:43], off
	global_load_dwordx4 v[216:219], v[36:37], off offset:64
	global_load_dwordx4 v[220:223], v[44:45], off
	global_load_dwordx4 v[224:227], v[46:47], off
	global_load_dwordx4 v[228:231], v[48:49], off
	global_load_dwordx4 v[232:235], v[36:37], off offset:128
	global_load_dwordx4 v[236:239], v[50:51], off
	global_load_dwordx4 v[240:243], v[52:53], off
	global_load_dwordx4 v[244:247], v[54:55], off
	global_load_dwordx4 v[248:251], v[36:37], off offset:192
	global_load_dwordx4 v[64:67], v[56:57], off
	global_load_dwordx4 v[178:181], v[58:59], off
	v_readlane_b32 s12, v255, 3
	s_mov_b32 s64, 32
	s_nop 0
	v_add_u32_e32 v20, s12, v62
	ds_read_b128 v[16:19], v20
	ds_read_b128 v[20:23], v20 offset:16
	s_waitcnt lgkmcnt(1)
	v_mov_b32_e32 v154, v17
	v_mov_b32_e32 v155, v18
	v_mov_b32_e32 v156, v16
	v_mov_b32_e32 v157, v19
	v_pk_add_f32 v[154:155], v[154:155], v[156:157]
	s_waitcnt lgkmcnt(0)
	v_mov_b32_e32 v156, v22
	v_mov_b32_e32 v157, v20
	v_mov_b32_e32 v158, v23
	v_mov_b32_e32 v159, v21
	v_pk_add_f32 v[156:157], v[156:157], v[158:159]
	v_add_f32_e32 v152, v154, v155
	v_add_f32_e32 v152, v152, v157
	v_add_f32_e32 v152, v156, v152
	s_waitcnt lgkmcnt(0)
	s_nop 1
	v_add_f32_dpp v152, v152, v152 quad_perm:[1,0,3,2] row_mask:0xf bank_mask:0xf
	s_nop 1
	v_add_f32_dpp v152, v152, v152 quad_perm:[2,3,0,1] row_mask:0xf bank_mask:0xf
	s_nop 1
	v_add_f32_dpp v152, v152, v152 row_half_mirror row_mask:0xf bank_mask:0xf
	s_nop 1
	v_add_f32_dpp v152, v152, v152 row_mirror row_mask:0xf bank_mask:0xf
	v_mov_b32_e32 v154, v152
	s_nop 1
	v_permlane16_swap_b32_e32 v154, v152
	v_add_f32_e32 v152, v152, v154
	v_mov_b32_e32 v154, v152
	s_nop 1
	v_permlane32_swap_b32_e32 v154, v152
	v_add_f32_e32 v152, v152, v154
	v_fmamk_f32 v19, v152, 0xbb000000, v19
	v_fmac_f32_e32 v17, 0xbb000000, v152
	v_fmamk_f32 v18, v152, 0xbb000000, v18
	v_fmamk_f32 v16, v152, 0xbb000000, v16
	v_fmamk_f32 v22, v152, 0xbb000000, v22
	v_fmamk_f32 v23, v152, 0xbb000000, v23
	v_fmamk_f32 v20, v152, 0xbb000000, v20
	v_fmac_f32_e32 v21, 0xbb000000, v152
	v_mul_f32_e32 v152, v17, v17
	v_mul_f32_e32 v154, v19, v19
	v_fmac_f32_e32 v152, v16, v16
	v_fmac_f32_e32 v154, v18, v18
	v_add_f32_e32 v152, v152, v154
	v_mul_f32_e32 v154, v21, v21
	v_fmac_f32_e32 v154, v20, v20
	v_add_f32_e32 v152, v154, v152
	v_mul_f32_e32 v154, v23, v23
	v_fmac_f32_e32 v154, v22, v22
	v_add_f32_e32 v152, v154, v152
	s_waitcnt lgkmcnt(0)
	s_nop 1
	v_add_f32_dpp v152, v152, v152 quad_perm:[1,0,3,2] row_mask:0xf bank_mask:0xf
	s_nop 1
	v_add_f32_dpp v152, v152, v152 quad_perm:[2,3,0,1] row_mask:0xf bank_mask:0xf
	s_nop 1
	v_add_f32_dpp v152, v152, v152 row_half_mirror row_mask:0xf bank_mask:0xf
	s_nop 1
	v_add_f32_dpp v152, v152, v152 row_mirror row_mask:0xf bank_mask:0xf
	v_mov_b32_e32 v154, v152
	s_nop 1
	v_permlane16_swap_b32_e32 v154, v152
	v_add_f32_e32 v152, v152, v154
	v_mov_b32_e32 v154, v152
	s_nop 1
	v_permlane32_swap_b32_e32 v154, v152
	v_add_f32_e32 v152, v152, v154
	v_fmamk_f32 v152, v152, 0x3b000000, v185
	v_cmp_gt_f32_e32 vcc, s55, v152
	v_mul_f32_e32 v154, 0x4f800000, v152
	s_nop 0
	v_cndmask_b32_e32 v152, v152, v154, vcc
	v_sqrt_f32_e32 v154, v152
	s_nop 0
	v_add_u32_e32 v155, -1, v154
	v_fma_f32 v156, -v155, v154, v152
	v_cmp_ge_f32_e64 s[12:13], 0, v156
	v_add_u32_e32 v156, 1, v154
	s_nop 0
	v_cndmask_b32_e64 v155, v154, v155, s[12:13]
	v_fma_f32 v154, -v156, v154, v152
	v_cmp_lt_f32_e64 s[12:13], 0, v154
	s_nop 1
	v_cndmask_b32_e64 v154, v155, v156, s[12:13]
	v_mul_f32_e32 v155, 0x37800000, v154
	v_cndmask_b32_e32 v154, v154, v155, vcc
	v_cmp_class_f32_e32 vcc, v152, v183
	s_nop 1
	v_cndmask_b32_e32 v152, v154, v152, vcc
	v_div_scale_f32 v154, s[12:13], v152, v152, 1.0
	v_rcp_f32_e32 v155, v154
	s_add_u32 s12, s22, s79
	v_readlane_b32 s13, v255, 4
	s_addc_u32 s13, s23, s13
	v_fma_f32 v156, -v154, v155, 1.0
	v_fmac_f32_e32 v155, v156, v155
	v_div_scale_f32 v156, vcc, 1.0, v152, 1.0
	v_mul_f32_e32 v157, v156, v155
	v_fma_f32 v158, -v154, v157, v156
	v_fmac_f32_e32 v157, v158, v155
	v_fma_f32 v154, -v154, v157, v156
	v_div_fmas_f32 v154, v154, v155, v157
	v_div_fixup_f32 v152, v154, v152, 1.0
	v_mul_f32_e32 v16, v16, v152
	s_waitcnt vmcnt(15)
; #define LAS __attribute__((address_space(3)))
; __device__ __forceinline__ unsigned pk2(float lo, float hi) { unsigned r; asm("v_cvt_pk_bf16_f32 %0, %1, %2" : "=v"(r) : "v"(lo), "v"(hi)); return r; }
; __device__ __forceinline__ float sigmoidf_(float x) { return __builtin_amdgcn_rcpf(1.0f + __builtin_amdgcn_exp2f(x * -1.44269504089f)); }
; __device__ __forceinline__ void phase_even_mix(CArgs a, LAS unsigned char* lds, int i2, int wv, int xw  ) {
;     ...
;                 f32x4 v0 = *(const LAS f32x4*)(ybuf + t * 512 + lane * 8), v1 = *(const LAS f32x4*)(ybuf + t * 512 + lane * 8 + 4);
;                 const float mean = wave_sum((v0.x + v0.y) + (v0.z + v0.w) + (v1.x + v1.y) + (v1.z + v1.w), lane) * (1.f / 512.f);
;                 v0 = v0 - mean; v1 = v1 - mean;
;                 const float var = wave_sum((v0.x * v0.x + v0.y * v0.y) + (v0.z * v0.z + v0.w * v0.w) + (v1.x * v1.x + v1.y * v1.y) + (v1.z * v1.z + v1.w * v1.w), lane) * (1.f / 512.f);
;                 const float rstd = 1.0f / sqrtf(var + LN_EPS);
;                 float o[8];
; #pragma unroll
;                 for (int j = 0; j < 4; ++j) { const float x0 = v0[j] * rstd * g0[j] + b0[j], x1 = v1[j] * rstd * g1[j] + b1[j]; o[j] = x0 * sigmoidf_(x0); o[4 + j] = x1 * sigmoidf_(x1); }
;                 u32x4 wv4; wv4.x = pk2(o[0], o[1]); wv4.y = pk2(o[2], o[3]); wv4.z = pk2(o[4], o[5]); wv4.w = pk2(o[6], o[7]);
;                 *(u32x4*)(YB + (tokbase + t) * DM + 512 + lane * 8) = wv4; }
	v_fma_f32 v16, v12, v16, v4
	v_mul_f32_e32 v154, 0xbfb8aa3b, v16
	v_exp_f32_e32 v154, v154
	v_mul_f32_e32 v20, v20, v152
	v_fma_f32 v20, v8, v20, v0
	v_mul_f32_e32 v17, v17, v152
	v_add_f32_e32 v154, 1.0, v154
	v_rcp_f32_e32 v154, v154
	v_fma_f32 v17, v13, v17, v5
	v_mul_f32_e32 v21, v21, v152
	v_fma_f32 v21, v9, v21, v1
	v_mul_f32_e32 v16, v16, v154
	v_mul_f32_e32 v154, 0xbfb8aa3b, v20
	v_exp_f32_e32 v154, v154
	v_mul_f32_e32 v18, v18, v152
	v_mul_f32_e32 v19, v19, v152
	v_fma_f32 v18, v14, v18, v6
	v_add_f32_e32 v154, 1.0, v154
	v_rcp_f32_e32 v154, v154
	v_fma_f32 v19, v15, v19, v7
	v_mul_f32_e32 v22, v22, v152
	v_mul_f32_e32 v23, v23, v152
	v_mul_f32_e32 v20, v20, v154
	v_mul_f32_e32 v154, 0xbfb8aa3b, v17
	v_exp_f32_e32 v154, v154
	v_mul_f32_e32 v152, 0xbfb8aa3b, v19
	v_exp_f32_e32 v152, v152
	v_fma_f32 v22, v10, v22, v2
	v_add_f32_e32 v154, 1.0, v154
	v_rcp_f32_e32 v154, v154
	v_add_f32_e32 v152, 1.0, v152
	v_rcp_f32_e32 v152, v152
	v_fma_f32 v23, v11, v23, v3
	v_mul_f32_e32 v17, v17, v154
	v_mul_f32_e32 v154, 0xbfb8aa3b, v21
	v_exp_f32_e32 v154, v154
	v_mul_f32_e32 v19, v19, v152
	v_mul_f32_e32 v152, 0xbfb8aa3b, v23
	v_exp_f32_e32 v152, v152
	v_add_f32_e32 v154, 1.0, v154
	v_rcp_f32_e32 v154, v154
	s_lshl_b64 s[12:13], s[12:13], 11
	v_add_f32_e32 v152, 1.0, v152
	v_rcp_f32_e32 v152, v152
	v_mul_f32_e32 v21, v21, v154
	v_mul_f32_e32 v154, 0xbfb8aa3b, v18
	v_exp_f32_e32 v154, v154
	v_cvt_pk_bf16_f32 v16, v16, v17
	v_mul_f32_e32 v23, v23, v152
	v_add_f32_e32 v154, 1.0, v154
	v_rcp_f32_e32 v154, v154
	s_nop 0
	v_mul_f32_e32 v18, v18, v154
	v_mul_f32_e32 v154, 0xbfb8aa3b, v22
	v_exp_f32_e32 v154, v154
	v_cvt_pk_bf16_f32 v17, v18, v19
	v_cvt_pk_bf16_f32 v18, v20, v21
	v_lshl_add_u64 v[20:21], v[32:33], 0, s[12:13]
	v_add_f32_e32 v154, 1.0, v154
	v_rcp_f32_e32 v154, v154
	v_readlane_b32 s12, v255, 5
	v_mul_f32_e32 v22, v22, v154
	v_cvt_pk_bf16_f32 v19, v22, v23
	global_store_dwordx4 v[20:21], v[16:19], off offset:1024
	v_add_u32_e32 v20, s12, v62
	ds_read_b128 v[16:19], v20
	ds_read_b128 v[20:23], v20 offset:16
	s_waitcnt lgkmcnt(1)
	v_mov_b32_e32 v154, v17
	v_mov_b32_e32 v155, v18
	v_mov_b32_e32 v156, v16
	v_mov_b32_e32 v157, v19
	v_pk_add_f32 v[154:155], v[154:155], v[156:157]
	s_waitcnt lgkmcnt(0)
	v_mov_b32_e32 v156, v22
	v_mov_b32_e32 v157, v20
	v_mov_b32_e32 v158, v23
	v_mov_b32_e32 v159, v21
	v_pk_add_f32 v[156:157], v[156:157], v[158:159]
	v_add_f32_e32 v152, v154, v155
	v_add_f32_e32 v152, v152, v157
	v_add_f32_e32 v152, v156, v152
	s_waitcnt lgkmcnt(0)
	s_nop 1
	v_add_f32_dpp v152, v152, v152 quad_perm:[1,0,3,2] row_mask:0xf bank_mask:0xf
	s_nop 1
	v_add_f32_dpp v152, v152, v152 quad_perm:[2,3,0,1] row_mask:0xf bank_mask:0xf
	s_nop 1
	v_add_f32_dpp v152, v152, v152 row_half_mirror row_mask:0xf bank_mask:0xf
	s_nop 1
	v_add_f32_dpp v152, v152, v152 row_mirror row_mask:0xf bank_mask:0xf
	v_mov_b32_e32 v154, v152
	s_nop 1
	v_permlane16_swap_b32_e32 v154, v152
	v_add_f32_e32 v152, v152, v154
	v_mov_b32_e32 v154, v152
	s_nop 1
	v_permlane32_swap_b32_e32 v154, v152
	v_add_f32_e32 v152, v152, v154
	v_fmamk_f32 v19, v152, 0xbb000000, v19
	v_fmac_f32_e32 v17, 0xbb000000, v152
	v_fmamk_f32 v18, v152, 0xbb000000, v18
	v_fmamk_f32 v16, v152, 0xbb000000, v16
	v_fmamk_f32 v22, v152, 0xbb000000, v22
	v_fmamk_f32 v23, v152, 0xbb000000, v23
	v_fmamk_f32 v20, v152, 0xbb000000, v20
	v_fmac_f32_e32 v21, 0xbb000000, v152
	v_mul_f32_e32 v152, v17, v17
	v_mul_f32_e32 v154, v19, v19
	v_fmac_f32_e32 v152, v16, v16
	v_fmac_f32_e32 v154, v18, v18
	v_add_f32_e32 v152, v152, v154
	v_mul_f32_e32 v154, v21, v21
	v_fmac_f32_e32 v154, v20, v20
	v_add_f32_e32 v152, v154, v152
	v_mul_f32_e32 v154, v23, v23
	v_fmac_f32_e32 v154, v22, v22
	v_add_f32_e32 v152, v154, v152
	s_waitcnt lgkmcnt(0)
	s_nop 1
	v_add_f32_dpp v152, v152, v152 quad_perm:[1,0,3,2] row_mask:0xf bank_mask:0xf
	s_nop 1
	v_add_f32_dpp v152, v152, v152 quad_perm:[2,3,0,1] row_mask:0xf bank_mask:0xf
	s_nop 1
	v_add_f32_dpp v152, v152, v152 row_half_mirror row_mask:0xf bank_mask:0xf
	s_nop 1
	v_add_f32_dpp v152, v152, v152 row_mirror row_mask:0xf bank_mask:0xf
	v_mov_b32_e32 v154, v152
	s_nop 1
	v_permlane16_swap_b32_e32 v154, v152
	v_add_f32_e32 v152, v152, v154
	v_mov_b32_e32 v154, v152
	s_nop 1
	v_permlane32_swap_b32_e32 v154, v152
	v_add_f32_e32 v152, v152, v154
	v_fmamk_f32 v152, v152, 0x3b000000, v185
	v_cmp_gt_f32_e32 vcc, s55, v152
	v_mul_f32_e32 v154, 0x4f800000, v152
	s_nop 0
	v_cndmask_b32_e32 v152, v152, v154, vcc
	v_sqrt_f32_e32 v154, v152
	s_nop 0
	v_add_u32_e32 v155, -1, v154
	v_fma_f32 v156, -v155, v154, v152
	v_cmp_ge_f32_e64 s[12:13], 0, v156
	v_add_u32_e32 v156, 1, v154
	s_nop 0
	v_cndmask_b32_e64 v155, v154, v155, s[12:13]
	v_fma_f32 v154, -v156, v154, v152
	v_cmp_lt_f32_e64 s[12:13], 0, v154
	s_nop 1
	v_cndmask_b32_e64 v154, v155, v156, s[12:13]
	v_mul_f32_e32 v155, 0x37800000, v154
	v_cndmask_b32_e32 v154, v154, v155, vcc
	v_cmp_class_f32_e32 vcc, v152, v183
	s_nop 1
	v_cndmask_b32_e32 v152, v154, v152, vcc
	v_div_scale_f32 v154, s[12:13], v152, v152, 1.0
	v_rcp_f32_e32 v155, v154
	s_add_u32 s12, s22, s33
	v_readlane_b32 s13, v255, 6
	s_addc_u32 s13, s23, s13
	v_fma_f32 v156, -v154, v155, 1.0
	v_fmac_f32_e32 v155, v156, v155
	v_div_scale_f32 v156, vcc, 1.0, v152, 1.0
	v_mul_f32_e32 v157, v156, v155
	v_fma_f32 v158, -v154, v157, v156
	v_fmac_f32_e32 v157, v158, v155
	v_fma_f32 v154, -v154, v157, v156
	v_div_fmas_f32 v154, v154, v155, v157
	v_div_fixup_f32 v152, v154, v152, 1.0
	v_mul_f32_e32 v16, v16, v152
	v_fma_f32 v16, v12, v16, v4
	v_mul_f32_e32 v154, 0xbfb8aa3b, v16
	v_exp_f32_e32 v154, v154
	v_mul_f32_e32 v20, v20, v152
	v_fma_f32 v20, v8, v20, v0
	v_mul_f32_e32 v17, v17, v152
; #define LAS __attribute__((address_space(3)))
; __device__ __forceinline__ unsigned pk2(float lo, float hi) { unsigned r; asm("v_cvt_pk_bf16_f32 %0, %1, %2" : "=v"(r) : "v"(lo), "v"(hi)); return r; }
; __device__ __forceinline__ float sigmoidf_(float x) { return __builtin_amdgcn_rcpf(1.0f + __builtin_amdgcn_exp2f(x * -1.44269504089f)); }
; __device__ __forceinline__ void phase_even_mix(CArgs a, LAS unsigned char* lds, int i2, int wv, int xw  ) {
;     ...
;                 f32x4 v0 = *(const LAS f32x4*)(ybuf + t * 512 + lane * 8), v1 = *(const LAS f32x4*)(ybuf + t * 512 + lane * 8 + 4);
;                 const float mean = wave_sum((v0.x + v0.y) + (v0.z + v0.w) + (v1.x + v1.y) + (v1.z + v1.w), lane) * (1.f / 512.f);
;                 v0 = v0 - mean; v1 = v1 - mean;
;                 const float var = wave_sum((v0.x * v0.x + v0.y * v0.y) + (v0.z * v0.z + v0.w * v0.w) + (v1.x * v1.x + v1.y * v1.y) + (v1.z * v1.z + v1.w * v1.w), lane) * (1.f / 512.f);
;                 const float rstd = 1.0f / sqrtf(var + LN_EPS);
;                 float o[8];
; #pragma unroll
;                 for (int j = 0; j < 4; ++j) { const float x0 = v0[j] * rstd * g0[j] + b0[j], x1 = v1[j] * rstd * g1[j] + b1[j]; o[j] = x0 * sigmoidf_(x0); o[4 + j] = x1 * sigmoidf_(x1); }
;                 u32x4 wv4; wv4.x = pk2(o[0], o[1]); wv4.y = pk2(o[2], o[3]); wv4.z = pk2(o[4], o[5]); wv4.w = pk2(o[6], o[7]);
;                 *(u32x4*)(YB + (tokbase + t) * DM + 512 + lane * 8) = wv4; }
	v_add_f32_e32 v154, 1.0, v154
	v_rcp_f32_e32 v154, v154
	v_fma_f32 v17, v13, v17, v5
	v_mul_f32_e32 v21, v21, v152
	v_fma_f32 v21, v9, v21, v1
	v_mul_f32_e32 v16, v16, v154
	v_mul_f32_e32 v154, 0xbfb8aa3b, v20
	v_exp_f32_e32 v154, v154
	v_mul_f32_e32 v18, v18, v152
	v_mul_f32_e32 v19, v19, v152
	v_fma_f32 v18, v14, v18, v6
	v_add_f32_e32 v154, 1.0, v154
	v_rcp_f32_e32 v154, v154
	v_fma_f32 v19, v15, v19, v7
	v_mul_f32_e32 v22, v22, v152
	v_mul_f32_e32 v23, v23, v152
	v_mul_f32_e32 v20, v20, v154
	v_mul_f32_e32 v154, 0xbfb8aa3b, v17
	v_exp_f32_e32 v154, v154
	v_mul_f32_e32 v152, 0xbfb8aa3b, v19
	v_exp_f32_e32 v152, v152
	v_fma_f32 v22, v10, v22, v2
	v_add_f32_e32 v154, 1.0, v154
	v_rcp_f32_e32 v154, v154
	v_add_f32_e32 v152, 1.0, v152
	v_rcp_f32_e32 v152, v152
	v_fma_f32 v23, v11, v23, v3
	v_mul_f32_e32 v17, v17, v154
	v_mul_f32_e32 v154, 0xbfb8aa3b, v21
	v_exp_f32_e32 v154, v154
	v_mul_f32_e32 v19, v19, v152
	v_mul_f32_e32 v152, 0xbfb8aa3b, v23
	v_exp_f32_e32 v152, v152
	v_add_f32_e32 v154, 1.0, v154
	v_rcp_f32_e32 v154, v154
	s_lshl_b64 s[12:13], s[12:13], 11
	v_add_f32_e32 v152, 1.0, v152
	v_rcp_f32_e32 v152, v152
	v_mul_f32_e32 v21, v21, v154
	v_mul_f32_e32 v154, 0xbfb8aa3b, v18
	v_exp_f32_e32 v154, v154
	v_cvt_pk_bf16_f32 v16, v16, v17
	v_mul_f32_e32 v23, v23, v152
	v_add_f32_e32 v154, 1.0, v154
	v_rcp_f32_e32 v154, v154
	s_nop 0
	v_mul_f32_e32 v18, v18, v154
	v_mul_f32_e32 v154, 0xbfb8aa3b, v22
	v_exp_f32_e32 v154, v154
	v_cvt_pk_bf16_f32 v17, v18, v19
	v_cvt_pk_bf16_f32 v18, v20, v21
	v_lshl_add_u64 v[20:21], v[32:33], 0, s[12:13]
	v_add_f32_e32 v154, 1.0, v154
	v_rcp_f32_e32 v154, v154
	v_readlane_b32 s12, v255, 7
	v_mul_f32_e32 v22, v22, v154
	v_cvt_pk_bf16_f32 v19, v22, v23
	global_store_dwordx4 v[20:21], v[16:19], off offset:1024
	v_add_u32_e32 v20, s12, v62
	ds_read_b128 v[16:19], v20
	ds_read_b128 v[20:23], v20 offset:16
	s_waitcnt lgkmcnt(1)
	v_mov_b32_e32 v154, v17
	v_mov_b32_e32 v155, v18
	v_mov_b32_e32 v156, v16
	v_mov_b32_e32 v157, v19
	v_pk_add_f32 v[154:155], v[154:155], v[156:157]
	s_waitcnt lgkmcnt(0)
	v_mov_b32_e32 v156, v22
	v_mov_b32_e32 v157, v20
	v_mov_b32_e32 v158, v23
	v_mov_b32_e32 v159, v21
	v_pk_add_f32 v[156:157], v[156:157], v[158:159]
	v_add_f32_e32 v152, v154, v155
	v_add_f32_e32 v152, v152, v157
	v_add_f32_e32 v152, v156, v152
	s_waitcnt lgkmcnt(0)
	s_nop 1
	v_add_f32_dpp v152, v152, v152 quad_perm:[1,0,3,2] row_mask:0xf bank_mask:0xf
	s_nop 1
	v_add_f32_dpp v152, v152, v152 quad_perm:[2,3,0,1] row_mask:0xf bank_mask:0xf
	s_nop 1
	v_add_f32_dpp v152, v152, v152 row_half_mirror row_mask:0xf bank_mask:0xf
	s_nop 1
	v_add_f32_dpp v152, v152, v152 row_mirror row_mask:0xf bank_mask:0xf
	v_mov_b32_e32 v154, v152
	s_nop 1
	v_permlane16_swap_b32_e32 v154, v152
	v_add_f32_e32 v152, v152, v154
	v_mov_b32_e32 v154, v152
	s_nop 1
	v_permlane32_swap_b32_e32 v154, v152
	v_add_f32_e32 v152, v152, v154
	v_fmamk_f32 v19, v152, 0xbb000000, v19
	v_fmac_f32_e32 v17, 0xbb000000, v152
	v_fmamk_f32 v18, v152, 0xbb000000, v18
	v_fmamk_f32 v16, v152, 0xbb000000, v16
	v_fmamk_f32 v22, v152, 0xbb000000, v22
	v_fmamk_f32 v23, v152, 0xbb000000, v23
	v_fmamk_f32 v20, v152, 0xbb000000, v20
	v_fmac_f32_e32 v21, 0xbb000000, v152
	v_mul_f32_e32 v152, v17, v17
	v_mul_f32_e32 v154, v19, v19
	v_fmac_f32_e32 v152, v16, v16
	v_fmac_f32_e32 v154, v18, v18
	v_add_f32_e32 v152, v152, v154
	v_mul_f32_e32 v154, v21, v21
	v_fmac_f32_e32 v154, v20, v20
	v_add_f32_e32 v152, v154, v152
	v_mul_f32_e32 v154, v23, v23
	v_fmac_f32_e32 v154, v22, v22
	v_add_f32_e32 v152, v154, v152
	s_waitcnt lgkmcnt(0)
	s_nop 1
	v_add_f32_dpp v152, v152, v152 quad_perm:[1,0,3,2] row_mask:0xf bank_mask:0xf
	s_nop 1
	v_add_f32_dpp v152, v152, v152 quad_perm:[2,3,0,1] row_mask:0xf bank_mask:0xf
	s_nop 1
	v_add_f32_dpp v152, v152, v152 row_half_mirror row_mask:0xf bank_mask:0xf
	s_nop 1
	v_add_f32_dpp v152, v152, v152 row_mirror row_mask:0xf bank_mask:0xf
	v_mov_b32_e32 v154, v152
	s_nop 1
	v_permlane16_swap_b32_e32 v154, v152
	v_add_f32_e32 v152, v152, v154
	v_mov_b32_e32 v154, v152
	s_nop 1
	v_permlane32_swap_b32_e32 v154, v152
	v_add_f32_e32 v152, v152, v154
	v_fmamk_f32 v152, v152, 0x3b000000, v185
	v_cmp_gt_f32_e32 vcc, s55, v152
	v_mul_f32_e32 v154, 0x4f800000, v152
	s_nop 0
	v_cndmask_b32_e32 v152, v152, v154, vcc
	v_sqrt_f32_e32 v154, v152
	s_nop 0
	v_add_u32_e32 v155, -1, v154
	v_fma_f32 v156, -v155, v154, v152
	v_cmp_ge_f32_e64 s[12:13], 0, v156
	v_add_u32_e32 v156, 1, v154
	s_nop 0
	v_cndmask_b32_e64 v155, v154, v155, s[12:13]
	v_fma_f32 v154, -v156, v154, v152
	v_cmp_lt_f32_e64 s[12:13], 0, v154
	s_nop 1
	v_cndmask_b32_e64 v154, v155, v156, s[12:13]
	v_mul_f32_e32 v155, 0x37800000, v154
	v_cndmask_b32_e32 v154, v154, v155, vcc
	v_cmp_class_f32_e32 vcc, v152, v183
	s_nop 1
	v_cndmask_b32_e32 v152, v154, v152, vcc
	v_div_scale_f32 v154, s[12:13], v152, v152, 1.0
	v_rcp_f32_e32 v155, v154
	s_add_u32 s12, s22, s57
	v_readlane_b32 s13, v255, 8
	s_addc_u32 s13, s23, s13
	v_fma_f32 v156, -v154, v155, 1.0
	v_fmac_f32_e32 v155, v156, v155
	v_div_scale_f32 v156, vcc, 1.0, v152, 1.0
	v_mul_f32_e32 v157, v156, v155
	v_fma_f32 v158, -v154, v157, v156
	v_fmac_f32_e32 v157, v158, v155
	v_fma_f32 v154, -v154, v157, v156
	v_div_fmas_f32 v154, v154, v155, v157
	v_div_fixup_f32 v152, v154, v152, 1.0
	v_mul_f32_e32 v16, v16, v152
	v_fma_f32 v16, v12, v16, v4
	v_mul_f32_e32 v154, 0xbfb8aa3b, v16
	v_exp_f32_e32 v154, v154
	v_mul_f32_e32 v20, v20, v152
	v_fma_f32 v20, v8, v20, v0
	v_mul_f32_e32 v17, v17, v152
	v_add_f32_e32 v154, 1.0, v154
	v_rcp_f32_e32 v154, v154
	v_fma_f32 v17, v13, v17, v5
	v_mul_f32_e32 v21, v21, v152
	v_fma_f32 v21, v9, v21, v1
	v_mul_f32_e32 v16, v16, v154
; #define LAS __attribute__((address_space(3)))
; __device__ __forceinline__ unsigned pk2(float lo, float hi) { unsigned r; asm("v_cvt_pk_bf16_f32 %0, %1, %2" : "=v"(r) : "v"(lo), "v"(hi)); return r; }
; __device__ __forceinline__ float sigmoidf_(float x) { return __builtin_amdgcn_rcpf(1.0f + __builtin_amdgcn_exp2f(x * -1.44269504089f)); }
; __device__ __forceinline__ void phase_even_mix(CArgs a, LAS unsigned char* lds, int i2, int wv, int xw  ) {
;     ...
;                 f32x4 v0 = *(const LAS f32x4*)(ybuf + t * 512 + lane * 8), v1 = *(const LAS f32x4*)(ybuf + t * 512 + lane * 8 + 4);
;                 const float mean = wave_sum((v0.x + v0.y) + (v0.z + v0.w) + (v1.x + v1.y) + (v1.z + v1.w), lane) * (1.f / 512.f);
;                 v0 = v0 - mean; v1 = v1 - mean;
;                 const float var = wave_sum((v0.x * v0.x + v0.y * v0.y) + (v0.z * v0.z + v0.w * v0.w) + (v1.x * v1.x + v1.y * v1.y) + (v1.z * v1.z + v1.w * v1.w), lane) * (1.f / 512.f);
;                 const float rstd = 1.0f / sqrtf(var + LN_EPS);
;                 float o[8];
; #pragma unroll
;                 for (int j = 0; j < 4; ++j) { const float x0 = v0[j] * rstd * g0[j] + b0[j], x1 = v1[j] * rstd * g1[j] + b1[j]; o[j] = x0 * sigmoidf_(x0); o[4 + j] = x1 * sigmoidf_(x1); }
;                 u32x4 wv4; wv4.x = pk2(o[0], o[1]); wv4.y = pk2(o[2], o[3]); wv4.z = pk2(o[4], o[5]); wv4.w = pk2(o[6], o[7]);
;                 *(u32x4*)(YB + (tokbase + t) * DM + 512 + lane * 8) = wv4; }
;         }
;         __syncthreads();
	v_mul_f32_e32 v154, 0xbfb8aa3b, v20
	v_exp_f32_e32 v154, v154
	v_mul_f32_e32 v18, v18, v152
	v_mul_f32_e32 v19, v19, v152
	v_fma_f32 v18, v14, v18, v6
	v_add_f32_e32 v154, 1.0, v154
	v_rcp_f32_e32 v154, v154
	v_fma_f32 v19, v15, v19, v7
	v_mul_f32_e32 v22, v22, v152
	v_mul_f32_e32 v23, v23, v152
	v_mul_f32_e32 v20, v20, v154
	v_mul_f32_e32 v154, 0xbfb8aa3b, v17
	v_exp_f32_e32 v154, v154
	v_mul_f32_e32 v152, 0xbfb8aa3b, v19
	v_exp_f32_e32 v152, v152
	v_fma_f32 v22, v10, v22, v2
	v_add_f32_e32 v154, 1.0, v154
	v_rcp_f32_e32 v154, v154
	v_add_f32_e32 v152, 1.0, v152
	v_rcp_f32_e32 v152, v152
	v_fma_f32 v23, v11, v23, v3
	v_mul_f32_e32 v17, v17, v154
	v_mul_f32_e32 v154, 0xbfb8aa3b, v21
	v_exp_f32_e32 v154, v154
	v_mul_f32_e32 v19, v19, v152
	v_mul_f32_e32 v152, 0xbfb8aa3b, v23
	v_exp_f32_e32 v152, v152
	v_add_f32_e32 v154, 1.0, v154
	v_rcp_f32_e32 v154, v154
	s_lshl_b64 s[12:13], s[12:13], 11
	v_add_f32_e32 v152, 1.0, v152
	v_rcp_f32_e32 v152, v152
	v_mul_f32_e32 v21, v21, v154
	v_mul_f32_e32 v154, 0xbfb8aa3b, v18
	v_exp_f32_e32 v154, v154
	v_cvt_pk_bf16_f32 v16, v16, v17
	v_mul_f32_e32 v23, v23, v152
	v_add_f32_e32 v154, 1.0, v154
	v_rcp_f32_e32 v154, v154
	s_nop 0
	v_mul_f32_e32 v18, v18, v154
	v_mul_f32_e32 v154, 0xbfb8aa3b, v22
	v_exp_f32_e32 v154, v154
	v_cvt_pk_bf16_f32 v17, v18, v19
	v_cvt_pk_bf16_f32 v18, v20, v21
	v_lshl_add_u64 v[20:21], v[32:33], 0, s[12:13]
	v_add_f32_e32 v154, 1.0, v154
	v_rcp_f32_e32 v154, v154
	v_readlane_b32 s12, v255, 9
	v_mul_f32_e32 v22, v22, v154
	v_cvt_pk_bf16_f32 v19, v22, v23
	global_store_dwordx4 v[20:21], v[16:19], off offset:1024
	v_add_u32_e32 v20, s12, v62
	ds_read_b128 v[16:19], v20
	ds_read_b128 v[20:23], v20 offset:16
	s_waitcnt lgkmcnt(1)
	v_mov_b32_e32 v154, v17
	v_mov_b32_e32 v155, v18
	v_mov_b32_e32 v156, v16
	v_mov_b32_e32 v157, v19
	v_pk_add_f32 v[154:155], v[154:155], v[156:157]
	s_waitcnt lgkmcnt(0)
	v_mov_b32_e32 v156, v22
	v_mov_b32_e32 v157, v20
	v_mov_b32_e32 v158, v23
	v_mov_b32_e32 v159, v21
	v_pk_add_f32 v[156:157], v[156:157], v[158:159]
	v_add_f32_e32 v152, v154, v155
	v_add_f32_e32 v152, v152, v157
	v_add_f32_e32 v152, v156, v152
	s_waitcnt lgkmcnt(0)
	s_nop 1
	v_add_f32_dpp v152, v152, v152 quad_perm:[1,0,3,2] row_mask:0xf bank_mask:0xf
	s_nop 1
	v_add_f32_dpp v152, v152, v152 quad_perm:[2,3,0,1] row_mask:0xf bank_mask:0xf
	s_nop 1
	v_add_f32_dpp v152, v152, v152 row_half_mirror row_mask:0xf bank_mask:0xf
	s_nop 1
	v_add_f32_dpp v152, v152, v152 row_mirror row_mask:0xf bank_mask:0xf
	v_mov_b32_e32 v154, v152
	s_nop 1
	v_permlane16_swap_b32_e32 v154, v152
	v_add_f32_e32 v152, v152, v154
	v_mov_b32_e32 v154, v152
	s_nop 1
	v_permlane32_swap_b32_e32 v154, v152
	v_add_f32_e32 v152, v152, v154
	v_fmamk_f32 v19, v152, 0xbb000000, v19
	v_fmac_f32_e32 v17, 0xbb000000, v152
	v_fmamk_f32 v18, v152, 0xbb000000, v18
	v_fmamk_f32 v16, v152, 0xbb000000, v16
	v_fmamk_f32 v22, v152, 0xbb000000, v22
	v_fmamk_f32 v23, v152, 0xbb000000, v23
	v_fmamk_f32 v20, v152, 0xbb000000, v20
	v_fmac_f32_e32 v21, 0xbb000000, v152
	v_mul_f32_e32 v152, v17, v17
	v_mul_f32_e32 v154, v19, v19
	v_fmac_f32_e32 v152, v16, v16
	v_fmac_f32_e32 v154, v18, v18
	v_add_f32_e32 v152, v152, v154
	v_mul_f32_e32 v154, v21, v21
	v_fmac_f32_e32 v154, v20, v20
	v_add_f32_e32 v152, v154, v152
	v_mul_f32_e32 v154, v23, v23
	v_fmac_f32_e32 v154, v22, v22
	v_add_f32_e32 v152, v154, v152
	s_waitcnt lgkmcnt(0)
	s_nop 1
	v_add_f32_dpp v152, v152, v152 quad_perm:[1,0,3,2] row_mask:0xf bank_mask:0xf
	s_nop 1
	v_add_f32_dpp v152, v152, v152 quad_perm:[2,3,0,1] row_mask:0xf bank_mask:0xf
	s_nop 1
	v_add_f32_dpp v152, v152, v152 row_half_mirror row_mask:0xf bank_mask:0xf
	s_nop 1
	v_add_f32_dpp v152, v152, v152 row_mirror row_mask:0xf bank_mask:0xf
	v_mov_b32_e32 v154, v152
	s_nop 1
	v_permlane16_swap_b32_e32 v154, v152
	v_add_f32_e32 v152, v152, v154
	v_mov_b32_e32 v154, v152
	s_nop 1
	v_permlane32_swap_b32_e32 v154, v152
	v_add_f32_e32 v152, v152, v154
	v_fmamk_f32 v152, v152, 0x3b000000, v185
	v_cmp_gt_f32_e32 vcc, s55, v152
	v_mul_f32_e32 v154, 0x4f800000, v152
	s_nop 0
	v_cndmask_b32_e32 v152, v152, v154, vcc
	v_sqrt_f32_e32 v154, v152
	s_nop 0
	v_add_u32_e32 v155, -1, v154
	v_fma_f32 v156, -v155, v154, v152
	v_cmp_ge_f32_e64 s[12:13], 0, v156
	v_add_u32_e32 v156, 1, v154
	s_nop 0
	v_cndmask_b32_e64 v155, v154, v155, s[12:13]
	v_fma_f32 v154, -v156, v154, v152
	v_cmp_lt_f32_e64 s[12:13], 0, v154
	s_nop 1
	v_cndmask_b32_e64 v154, v155, v156, s[12:13]
	v_mul_f32_e32 v155, 0x37800000, v154
	v_cndmask_b32_e32 v154, v154, v155, vcc
	v_cmp_class_f32_e32 vcc, v152, v183
	s_nop 1
	v_cndmask_b32_e32 v152, v154, v152, vcc
	v_div_scale_f32 v154, s[12:13], v152, v152, 1.0
	v_rcp_f32_e32 v155, v154
	s_add_u32 s12, s22, s14
	v_readlane_b32 s13, v255, 10
	s_addc_u32 s13, s23, s13
	v_fma_f32 v156, -v154, v155, 1.0
	v_fmac_f32_e32 v155, v156, v155
	v_div_scale_f32 v156, vcc, 1.0, v152, 1.0
	v_mul_f32_e32 v157, v156, v155
	v_fma_f32 v158, -v154, v157, v156
	v_fmac_f32_e32 v157, v158, v155
	v_fma_f32 v154, -v154, v157, v156
	v_div_fmas_f32 v154, v154, v155, v157
	v_div_fixup_f32 v152, v154, v152, 1.0
	v_mul_f32_e32 v16, v16, v152
	v_fma_f32 v4, v12, v16, v4
	v_mul_f32_e32 v12, v20, v152
	v_fma_f32 v0, v8, v12, v0
	v_mul_f32_e32 v8, 0xbfb8aa3b, v4
	v_exp_f32_e32 v8, v8
	s_lshl_b64 s[12:13], s[12:13], 11
	v_add_f32_e32 v8, 1.0, v8
	v_rcp_f32_e32 v8, v8
	s_nop 0
	v_mul_f32_e32 v4, v4, v8
	v_mul_f32_e32 v8, 0xbfb8aa3b, v0
	v_exp_f32_e32 v8, v8
	s_nop 0
	v_add_f32_e32 v8, 1.0, v8
	v_rcp_f32_e32 v8, v8
	s_nop 0
	v_mul_f32_e32 v8, v0, v8
	v_mul_f32_e32 v0, v17, v152
	v_fma_f32 v0, v13, v0, v5
	v_mul_f32_e32 v5, v21, v152
	v_fma_f32 v1, v9, v5, v1
	v_mul_f32_e32 v5, 0xbfb8aa3b, v0
	v_exp_f32_e32 v5, v5
	s_nop 0
	v_add_f32_e32 v5, 1.0, v5
	v_rcp_f32_e32 v5, v5
	s_nop 0
	v_mul_f32_e32 v0, v0, v5
	v_mul_f32_e32 v5, 0xbfb8aa3b, v1
	v_exp_f32_e32 v5, v5
	v_cvt_pk_bf16_f32 v0, v4, v0
	s_nop 0
	v_add_f32_e32 v5, 1.0, v5
	v_rcp_f32_e32 v5, v5
	s_nop 0
	v_mul_f32_e32 v5, v1, v5
	v_mul_f32_e32 v1, v18, v152
	v_fma_f32 v1, v14, v1, v6
	v_mul_f32_e32 v6, v22, v152
	v_fma_f32 v2, v10, v6, v2
	v_mul_f32_e32 v6, 0xbfb8aa3b, v1
	v_exp_f32_e32 v6, v6
	s_nop 0
	v_add_f32_e32 v6, 1.0, v6
	v_rcp_f32_e32 v6, v6
	s_nop 0
	v_mul_f32_e32 v1, v1, v6
	v_mul_f32_e32 v6, 0xbfb8aa3b, v2
	v_exp_f32_e32 v6, v6
	s_nop 0
	v_add_f32_e32 v6, 1.0, v6
	v_rcp_f32_e32 v6, v6
	s_nop 0
	v_mul_f32_e32 v6, v2, v6
	v_mul_f32_e32 v2, v19, v152
	v_fmac_f32_e32 v7, v15, v2
	v_mul_f32_e32 v2, v23, v152
	v_fmac_f32_e32 v3, v11, v2
	v_mul_f32_e32 v2, 0xbfb8aa3b, v7
	v_exp_f32_e32 v2, v2
	s_nop 0
	v_add_f32_e32 v2, 1.0, v2
	v_rcp_f32_e32 v2, v2
	s_nop 0
	v_mul_f32_e32 v2, v7, v2
	v_mul_f32_e32 v7, 0xbfb8aa3b, v3
	v_exp_f32_e32 v7, v7
	v_cvt_pk_bf16_f32 v1, v1, v2
	v_cvt_pk_bf16_f32 v2, v8, v5
	v_lshl_add_u64 v[4:5], v[32:33], 0, s[12:13]
	v_add_f32_e32 v7, 1.0, v7
	v_rcp_f32_e32 v7, v7
	s_or_b32 s12, s15, 1
	s_min_i32 s12, s12, s28
	v_mul_f32_e32 v3, v3, v7
	v_cvt_pk_bf16_f32 v3, v6, v3
	global_store_dwordx4 v[4:5], v[0:3], off offset:1024
	s_barrier
; __device__ __forceinline__ unsigned f2bf(float f) { unsigned u = __builtin_bit_cast(unsigned, f); return (u + 0x7fffu + ((u >> 16) & 1u)) >> 16; }
; __device__ __forceinline__ void phase_even_mix(CArgs a, LAS unsigned char* lds, int i2, int wv, int xw  ) {
;     ...
;             const int g = wave >> 1, winw = 2 << g;
;             float pprev = 0.f, a2r[3] = {0.f, 0.f, 0.f}, a4r[5] = {0.f, 0.f, 0.f, 0.f, 0.f}, a8r[9] = {0.f, 0.f, 0.f, 0.f, 0.f, 0.f, 0.f, 0.f, 0.f};
; #pragma clang loop unroll(full)
;             for (int r = 0; r < 48; ++r) {
;                 const float p = bf2f(glu[r * 512 + c]);
;                 const float a2 = p + pprev, a4 = a2 + a2r[(r + 1) % 3], a8 = a4 + a4r[(r + 1) % 5], a16 = a8 + a8r[(r + 1) % 9];
;                 a2r[r % 3] = a2; a4r[r % 5] = a4; a8r[r % 9] = a8; pprev = p;
;                 if (r >= 16) { const float s = g == 0 ? a2 : (g == 1 ? a4 : (g == 2 ? a8 : a16));
;                     const int pos = t0 + r - 16; const float cnt = (float)((pos + 1) < winw ? (pos + 1) : winw);
;                     pl[(r - 16) * PLS + c] = (bf16)f2bf(s / cnt - p); }
;             }
;         }
	ds_read_u16 v0, v35 offset:1024
	ds_read_u16 v1, v35 offset:2048
	ds_read_u16 v2, v35 offset:3072
	ds_read_u16 v3, v35 offset:4096
	ds_read_u16 v4, v35 offset:5120
	ds_read_u16 v5, v35 offset:6144
	ds_read_u16 v6, v35 offset:7168
	ds_read_u16 v7, v35 offset:8192
	s_waitcnt lgkmcnt(7)
	v_lshlrev_b32_e32 v0, 16, v0
	s_waitcnt lgkmcnt(6)
	v_lshlrev_b32_e32 v1, 16, v1
	s_waitcnt lgkmcnt(5)
	v_lshlrev_b32_e32 v2, 16, v2
	s_waitcnt lgkmcnt(4)
	v_lshlrev_b32_e32 v3, 16, v3
	s_waitcnt lgkmcnt(3)
	v_lshlrev_b32_e32 v4, 16, v4
	s_waitcnt lgkmcnt(2)
	v_lshlrev_b32_e32 v5, 16, v5
	s_waitcnt lgkmcnt(1)
	v_lshlrev_b32_e32 v6, 16, v6
	s_waitcnt lgkmcnt(0)
	v_lshlrev_b32_e32 v7, 16, v7
	v_add_f32_e32 v0, v0, v1
	v_add_f32_e32 v1, v1, v2
	v_add_f32_e32 v2, v2, v3
	v_add_f32_e32 v3, v3, v4
	v_add_f32_e32 v4, v4, v5
	v_add_f32_e32 v5, v5, v6
	v_add_f32_e32 v6, v6, v7
	v_add_f32_e32 v0, v0, v2
	v_add_f32_e32 v2, v2, v4
	v_add_f32_e32 v4, v4, v6
	v_add_f32_e32 v8, v0, v4
	ds_read_u16 v0, v35 offset:9216
	v_add_f32_e32 v1, v1, v3
	v_add_f32_e32 v3, v3, v5
	s_waitcnt lgkmcnt(0)
	v_lshlrev_b32_e32 v0, 16, v0
	v_add_f32_e32 v7, v7, v0
	v_add_f32_e32 v9, v5, v7
	v_add_f32_e32 v11, v1, v9
	ds_read_u16 v1, v35 offset:10240
	s_waitcnt lgkmcnt(0)
	v_lshlrev_b32_e32 v1, 16, v1
	v_add_f32_e32 v0, v0, v1
	v_add_f32_e32 v10, v6, v0
	v_add_f32_e32 v13, v2, v10
	ds_read_u16 v2, v35 offset:11264
	s_waitcnt lgkmcnt(0)
	v_lshlrev_b32_e32 v2, 16, v2
	v_add_f32_e32 v1, v1, v2
	v_add_f32_e32 v12, v7, v1
	v_add_f32_e32 v5, v3, v12
	ds_read_u16 v3, v35 offset:12288
	s_waitcnt lgkmcnt(0)
	v_lshlrev_b32_e32 v3, 16, v3
	v_add_f32_e32 v2, v2, v3
	v_add_f32_e32 v14, v0, v2
	ds_read_u16 v0, v35 offset:13312
	v_add_f32_e32 v6, v4, v14
	s_waitcnt lgkmcnt(0)
	v_lshlrev_b32_e32 v0, 16, v0
	v_add_f32_e32 v3, v3, v0
	v_add_f32_e32 v4, v1, v3
	ds_read_u16 v1, v35 offset:14336
	v_add_f32_e32 v7, v9, v4
	s_waitcnt lgkmcnt(0)
	v_lshlrev_b32_e32 v1, 16, v1
	v_add_f32_e32 v9, v0, v1
	v_add_f32_e32 v15, v2, v9
	ds_read_u16 v2, v35 offset:15360
	v_add_f32_e32 v0, v10, v15
	s_waitcnt lgkmcnt(0)
	v_lshlrev_b32_e32 v2, 16, v2
	v_add_f32_e32 v10, v1, v2
	ds_read_u16 v1, v35 offset:16384
	v_add_f32_e32 v17, v3, v10
	v_add_f32_e32 v12, v12, v17
	s_waitcnt lgkmcnt(0)
	v_lshlrev_b32_e32 v3, 16, v1
	v_add_f32_e32 v16, v2, v3
	v_add_f32_e32 v9, v9, v16
	v_add_f32_e32 v1, v14, v9
	v_add_f32_e32 v2, v8, v1
	v_cvt_f32_i32_e32 v8, s12
	v_cndmask_b32_e64 v2, v2, v1, s[10:11]
	v_cndmask_b32_e64 v2, v2, v9, s[8:9]
	v_cndmask_b32_e64 v2, v2, v16, s[6:7]
	v_div_scale_f32 v14, s[12:13], v8, v8, v2
	v_rcp_f32_e32 v18, v14
	s_or_b32 s12, s15, 2
	s_min_i32 s12, s12, s28
	v_fma_f32 v19, -v14, v18, 1.0
	v_fmac_f32_e32 v18, v19, v18
	v_div_scale_f32 v19, vcc, v2, v8, v2
	v_mul_f32_e32 v20, v19, v18
	v_fma_f32 v21, -v14, v20, v19
	v_fmac_f32_e32 v20, v21, v18
	v_fma_f32 v14, -v14, v20, v19
	v_div_fmas_f32 v14, v14, v18, v20
	v_div_fixup_f32 v2, v14, v8, v2
	v_sub_f32_e32 v2, v2, v3
	v_bfe_u32 v8, v2, 16, 1
	v_add3_u32 v2, v2, v8, s49
	ds_write_b16_d16_hi v77, v2
	ds_read_u16 v2, v35 offset:17408
	s_waitcnt lgkmcnt(0)
	v_lshlrev_b32_e32 v8, 16, v2
	v_add_f32_e32 v14, v3, v8
	v_add_f32_e32 v10, v10, v14
	v_add_f32_e32 v2, v4, v10
	v_add_f32_e32 v3, v11, v2
	v_cvt_f32_i32_e32 v4, s12
	v_cndmask_b32_e64 v3, v3, v2, s[10:11]
	v_cndmask_b32_e64 v3, v3, v10, s[8:9]
	v_cndmask_b32_e64 v3, v3, v14, s[6:7]
	v_div_scale_f32 v11, s[12:13], v4, v4, v3
	v_rcp_f32_e32 v18, v11
	s_or_b32 s12, s15, 3
	s_min_i32 s12, s12, s28
	v_fma_f32 v19, -v11, v18, 1.0
	v_fmac_f32_e32 v18, v19, v18
	v_div_scale_f32 v19, vcc, v3, v4, v3
	v_mul_f32_e32 v20, v19, v18
	v_fma_f32 v21, -v11, v20, v19
	v_fmac_f32_e32 v20, v21, v18
	v_fma_f32 v11, -v11, v20, v19
	v_div_fmas_f32 v11, v11, v18, v20
	v_div_fixup_f32 v3, v11, v4, v3
	v_sub_f32_e32 v3, v3, v8
	v_bfe_u32 v4, v3, 16, 1
	v_add3_u32 v3, v3, v4, s49
	ds_write_b16_d16_hi v110, v3
	ds_read_u16 v3, v35 offset:18432
	s_waitcnt lgkmcnt(0)
	v_lshlrev_b32_e32 v4, 16, v3
	v_add_f32_e32 v8, v8, v4
	v_add_f32_e32 v11, v16, v8
	v_add_f32_e32 v3, v15, v11
	v_add_f32_e32 v13, v13, v3
	v_cvt_f32_i32_e32 v15, s12
	v_cndmask_b32_e64 v13, v13, v3, s[10:11]
	v_cndmask_b32_e64 v13, v13, v11, s[8:9]
	v_cndmask_b32_e64 v13, v13, v8, s[6:7]
	v_div_scale_f32 v16, s[12:13], v15, v15, v13
	v_rcp_f32_e32 v18, v16
	s_or_b32 s12, s15, 4
	s_min_i32 s12, s12, s28
	v_fma_f32 v19, -v16, v18, 1.0
	v_fmac_f32_e32 v18, v19, v18
	v_div_scale_f32 v19, vcc, v13, v15, v13
	v_mul_f32_e32 v20, v19, v18
	v_fma_f32 v21, -v16, v20, v19
	v_fmac_f32_e32 v20, v21, v18
	v_fma_f32 v16, -v16, v20, v19
	v_div_fmas_f32 v16, v16, v18, v20
	v_div_fixup_f32 v13, v16, v15, v13
	v_sub_f32_e32 v13, v13, v4
	v_bfe_u32 v15, v13, 16, 1
	v_add3_u32 v13, v13, v15, s49
	ds_write_b16_d16_hi v111, v13
	ds_read_u16 v13, v35 offset:19456
	s_waitcnt lgkmcnt(0)
	v_lshlrev_b32_e32 v13, 16, v13
	v_add_f32_e32 v15, v4, v13
	v_add_f32_e32 v16, v14, v15
	v_add_f32_e32 v4, v17, v16
	v_add_f32_e32 v5, v5, v4
	v_cvt_f32_i32_e32 v14, s12
	v_cndmask_b32_e64 v5, v5, v4, s[10:11]
	v_cndmask_b32_e64 v5, v5, v16, s[8:9]
	v_cndmask_b32_e64 v5, v5, v15, s[6:7]
	v_div_scale_f32 v17, s[12:13], v14, v14, v5
	v_rcp_f32_e32 v18, v17
	s_or_b32 s12, s15, 5
	s_min_i32 s12, s12, s28
	v_fma_f32 v19, -v17, v18, 1.0
	v_fmac_f32_e32 v18, v19, v18
	v_div_scale_f32 v19, vcc, v5, v14, v5
	v_mul_f32_e32 v20, v19, v18
	v_fma_f32 v21, -v17, v20, v19
	v_fmac_f32_e32 v20, v21, v18
	v_fma_f32 v17, -v17, v20, v19
	v_div_fmas_f32 v17, v17, v18, v20
	v_div_fixup_f32 v5, v17, v14, v5
	v_sub_f32_e32 v5, v5, v13
	v_bfe_u32 v14, v5, 16, 1
	v_add3_u32 v5, v5, v14, s49
	ds_write_b16_d16_hi v112, v5
	ds_read_u16 v5, v35 offset:20480
	s_waitcnt lgkmcnt(0)
; __device__ __forceinline__ unsigned f2bf(float f) { unsigned u = __builtin_bit_cast(unsigned, f); return (u + 0x7fffu + ((u >> 16) & 1u)) >> 16; }
; __device__ __forceinline__ void phase_even_mix(CArgs a, LAS unsigned char* lds, int i2, int wv, int xw  ) {
;     ...
;             for (int r = 0; r < 48; ++r) {
;                 const float p = bf2f(glu[r * 512 + c]);
;                 const float a2 = p + pprev, a4 = a2 + a2r[(r + 1) % 3], a8 = a4 + a4r[(r + 1) % 5], a16 = a8 + a8r[(r + 1) % 9];
;                 a2r[r % 3] = a2; a4r[r % 5] = a4; a8r[r % 9] = a8; pprev = p;
;                 if (r >= 16) { const float s = g == 0 ? a2 : (g == 1 ? a4 : (g == 2 ? a8 : a16));
;                     const int pos = t0 + r - 16; const float cnt = (float)((pos + 1) < winw ? (pos + 1) : winw);
;                     pl[(r - 16) * PLS + c] = (bf16)f2bf(s / cnt - p); }
	v_lshlrev_b32_e32 v14, 16, v5
	v_add_f32_e32 v17, v13, v14
	v_add_f32_e32 v8, v8, v17
	v_add_f32_e32 v5, v9, v8
	v_add_f32_e32 v6, v6, v5
	v_cvt_f32_i32_e32 v9, s12
	v_cndmask_b32_e64 v6, v6, v5, s[10:11]
	v_cndmask_b32_e64 v6, v6, v8, s[8:9]
	v_cndmask_b32_e64 v6, v6, v17, s[6:7]
	v_div_scale_f32 v13, s[12:13], v9, v9, v6
	v_rcp_f32_e32 v18, v13
	s_or_b32 s12, s15, 6
	s_min_i32 s12, s12, s28
	v_fma_f32 v19, -v13, v18, 1.0
	v_fmac_f32_e32 v18, v19, v18
	v_div_scale_f32 v19, vcc, v6, v9, v6
	v_mul_f32_e32 v20, v19, v18
	v_fma_f32 v21, -v13, v20, v19
	v_fmac_f32_e32 v20, v21, v18
	v_fma_f32 v13, -v13, v20, v19
	v_div_fmas_f32 v13, v13, v18, v20
	v_div_fixup_f32 v6, v13, v9, v6
	v_sub_f32_e32 v6, v6, v14
	v_bfe_u32 v9, v6, 16, 1
	v_add3_u32 v6, v6, v9, s49
	ds_write_b16_d16_hi v113, v6
	ds_read_u16 v6, v35 offset:21504
	s_waitcnt lgkmcnt(0)
	v_lshlrev_b32_e32 v13, 16, v6
	v_add_f32_e32 v18, v14, v13
	v_add_f32_e32 v9, v15, v18
	v_add_f32_e32 v6, v10, v9
	v_add_f32_e32 v7, v7, v6
	v_cvt_f32_i32_e32 v10, s12
	v_cndmask_b32_e64 v7, v7, v6, s[10:11]
	v_cndmask_b32_e64 v7, v7, v9, s[8:9]
	v_cndmask_b32_e64 v7, v7, v18, s[6:7]
	v_div_scale_f32 v14, s[12:13], v10, v10, v7
	v_rcp_f32_e32 v15, v14
	s_or_b32 s12, s15, 7
	s_min_i32 s12, s12, s28
	v_fma_f32 v19, -v14, v15, 1.0
	v_fmac_f32_e32 v15, v19, v15
	v_div_scale_f32 v19, vcc, v7, v10, v7
	v_mul_f32_e32 v20, v19, v15
	v_fma_f32 v21, -v14, v20, v19
	v_fmac_f32_e32 v20, v21, v15
	v_fma_f32 v14, -v14, v20, v19
	v_div_fmas_f32 v14, v14, v15, v20
	v_div_fixup_f32 v7, v14, v10, v7
	v_sub_f32_e32 v7, v7, v13
	v_bfe_u32 v10, v7, 16, 1
	v_add3_u32 v7, v7, v10, s49
	ds_write_b16_d16_hi v114, v7
	ds_read_u16 v7, v35 offset:22528
	s_waitcnt lgkmcnt(0)
	v_lshlrev_b32_e32 v15, 16, v7
	v_add_f32_e32 v13, v13, v15
	v_add_f32_e32 v10, v17, v13
	v_add_f32_e32 v7, v11, v10
	v_add_f32_e32 v0, v0, v7
	v_cvt_f32_i32_e32 v11, s12
	v_cndmask_b32_e64 v0, v0, v7, s[10:11]
	v_cndmask_b32_e64 v0, v0, v10, s[8:9]
	v_cndmask_b32_e64 v0, v0, v13, s[6:7]
	v_div_scale_f32 v14, s[12:13], v11, v11, v0
	v_rcp_f32_e32 v17, v14
	s_or_b32 s12, s15, 8
	s_min_i32 s12, s12, s28
	v_fma_f32 v19, -v14, v17, 1.0
	v_fmac_f32_e32 v17, v19, v17
	v_div_scale_f32 v19, vcc, v0, v11, v0
	v_mul_f32_e32 v20, v19, v17
	v_fma_f32 v21, -v14, v20, v19
	v_fmac_f32_e32 v20, v21, v17
	v_fma_f32 v14, -v14, v20, v19
	v_div_fmas_f32 v14, v14, v17, v20
	v_div_fixup_f32 v0, v14, v11, v0
	v_sub_f32_e32 v0, v0, v15
	v_bfe_u32 v11, v0, 16, 1
	v_add3_u32 v0, v0, v11, s49
	ds_write_b16_d16_hi v115, v0
	ds_read_u16 v0, v35 offset:23552
	s_waitcnt lgkmcnt(0)
	v_lshlrev_b32_e32 v14, 16, v0
	v_add_f32_e32 v15, v15, v14
	v_add_f32_e32 v11, v18, v15
	v_add_f32_e32 v0, v16, v11
	v_add_f32_e32 v12, v12, v0
	v_cvt_f32_i32_e32 v16, s12
	v_cndmask_b32_e64 v12, v12, v0, s[10:11]
	v_cndmask_b32_e64 v12, v12, v11, s[8:9]
	v_cndmask_b32_e64 v12, v12, v15, s[6:7]
	v_div_scale_f32 v17, s[12:13], v16, v16, v12
	v_rcp_f32_e32 v18, v17
	s_or_b32 s12, s15, 9
	s_min_i32 s12, s12, s28
	v_fma_f32 v19, -v17, v18, 1.0
	v_fmac_f32_e32 v18, v19, v18
	v_div_scale_f32 v19, vcc, v12, v16, v12
	v_mul_f32_e32 v20, v19, v18
	v_fma_f32 v21, -v17, v20, v19
	v_fmac_f32_e32 v20, v21, v18
	v_fma_f32 v17, -v17, v20, v19
	v_div_fmas_f32 v17, v17, v18, v20
	v_div_fixup_f32 v12, v17, v16, v12
	v_sub_f32_e32 v12, v12, v14
	v_bfe_u32 v16, v12, 16, 1
	v_add3_u32 v12, v12, v16, s49
	ds_write_b16_d16_hi v116, v12
	ds_read_u16 v12, v35 offset:24576
	s_waitcnt lgkmcnt(0)
	v_lshlrev_b32_e32 v12, 16, v12
	v_add_f32_e32 v16, v14, v12
	v_add_f32_e32 v17, v13, v16
	v_add_f32_e32 v14, v8, v17
	v_add_f32_e32 v1, v1, v14
	v_cvt_f32_i32_e32 v8, s12
	v_cndmask_b32_e64 v1, v1, v14, s[10:11]
	v_cndmask_b32_e64 v1, v1, v17, s[8:9]
	v_cndmask_b32_e64 v1, v1, v16, s[6:7]
	v_div_scale_f32 v13, s[12:13], v8, v8, v1
	v_rcp_f32_e32 v18, v13
	s_or_b32 s12, s15, 10
	s_min_i32 s12, s12, s28
	v_fma_f32 v19, -v13, v18, 1.0
	v_fmac_f32_e32 v18, v19, v18
	v_div_scale_f32 v19, vcc, v1, v8, v1
	v_mul_f32_e32 v20, v19, v18
	v_fma_f32 v21, -v13, v20, v19
	v_fmac_f32_e32 v20, v21, v18
	v_fma_f32 v13, -v13, v20, v19
	v_div_fmas_f32 v13, v13, v18, v20
	v_div_fixup_f32 v1, v13, v8, v1
	v_sub_f32_e32 v1, v1, v12
	v_bfe_u32 v8, v1, 16, 1
	v_add3_u32 v1, v1, v8, s49
	ds_write_b16_d16_hi v117, v1
	ds_read_u16 v1, v35 offset:25600
	s_waitcnt lgkmcnt(0)
	v_lshlrev_b32_e32 v1, 16, v1
	v_add_f32_e32 v18, v12, v1
	v_add_f32_e32 v12, v15, v18
	v_add_f32_e32 v8, v9, v12
	v_add_f32_e32 v2, v2, v8
	v_cvt_f32_i32_e32 v9, s12
	v_cndmask_b32_e64 v2, v2, v8, s[10:11]
	v_cndmask_b32_e64 v2, v2, v12, s[8:9]
	v_cndmask_b32_e64 v2, v2, v18, s[6:7]
	v_div_scale_f32 v13, s[12:13], v9, v9, v2
	v_rcp_f32_e32 v15, v13
	s_or_b32 s12, s15, 11
	s_min_i32 s12, s12, s28
	v_fma_f32 v19, -v13, v15, 1.0
	v_fmac_f32_e32 v15, v19, v15
	v_div_scale_f32 v19, vcc, v2, v9, v2
	v_mul_f32_e32 v20, v19, v15
	v_fma_f32 v21, -v13, v20, v19
	v_fmac_f32_e32 v20, v21, v15
	v_fma_f32 v13, -v13, v20, v19
	v_div_fmas_f32 v13, v13, v15, v20
	v_div_fixup_f32 v2, v13, v9, v2
	v_sub_f32_e32 v2, v2, v1
	v_bfe_u32 v9, v2, 16, 1
	v_add3_u32 v2, v2, v9, s49
	ds_write_b16_d16_hi v118, v2
	ds_read_u16 v2, v35 offset:26624
	s_waitcnt lgkmcnt(0)
	v_lshlrev_b32_e32 v2, 16, v2
	v_add_f32_e32 v15, v1, v2
	v_add_f32_e32 v13, v16, v15
	v_add_f32_e32 v9, v10, v13
	v_add_f32_e32 v1, v3, v9
	v_cvt_f32_i32_e32 v3, s12
	v_cndmask_b32_e64 v1, v1, v9, s[10:11]
	v_cndmask_b32_e64 v1, v1, v13, s[8:9]
	v_cndmask_b32_e64 v1, v1, v15, s[6:7]
	v_div_scale_f32 v10, s[12:13], v3, v3, v1
	v_rcp_f32_e32 v16, v10
	s_or_b32 s12, s15, 12
	s_min_i32 s12, s12, s28
	v_fma_f32 v19, -v10, v16, 1.0
	v_fmac_f32_e32 v16, v19, v16
	v_div_scale_f32 v19, vcc, v1, v3, v1
	v_mul_f32_e32 v20, v19, v16
	v_fma_f32 v21, -v10, v20, v19
	v_fmac_f32_e32 v20, v21, v16
	v_fma_f32 v10, -v10, v20, v19
	v_div_fmas_f32 v10, v10, v16, v20
	v_div_fixup_f32 v1, v10, v3, v1
	v_sub_f32_e32 v1, v1, v2
	v_bfe_u32 v3, v1, 16, 1
	v_add3_u32 v1, v1, v3, s49
	ds_write_b16_d16_hi v119, v1
	ds_read_u16 v1, v35 offset:27648
	s_waitcnt lgkmcnt(0)
; __device__ __forceinline__ unsigned f2bf(float f) { unsigned u = __builtin_bit_cast(unsigned, f); return (u + 0x7fffu + ((u >> 16) & 1u)) >> 16; }
; __device__ __forceinline__ void phase_even_mix(CArgs a, LAS unsigned char* lds, int i2, int wv, int xw  ) {
;     ...
;             for (int r = 0; r < 48; ++r) {
;                 const float p = bf2f(glu[r * 512 + c]);
;                 const float a2 = p + pprev, a4 = a2 + a2r[(r + 1) % 3], a8 = a4 + a4r[(r + 1) % 5], a16 = a8 + a8r[(r + 1) % 9];
;                 a2r[r % 3] = a2; a4r[r % 5] = a4; a8r[r % 9] = a8; pprev = p;
;                 if (r >= 16) { const float s = g == 0 ? a2 : (g == 1 ? a4 : (g == 2 ? a8 : a16));
;                     const int pos = t0 + r - 16; const float cnt = (float)((pos + 1) < winw ? (pos + 1) : winw);
;                     pl[(r - 16) * PLS + c] = (bf16)f2bf(s / cnt - p); }
	v_lshlrev_b32_e32 v3, 16, v1
	v_add_f32_e32 v16, v2, v3
	v_add_f32_e32 v1, v18, v16
	v_add_f32_e32 v10, v11, v1
	v_add_f32_e32 v2, v4, v10
	v_cvt_f32_i32_e32 v4, s12
	v_cndmask_b32_e64 v2, v2, v10, s[10:11]
	v_cndmask_b32_e64 v2, v2, v1, s[8:9]
	v_cndmask_b32_e64 v2, v2, v16, s[6:7]
	v_div_scale_f32 v11, s[12:13], v4, v4, v2
	v_rcp_f32_e32 v18, v11
	s_or_b32 s12, s15, 13
	s_min_i32 s12, s12, s28
	v_fma_f32 v19, -v11, v18, 1.0
	v_fmac_f32_e32 v18, v19, v18
	v_div_scale_f32 v19, vcc, v2, v4, v2
	v_mul_f32_e32 v20, v19, v18
	v_fma_f32 v21, -v11, v20, v19
	v_fmac_f32_e32 v20, v21, v18
	v_fma_f32 v11, -v11, v20, v19
	v_div_fmas_f32 v11, v11, v18, v20
	v_div_fixup_f32 v2, v11, v4, v2
	v_sub_f32_e32 v2, v2, v3
	v_bfe_u32 v4, v2, 16, 1
	v_add3_u32 v2, v2, v4, s49
	ds_write_b16_d16_hi v120, v2
	ds_read_u16 v2, v35 offset:28672
	s_waitcnt lgkmcnt(0)
	v_lshlrev_b32_e32 v4, 16, v2
	v_add_f32_e32 v18, v3, v4
	v_add_f32_e32 v2, v15, v18
	v_add_f32_e32 v11, v17, v2
	v_add_f32_e32 v3, v5, v11
	v_cvt_f32_i32_e32 v5, s12
	v_cndmask_b32_e64 v3, v3, v11, s[10:11]
	v_cndmask_b32_e64 v3, v3, v2, s[8:9]
	v_cndmask_b32_e64 v3, v3, v18, s[6:7]
	v_div_scale_f32 v15, s[12:13], v5, v5, v3
	v_rcp_f32_e32 v17, v15
	s_or_b32 s12, s15, 14
	s_min_i32 s12, s12, s28
	v_fma_f32 v19, -v15, v17, 1.0
	v_fmac_f32_e32 v17, v19, v17
	v_div_scale_f32 v19, vcc, v3, v5, v3
	v_mul_f32_e32 v20, v19, v17
	v_fma_f32 v21, -v15, v20, v19
	v_fmac_f32_e32 v20, v21, v17
	v_fma_f32 v15, -v15, v20, v19
	v_div_fmas_f32 v15, v15, v17, v20
	v_div_fixup_f32 v3, v15, v5, v3
	v_sub_f32_e32 v3, v3, v4
	v_bfe_u32 v5, v3, 16, 1
	v_add3_u32 v3, v3, v5, s49
	ds_write_b16_d16_hi v121, v3
	ds_read_u16 v3, v35 offset:29696
	s_waitcnt lgkmcnt(0)
	v_lshlrev_b32_e32 v17, 16, v3
	v_add_f32_e32 v5, v4, v17
	v_add_f32_e32 v3, v16, v5
	v_add_f32_e32 v12, v12, v3
	v_add_f32_e32 v4, v6, v12
	v_cvt_f32_i32_e32 v6, s12
	v_cndmask_b32_e64 v4, v4, v12, s[10:11]
	v_cndmask_b32_e64 v4, v4, v3, s[8:9]
	v_cndmask_b32_e64 v4, v4, v5, s[6:7]
	v_div_scale_f32 v15, s[12:13], v6, v6, v4
	v_rcp_f32_e32 v16, v15
	s_or_b32 s12, s15, 15
	s_min_i32 s12, s12, s28
	v_fma_f32 v19, -v15, v16, 1.0
	v_fmac_f32_e32 v16, v19, v16
	v_div_scale_f32 v19, vcc, v4, v6, v4
	v_mul_f32_e32 v20, v19, v16
	v_fma_f32 v21, -v15, v20, v19
	v_fmac_f32_e32 v20, v21, v16
	v_fma_f32 v15, -v15, v20, v19
	v_div_fmas_f32 v15, v15, v16, v20
	v_div_fixup_f32 v4, v15, v6, v4
	v_sub_f32_e32 v4, v4, v17
	v_bfe_u32 v6, v4, 16, 1
	v_add3_u32 v4, v4, v6, s49
	ds_write_b16_d16_hi v122, v4
	ds_read_u16 v4, v35 offset:30720
	v_cvt_f32_i32_e32 v16, s12
	s_waitcnt lgkmcnt(0)
	v_lshlrev_b32_e32 v15, 16, v4
	v_add_f32_e32 v6, v17, v15
	v_add_f32_e32 v4, v18, v6
	v_add_f32_e32 v13, v13, v4
	v_add_f32_e32 v7, v7, v13
	v_cndmask_b32_e64 v7, v7, v13, s[10:11]
	v_cndmask_b32_e64 v7, v7, v4, s[8:9]
	v_cndmask_b32_e64 v7, v7, v6, s[6:7]
	v_div_scale_f32 v17, s[12:13], v16, v16, v7
	v_rcp_f32_e32 v18, v17
	s_or_b32 s12, s15, 16
	s_min_i32 s12, s12, s28
	v_fma_f32 v19, -v17, v18, 1.0
	v_fmac_f32_e32 v18, v19, v18
	v_div_scale_f32 v19, vcc, v7, v16, v7
	v_mul_f32_e32 v20, v19, v18
	v_fma_f32 v21, -v17, v20, v19
	v_fmac_f32_e32 v20, v21, v18
	v_fma_f32 v17, -v17, v20, v19
	v_div_fmas_f32 v17, v17, v18, v20
	v_div_fixup_f32 v7, v17, v16, v7
	v_sub_f32_e32 v7, v7, v15
	v_bfe_u32 v16, v7, 16, 1
	v_add3_u32 v7, v7, v16, s49
	ds_write_b16_d16_hi v123, v7
	ds_read_u16 v7, v35 offset:31744
	s_waitcnt lgkmcnt(0)
	v_lshlrev_b32_e32 v7, 16, v7
	v_add_f32_e32 v15, v15, v7
	v_add_f32_e32 v16, v5, v15
	v_add_f32_e32 v1, v1, v16
	v_add_f32_e32 v0, v0, v1
	v_cvt_f32_i32_e32 v5, s12
	v_cndmask_b32_e64 v0, v0, v1, s[10:11]
	v_cndmask_b32_e64 v0, v0, v16, s[8:9]
	v_cndmask_b32_e64 v0, v0, v15, s[6:7]
	v_div_scale_f32 v17, s[12:13], v5, v5, v0
	v_rcp_f32_e32 v18, v17
	s_or_b32 s12, s15, 17
	s_min_i32 s12, s12, s28
	v_fma_f32 v19, -v17, v18, 1.0
	v_fmac_f32_e32 v18, v19, v18
	v_div_scale_f32 v19, vcc, v0, v5, v0
	v_mul_f32_e32 v20, v19, v18
	v_fma_f32 v21, -v17, v20, v19
	v_fmac_f32_e32 v20, v21, v18
	v_fma_f32 v17, -v17, v20, v19
	v_div_fmas_f32 v17, v17, v18, v20
	v_div_fixup_f32 v0, v17, v5, v0
	v_sub_f32_e32 v0, v0, v7
	v_bfe_u32 v5, v0, 16, 1
	v_add3_u32 v0, v0, v5, s49
	ds_write_b16_d16_hi v124, v0
	ds_read_u16 v0, v35 offset:32768
	s_waitcnt lgkmcnt(0)
	v_lshlrev_b32_e32 v17, 16, v0
	v_add_f32_e32 v7, v7, v17
	v_add_f32_e32 v5, v6, v7
	v_add_f32_e32 v0, v2, v5
	v_add_f32_e32 v2, v14, v0
	v_cvt_f32_i32_e32 v6, s12
	v_cndmask_b32_e64 v2, v2, v0, s[10:11]
	v_cndmask_b32_e64 v2, v2, v5, s[8:9]
	v_cndmask_b32_e64 v2, v2, v7, s[6:7]
	v_div_scale_f32 v14, s[12:13], v6, v6, v2
	v_rcp_f32_e32 v18, v14
	s_or_b32 s12, s15, 18
	s_min_i32 s12, s12, s28
	v_fma_f32 v19, -v14, v18, 1.0
	v_fmac_f32_e32 v18, v19, v18
	v_div_scale_f32 v19, vcc, v2, v6, v2
	v_mul_f32_e32 v20, v19, v18
	v_fma_f32 v21, -v14, v20, v19
	v_fmac_f32_e32 v20, v21, v18
	v_fma_f32 v14, -v14, v20, v19
	v_div_fmas_f32 v14, v14, v18, v20
	v_div_fixup_f32 v2, v14, v6, v2
	v_sub_f32_e32 v2, v2, v17
	v_bfe_u32 v6, v2, 16, 1
	v_add3_u32 v2, v2, v6, s49
	ds_write_b16_d16_hi v125, v2
	ds_read_u16 v2, v35 offset:33792
	s_waitcnt lgkmcnt(0)
	v_lshlrev_b32_e32 v14, 16, v2
	v_add_f32_e32 v17, v17, v14
	v_add_f32_e32 v6, v15, v17
	v_add_f32_e32 v2, v3, v6
	v_add_f32_e32 v3, v8, v2
	v_cvt_f32_i32_e32 v8, s12
	v_cndmask_b32_e64 v3, v3, v2, s[10:11]
	v_cndmask_b32_e64 v3, v3, v6, s[8:9]
	v_cndmask_b32_e64 v3, v3, v17, s[6:7]
	v_div_scale_f32 v15, s[12:13], v8, v8, v3
	v_rcp_f32_e32 v18, v15
	s_or_b32 s12, s15, 19
	s_min_i32 s12, s12, s28
	v_fma_f32 v19, -v15, v18, 1.0
	v_fmac_f32_e32 v18, v19, v18
	v_div_scale_f32 v19, vcc, v3, v8, v3
	v_mul_f32_e32 v20, v19, v18
	v_fma_f32 v21, -v15, v20, v19
	v_fmac_f32_e32 v20, v21, v18
	v_fma_f32 v15, -v15, v20, v19
	v_div_fmas_f32 v15, v15, v18, v20
	v_div_fixup_f32 v3, v15, v8, v3
	v_sub_f32_e32 v3, v3, v14
	v_bfe_u32 v8, v3, 16, 1
	v_add3_u32 v3, v3, v8, s49
	ds_write_b16_d16_hi v126, v3
	ds_read_u16 v3, v35 offset:34816
	s_waitcnt lgkmcnt(0)
; __device__ __forceinline__ unsigned f2bf(float f) { unsigned u = __builtin_bit_cast(unsigned, f); return (u + 0x7fffu + ((u >> 16) & 1u)) >> 16; }
; __device__ __forceinline__ void phase_even_mix(CArgs a, LAS unsigned char* lds, int i2, int wv, int xw  ) {
;     ...
;             for (int r = 0; r < 48; ++r) {
;                 const float p = bf2f(glu[r * 512 + c]);
;                 const float a2 = p + pprev, a4 = a2 + a2r[(r + 1) % 3], a8 = a4 + a4r[(r + 1) % 5], a16 = a8 + a8r[(r + 1) % 9];
;                 a2r[r % 3] = a2; a4r[r % 5] = a4; a8r[r % 9] = a8; pprev = p;
;                 if (r >= 16) { const float s = g == 0 ? a2 : (g == 1 ? a4 : (g == 2 ? a8 : a16));
;                     const int pos = t0 + r - 16; const float cnt = (float)((pos + 1) < winw ? (pos + 1) : winw);
;                     pl[(r - 16) * PLS + c] = (bf16)f2bf(s / cnt - p); }
	v_lshlrev_b32_e32 v8, 16, v3
	v_add_f32_e32 v14, v14, v8
	v_add_f32_e32 v7, v7, v14
	v_add_f32_e32 v3, v4, v7
	v_add_f32_e32 v4, v9, v3
	v_cvt_f32_i32_e32 v9, s12
	v_cndmask_b32_e64 v4, v4, v3, s[10:11]
	v_cndmask_b32_e64 v4, v4, v7, s[8:9]
	v_cndmask_b32_e64 v4, v4, v14, s[6:7]
	v_div_scale_f32 v15, s[12:13], v9, v9, v4
	v_rcp_f32_e32 v18, v15
	s_or_b32 s12, s15, 20
	s_min_i32 s12, s12, s28
	v_fma_f32 v19, -v15, v18, 1.0
	v_fmac_f32_e32 v18, v19, v18
	v_div_scale_f32 v19, vcc, v4, v9, v4
	v_mul_f32_e32 v20, v19, v18
	v_fma_f32 v21, -v15, v20, v19
	v_fmac_f32_e32 v20, v21, v18
	v_fma_f32 v15, -v15, v20, v19
	v_div_fmas_f32 v15, v15, v18, v20
	v_div_fixup_f32 v4, v15, v9, v4
	v_sub_f32_e32 v4, v4, v8
	v_bfe_u32 v9, v4, 16, 1
	v_add3_u32 v4, v4, v9, s49
	ds_write_b16_d16_hi v127, v4
	ds_read_u16 v4, v35 offset:35840
	s_waitcnt lgkmcnt(0)
	v_lshlrev_b32_e32 v9, 16, v4
	v_add_f32_e32 v15, v8, v9
	v_add_f32_e32 v8, v17, v15
	v_add_f32_e32 v4, v16, v8
	v_add_f32_e32 v10, v10, v4
	v_cvt_f32_i32_e32 v16, s12
	v_cndmask_b32_e64 v10, v10, v4, s[10:11]
	v_cndmask_b32_e64 v10, v10, v8, s[8:9]
	v_cndmask_b32_e64 v10, v10, v15, s[6:7]
	v_div_scale_f32 v17, s[12:13], v16, v16, v10
	v_rcp_f32_e32 v18, v17
	s_or_b32 s12, s15, 21
	s_min_i32 s12, s12, s28
	v_fma_f32 v19, -v17, v18, 1.0
	v_fmac_f32_e32 v18, v19, v18
	v_div_scale_f32 v19, vcc, v10, v16, v10
	v_mul_f32_e32 v20, v19, v18
	v_fma_f32 v21, -v17, v20, v19
	v_fmac_f32_e32 v20, v21, v18
	v_fma_f32 v17, -v17, v20, v19
	v_div_fmas_f32 v17, v17, v18, v20
	v_div_fixup_f32 v10, v17, v16, v10
	v_sub_f32_e32 v10, v10, v9
	v_bfe_u32 v16, v10, 16, 1
	v_add3_u32 v10, v10, v16, s49
	ds_write_b16_d16_hi v128, v10
	ds_read_u16 v10, v35 offset:36864
	s_waitcnt lgkmcnt(0)
	v_lshlrev_b32_e32 v10, 16, v10
	v_add_f32_e32 v16, v9, v10
	v_add_f32_e32 v9, v14, v16
	v_add_f32_e32 v5, v5, v9
	v_add_f32_e32 v11, v11, v5
	v_cvt_f32_i32_e32 v14, s12
	v_cndmask_b32_e64 v11, v11, v5, s[10:11]
	v_cndmask_b32_e64 v11, v11, v9, s[8:9]
	v_cndmask_b32_e64 v11, v11, v16, s[6:7]
	v_div_scale_f32 v17, s[12:13], v14, v14, v11
	v_rcp_f32_e32 v18, v17
	s_or_b32 s12, s15, 22
	s_min_i32 s12, s12, s28
	v_fma_f32 v19, -v17, v18, 1.0
	v_fmac_f32_e32 v18, v19, v18
	v_div_scale_f32 v19, vcc, v11, v14, v11
	v_mul_f32_e32 v20, v19, v18
	v_fma_f32 v21, -v17, v20, v19
	v_fmac_f32_e32 v20, v21, v18
	v_fma_f32 v17, -v17, v20, v19
	v_div_fmas_f32 v17, v17, v18, v20
	v_div_fixup_f32 v11, v17, v14, v11
	v_sub_f32_e32 v11, v11, v10
	v_bfe_u32 v14, v11, 16, 1
	v_add3_u32 v11, v11, v14, s49
	ds_write_b16_d16_hi v129, v11
	ds_read_u16 v11, v35 offset:37888
	s_waitcnt lgkmcnt(0)
	v_lshlrev_b32_e32 v11, 16, v11
	v_add_f32_e32 v14, v10, v11
	v_add_f32_e32 v10, v15, v14
	v_add_f32_e32 v6, v6, v10
	v_add_f32_e32 v12, v12, v6
	v_cvt_f32_i32_e32 v15, s12
	v_cndmask_b32_e64 v12, v12, v6, s[10:11]
	v_cndmask_b32_e64 v12, v12, v10, s[8:9]
	v_cndmask_b32_e64 v12, v12, v14, s[6:7]
	v_div_scale_f32 v17, s[12:13], v15, v15, v12
	v_rcp_f32_e32 v18, v17
	s_or_b32 s12, s15, 23
	s_min_i32 s12, s12, s28
	v_fma_f32 v19, -v17, v18, 1.0
	v_fmac_f32_e32 v18, v19, v18
	v_div_scale_f32 v19, vcc, v12, v15, v12
	v_mul_f32_e32 v20, v19, v18
	v_fma_f32 v21, -v17, v20, v19
	v_fmac_f32_e32 v20, v21, v18
	v_fma_f32 v17, -v17, v20, v19
	v_div_fmas_f32 v17, v17, v18, v20
	v_div_fixup_f32 v12, v17, v15, v12
	v_sub_f32_e32 v12, v12, v11
	v_bfe_u32 v15, v12, 16, 1
	v_add3_u32 v12, v12, v15, s49
	ds_write_b16_d16_hi v130, v12
	ds_read_u16 v12, v35 offset:38912
	s_waitcnt lgkmcnt(0)
	v_lshlrev_b32_e32 v15, 16, v12
	v_add_f32_e32 v12, v11, v15
	v_add_f32_e32 v11, v16, v12
	v_add_f32_e32 v7, v7, v11
	v_add_f32_e32 v13, v13, v7
	v_cvt_f32_i32_e32 v16, s12
	v_cndmask_b32_e64 v13, v13, v7, s[10:11]
	v_cndmask_b32_e64 v13, v13, v11, s[8:9]
	v_cndmask_b32_e64 v13, v13, v12, s[6:7]
	v_div_scale_f32 v17, s[12:13], v16, v16, v13
	v_rcp_f32_e32 v18, v17
	s_or_b32 s12, s15, 24
	s_min_i32 s12, s12, s28
	v_fma_f32 v19, -v17, v18, 1.0
	v_fmac_f32_e32 v18, v19, v18
	v_div_scale_f32 v19, vcc, v13, v16, v13
	v_mul_f32_e32 v20, v19, v18
	v_fma_f32 v21, -v17, v20, v19
	v_fmac_f32_e32 v20, v21, v18
	v_fma_f32 v17, -v17, v20, v19
	v_div_fmas_f32 v17, v17, v18, v20
	v_div_fixup_f32 v13, v17, v16, v13
	v_sub_f32_e32 v13, v13, v15
	v_bfe_u32 v16, v13, 16, 1
	v_add3_u32 v13, v13, v16, s49
	ds_write_b16_d16_hi v131, v13
	ds_read_u16 v13, v35 offset:39936
	v_cvt_f32_i32_e32 v16, s12
	s_waitcnt lgkmcnt(0)
	v_lshlrev_b32_e32 v13, 16, v13
	v_add_f32_e32 v15, v15, v13
	v_add_f32_e32 v14, v14, v15
	v_add_f32_e32 v8, v8, v14
	v_add_f32_e32 v1, v1, v8
	v_cndmask_b32_e64 v1, v1, v8, s[10:11]
	v_cndmask_b32_e64 v1, v1, v14, s[8:9]
	v_cndmask_b32_e64 v1, v1, v15, s[6:7]
	v_div_scale_f32 v17, s[12:13], v16, v16, v1
	v_rcp_f32_e32 v18, v17
	s_or_b32 s12, s15, 25
	s_min_i32 s12, s12, s28
	v_fma_f32 v19, -v17, v18, 1.0
	v_fmac_f32_e32 v18, v19, v18
	v_div_scale_f32 v19, vcc, v1, v16, v1
	v_mul_f32_e32 v20, v19, v18
	v_fma_f32 v21, -v17, v20, v19
	v_fmac_f32_e32 v20, v21, v18
	v_fma_f32 v17, -v17, v20, v19
	v_div_fmas_f32 v17, v17, v18, v20
	v_div_fixup_f32 v1, v17, v16, v1
	v_sub_f32_e32 v1, v1, v13
	v_bfe_u32 v16, v1, 16, 1
	v_add3_u32 v1, v1, v16, s49
	ds_write_b16_d16_hi v132, v1
	ds_read_u16 v1, v35 offset:40960
	s_waitcnt lgkmcnt(0)
; __device__ __forceinline__ unsigned f2bf(float f) { unsigned u = __builtin_bit_cast(unsigned, f); return (u + 0x7fffu + ((u >> 16) & 1u)) >> 16; }
; __device__ __forceinline__ void phase_even_mix(CArgs a, LAS unsigned char* lds, int i2, int wv, int xw  ) {
;     ...
;             for (int r = 0; r < 48; ++r) {
;                 const float p = bf2f(glu[r * 512 + c]);
;                 const float a2 = p + pprev, a4 = a2 + a2r[(r + 1) % 3], a8 = a4 + a4r[(r + 1) % 5], a16 = a8 + a8r[(r + 1) % 9];
;                 a2r[r % 3] = a2; a4r[r % 5] = a4; a8r[r % 9] = a8; pprev = p;
;                 if (r >= 16) { const float s = g == 0 ? a2 : (g == 1 ? a4 : (g == 2 ? a8 : a16));
;                     const int pos = t0 + r - 16; const float cnt = (float)((pos + 1) < winw ? (pos + 1) : winw);
;                     pl[(r - 16) * PLS + c] = (bf16)f2bf(s / cnt - p); }
;             }
;         }
;         __syncthreads();
	v_lshlrev_b32_e32 v16, 16, v1
	v_add_f32_e32 v13, v13, v16
	v_add_f32_e32 v1, v12, v13
	v_add_f32_e32 v9, v9, v1
	v_add_f32_e32 v0, v0, v9
	v_cndmask_b32_e64 v0, v0, v9, s[10:11]
	v_cvt_f32_i32_e32 v9, s12
	v_cndmask_b32_e64 v0, v0, v1, s[8:9]
	v_cndmask_b32_e64 v0, v0, v13, s[6:7]
	v_div_scale_f32 v12, s[12:13], v9, v9, v0
	v_rcp_f32_e32 v17, v12
	s_or_b32 s12, s15, 26
	s_min_i32 s12, s12, s28
	v_fma_f32 v18, -v12, v17, 1.0
	v_fmac_f32_e32 v17, v18, v17
	v_div_scale_f32 v18, vcc, v0, v9, v0
	v_mul_f32_e32 v19, v18, v17
	v_fma_f32 v20, -v12, v19, v18
	v_fmac_f32_e32 v19, v20, v17
	v_fma_f32 v12, -v12, v19, v18
	v_div_fmas_f32 v12, v12, v17, v19
	v_div_fixup_f32 v0, v12, v9, v0
	v_sub_f32_e32 v0, v0, v16
	v_bfe_u32 v9, v0, 16, 1
	v_add3_u32 v0, v0, v9, s49
	ds_write_b16_d16_hi v133, v0
	ds_read_u16 v0, v35 offset:41984
	s_waitcnt lgkmcnt(0)
	v_lshlrev_b32_e32 v0, 16, v0
	v_add_f32_e32 v12, v16, v0
	v_add_f32_e32 v9, v15, v12
	v_add_f32_e32 v10, v10, v9
	v_add_f32_e32 v2, v2, v10
	v_cndmask_b32_e64 v2, v2, v10, s[10:11]
	v_cvt_f32_i32_e32 v10, s12
	v_cndmask_b32_e64 v2, v2, v9, s[8:9]
	v_cndmask_b32_e64 v2, v2, v12, s[6:7]
	v_div_scale_f32 v15, s[12:13], v10, v10, v2
	v_rcp_f32_e32 v16, v15
	s_or_b32 s12, s15, 27
	s_min_i32 s12, s12, s28
	v_fma_f32 v17, -v15, v16, 1.0
	v_fmac_f32_e32 v16, v17, v16
	v_div_scale_f32 v17, vcc, v2, v10, v2
	v_mul_f32_e32 v18, v17, v16
	v_fma_f32 v19, -v15, v18, v17
	v_fmac_f32_e32 v18, v19, v16
	v_fma_f32 v15, -v15, v18, v17
	v_div_fmas_f32 v15, v15, v16, v18
	v_div_fixup_f32 v2, v15, v10, v2
	v_sub_f32_e32 v2, v2, v0
	v_bfe_u32 v10, v2, 16, 1
	v_add3_u32 v2, v2, v10, s49
	ds_write_b16_d16_hi v134, v2
	ds_read_u16 v2, v35 offset:43008
	s_waitcnt lgkmcnt(0)
	v_lshlrev_b32_e32 v2, 16, v2
	v_add_f32_e32 v15, v0, v2
	v_add_f32_e32 v10, v13, v15
	v_add_f32_e32 v0, v11, v10
	v_add_f32_e32 v3, v3, v0
	v_cndmask_b32_e64 v0, v3, v0, s[10:11]
	v_cvt_f32_i32_e32 v3, s12
	v_cndmask_b32_e64 v0, v0, v10, s[8:9]
	v_cndmask_b32_e64 v0, v0, v15, s[6:7]
	v_div_scale_f32 v11, s[12:13], v3, v3, v0
	v_rcp_f32_e32 v13, v11
	s_or_b32 s12, s15, 28
	s_min_i32 s12, s12, s28
	v_fma_f32 v16, -v11, v13, 1.0
	v_fmac_f32_e32 v13, v16, v13
	v_div_scale_f32 v16, vcc, v0, v3, v0
	v_mul_f32_e32 v17, v16, v13
	v_fma_f32 v18, -v11, v17, v16
	v_fmac_f32_e32 v17, v18, v13
	v_fma_f32 v11, -v11, v17, v16
	v_div_fmas_f32 v11, v11, v13, v17
	v_div_fixup_f32 v0, v11, v3, v0
	v_sub_f32_e32 v0, v0, v2
	v_bfe_u32 v3, v0, 16, 1
	v_add3_u32 v0, v0, v3, s49
	ds_write_b16_d16_hi v135, v0
	ds_read_u16 v0, v35 offset:44032
	s_waitcnt lgkmcnt(0)
	v_lshlrev_b32_e32 v3, 16, v0
	v_add_f32_e32 v2, v2, v3
	v_add_f32_e32 v0, v12, v2
	v_add_f32_e32 v11, v14, v0
	v_add_f32_e32 v4, v4, v11
	v_cndmask_b32_e64 v4, v4, v11, s[10:11]
	v_cvt_f32_i32_e32 v11, s12
	v_cndmask_b32_e64 v4, v4, v0, s[8:9]
	v_cndmask_b32_e64 v4, v4, v2, s[6:7]
	v_div_scale_f32 v12, s[12:13], v11, v11, v4
	v_rcp_f32_e32 v13, v12
	s_or_b32 s12, s15, 29
	s_min_i32 s12, s12, s28
	v_fma_f32 v14, -v12, v13, 1.0
	v_fmac_f32_e32 v13, v14, v13
	v_div_scale_f32 v14, vcc, v4, v11, v4
	v_mul_f32_e32 v16, v14, v13
	v_fma_f32 v17, -v12, v16, v14
	v_fmac_f32_e32 v16, v17, v13
	v_fma_f32 v12, -v12, v16, v14
	v_div_fmas_f32 v12, v12, v13, v16
	v_div_fixup_f32 v4, v12, v11, v4
	v_sub_f32_e32 v4, v4, v3
	v_bfe_u32 v11, v4, 16, 1
	v_add3_u32 v4, v4, v11, s49
	ds_write_b16_d16_hi v136, v4
	ds_read_u16 v4, v35 offset:45056
	s_waitcnt lgkmcnt(0)
	v_lshlrev_b32_e32 v4, 16, v4
	v_add_f32_e32 v3, v3, v4
	v_add_f32_e32 v11, v15, v3
	v_add_f32_e32 v1, v1, v11
	v_add_f32_e32 v5, v5, v1
	v_cndmask_b32_e64 v1, v5, v1, s[10:11]
	v_cvt_f32_i32_e32 v5, s12
	v_cndmask_b32_e64 v1, v1, v11, s[8:9]
	v_cndmask_b32_e64 v1, v1, v3, s[6:7]
	v_div_scale_f32 v11, s[12:13], v5, v5, v1
	v_rcp_f32_e32 v12, v11
	s_or_b32 s12, s15, 30
	s_min_i32 s12, s12, s28
	v_fma_f32 v13, -v11, v12, 1.0
	v_fmac_f32_e32 v12, v13, v12
	v_div_scale_f32 v13, vcc, v1, v5, v1
	v_mul_f32_e32 v14, v13, v12
	v_fma_f32 v15, -v11, v14, v13
	v_fmac_f32_e32 v14, v15, v12
	v_fma_f32 v11, -v11, v14, v13
	v_div_fmas_f32 v11, v11, v12, v14
	v_div_fixup_f32 v1, v11, v5, v1
	v_sub_f32_e32 v1, v1, v4
	v_bfe_u32 v5, v1, 16, 1
	v_add3_u32 v1, v1, v5, s49
	ds_write_b16_d16_hi v137, v1
	ds_read_u16 v1, v35 offset:46080
	s_waitcnt lgkmcnt(0)
	v_lshlrev_b32_e32 v5, 16, v1
	v_add_f32_e32 v1, v4, v5
	v_add_f32_e32 v2, v2, v1
	v_add_f32_e32 v4, v9, v2
	v_add_f32_e32 v6, v6, v4
	v_cndmask_b32_e64 v4, v6, v4, s[10:11]
	v_cndmask_b32_e64 v2, v4, v2, s[8:9]
	v_cvt_f32_i32_e32 v4, s12
	v_cndmask_b32_e64 v2, v2, v1, s[6:7]
	v_div_scale_f32 v6, s[12:13], v4, v4, v2
	v_rcp_f32_e32 v9, v6
	s_or_b32 s12, s15, 31
	s_min_i32 s12, s12, s28
	s_add_i32 s15, s15, 32
	v_fma_f32 v11, -v6, v9, 1.0
	v_fmac_f32_e32 v9, v11, v9
	v_div_scale_f32 v11, vcc, v2, v4, v2
	v_mul_f32_e32 v12, v11, v9
	v_fma_f32 v13, -v6, v12, v11
	v_fmac_f32_e32 v12, v13, v9
	v_fma_f32 v6, -v6, v12, v11
	v_div_fmas_f32 v6, v6, v9, v12
	v_div_fixup_f32 v2, v6, v4, v2
	v_sub_f32_e32 v2, v2, v5
	v_bfe_u32 v4, v2, 16, 1
	v_add3_u32 v2, v2, v4, s49
	ds_write_b16_d16_hi v138, v2
	ds_read_u16 v2, v35 offset:47104
	s_waitcnt lgkmcnt(0)
	v_lshlrev_b32_e32 v2, 16, v2
	v_add_f32_e32 v4, v5, v2
	v_add_f32_e32 v3, v3, v4
	v_add_f32_e32 v5, v10, v3
	v_add_f32_e32 v6, v7, v5
	v_cndmask_b32_e64 v5, v6, v5, s[10:11]
	v_cndmask_b32_e64 v3, v5, v3, s[8:9]
	v_cndmask_b32_e64 v3, v3, v4, s[6:7]
	v_cvt_f32_i32_e32 v4, s12
	v_div_scale_f32 v5, s[12:13], v4, v4, v3
	v_rcp_f32_e32 v6, v5
	s_min_i32 s12, s15, s28
	v_fma_f32 v7, -v5, v6, 1.0
	v_fmac_f32_e32 v6, v7, v6
	v_div_scale_f32 v7, vcc, v3, v4, v3
	v_mul_f32_e32 v9, v7, v6
	v_fma_f32 v10, -v5, v9, v7
	v_fmac_f32_e32 v9, v10, v6
	v_fma_f32 v5, -v5, v9, v7
	v_div_fmas_f32 v5, v5, v6, v9
	v_div_fixup_f32 v3, v5, v4, v3
	v_sub_f32_e32 v3, v3, v2
	v_bfe_u32 v4, v3, 16, 1
	v_add3_u32 v3, v3, v4, s49
	ds_write_b16_d16_hi v139, v3
	ds_read_u16 v3, v35 offset:48128
	s_waitcnt lgkmcnt(0)
	v_lshlrev_b32_e32 v3, 16, v3
	v_add_f32_e32 v2, v2, v3
	v_add_f32_e32 v1, v1, v2
	v_add_f32_e32 v0, v0, v1
	v_add_f32_e32 v4, v8, v0
	v_cndmask_b32_e64 v0, v4, v0, s[10:11]
	v_cndmask_b32_e64 v0, v0, v1, s[8:9]
	v_cvt_f32_i32_e32 v1, s12
	v_cndmask_b32_e64 v0, v0, v2, s[6:7]
	v_div_scale_f32 v2, s[12:13], v1, v1, v0
	v_rcp_f32_e32 v4, v2
	s_lshl_b64 s[12:13], s[94:95], 2
	s_add_u32 s12, s16, s12
	s_addc_u32 s13, s17, s13
	v_fma_f32 v5, -v2, v4, 1.0
	v_fmac_f32_e32 v4, v5, v4
	v_div_scale_f32 v5, vcc, v0, v1, v0
	v_mul_f32_e32 v6, v5, v4
	v_fma_f32 v7, -v2, v6, v5
	v_fmac_f32_e32 v6, v7, v4
	v_fma_f32 v2, -v2, v6, v5
	v_div_fmas_f32 v2, v2, v4, v6
	v_div_fixup_f32 v0, v2, v1, v0
	v_sub_f32_e32 v0, v0, v3
	v_bfe_u32 v1, v0, 16, 1
	v_add3_u32 v0, v0, v1, s49
	ds_write_b16_d16_hi v140, v0
	s_waitcnt lgkmcnt(0)
	s_barrier
; #define LAS __attribute__((address_space(3)))
; __device__ __forceinline__ unsigned pk2(float lo, float hi) { unsigned r; asm("v_cvt_pk_bf16_f32 %0, %1, %2" : "=v"(r) : "v"(lo), "v"(hi)); return r; }
; __device__ __forceinline__ void phase_even_mix(CArgs a, LAS unsigned char* lds, int i2, int wv, int xw  ) {
;     ...
;         {
;             const int g = wave >> 1, nh = wave & 1, fr = lane & 15, fq = lane >> 4;
;             const bf16* wp = (const bf16*)(a->ws + WS_WPOOL) + ((size_t)i2 * 4 + g) * 128 * 128;
;             f32x4 acc[2][4];
; #pragma unroll
;             for (int m = 0; m < 2; ++m)
; #pragma unroll
;                 for (int n = 0; n < 4; ++n) acc[m][n] = (f32x4){0.f, 0.f, 0.f, 0.f};
; #pragma unroll
;             for (int ks = 0; ks < 4; ++ks) {
;                 bf16x8 af[2], bfr[4];
; #pragma unroll
;                 for (int m = 0; m < 2; ++m) af[m] = *(const LAS bf16x8*)(pl + (m * 16 + fr) * PLS + g * 128 + ks * 32 + fq * 8);
; #pragma unroll
;                 for (int n = 0; n < 4; ++n) bfr[n] = *(const bf16x8*)(wp + (size_t)(nh * 64 + n * 16 + fr) * 128 + ks * 32 + fq * 8);
; #pragma unroll
;                 for (int m = 0; m < 2; ++m)
; #pragma unroll
;                     for (int n = 0; n < 4; ++n) acc[m][n] = __builtin_amdgcn_mfma_f32_16x16x32_bf16(bfr[n], af[m], acc[m][n], 0, 0, 0);
;             }
; #pragma unroll
;             for (int n = 0; n < 4; ++n) { const int d = nh * 64 + n * 16 + 4 * fq;
;                 const f32x4 pb = *(const f32x4*)(a->in[I_POOLB] + ((size_t)i2 * 4 + g) * 128 + d), ps = *(const f32x4*)(a->in[I_POOLS] + (size_t)i2 * 512 + g * 128 + d);
; #pragma unroll
;                 for (int m = 0; m < 2; ++m) { const f32x4 v = (acc[m][n] + pb) * ps; u32x2 wv2; wv2.x = pk2(v.x, v.y); wv2.y = pk2(v.z, v.w);
;                     *(u32x2*)(YB + (tokbase + m * 16 + fr) * DM + g * 128 + d) = wv2; } }
;         }
;         __syncthreads();
	s_add_u32 s15, s18, s96
	s_addc_u32 s17, s19, s97
	s_add_u32 s16, s15, s58
	s_addc_u32 s17, s17, s59
	s_andn2_b64 vcc, exec, s[68:69]
	global_load_dwordx4 v[16:19], v[60:61], off
	ds_read_b128 v[0:3], v144
	ds_read_b128 v[4:7], v144 offset:16640
	ds_read_b128 v[8:11], v144 offset:64
	ds_read_b128 v[12:15], v144 offset:16704
	s_waitcnt vmcnt(1) lgkmcnt(2)
	v_mfma_f32_16x16x32_bf16 v[154:157], v[200:203], v[0:3], 0
	v_mfma_f32_16x16x32_bf16 v[158:161], v[204:207], v[0:3], 0
	v_mfma_f32_16x16x32_bf16 v[162:165], v[208:211], v[0:3], 0
	v_mfma_f32_16x16x32_bf16 v[166:169], v[212:215], v[0:3], 0
	v_mfma_f32_16x16x32_bf16 v[170:173], v[200:203], v[4:7], 0
	v_mfma_f32_16x16x32_bf16 v[174:177], v[204:207], v[4:7], 0
	v_mfma_f32_16x16x32_bf16 v[192:195], v[208:211], v[4:7], 0
	v_mfma_f32_16x16x32_bf16 v[196:199], v[212:215], v[4:7], 0
	ds_read_b128 v[0:3], v144 offset:128
	ds_read_b128 v[4:7], v144 offset:16768
	s_waitcnt lgkmcnt(2)
	v_mfma_f32_16x16x32_bf16 v[154:157], v[216:219], v[8:11], v[154:157]
	v_mfma_f32_16x16x32_bf16 v[158:161], v[220:223], v[8:11], v[158:161]
	v_mfma_f32_16x16x32_bf16 v[162:165], v[224:227], v[8:11], v[162:165]
	v_mfma_f32_16x16x32_bf16 v[166:169], v[228:231], v[8:11], v[166:169]
	v_mfma_f32_16x16x32_bf16 v[170:173], v[216:219], v[12:15], v[170:173]
	v_mfma_f32_16x16x32_bf16 v[174:177], v[220:223], v[12:15], v[174:177]
	v_mfma_f32_16x16x32_bf16 v[192:195], v[224:227], v[12:15], v[192:195]
	v_mfma_f32_16x16x32_bf16 v[196:199], v[228:231], v[12:15], v[196:199]
	global_load_dwordx4 v[200:203], v145, s[12:13]
	global_load_dwordx4 v[204:207], v145, s[16:17]
	global_load_dwordx4 v[208:211], v145, s[12:13] offset:64
	global_load_dwordx4 v[212:215], v145, s[16:17] offset:64
	ds_read_b128 v[8:11], v144 offset:192
	ds_read_b128 v[12:15], v144 offset:16832
	s_waitcnt lgkmcnt(2)
	v_mfma_f32_16x16x32_bf16 v[154:157], v[232:235], v[0:3], v[154:157]
	v_mfma_f32_16x16x32_bf16 v[158:161], v[236:239], v[0:3], v[158:161]
	v_mfma_f32_16x16x32_bf16 v[162:165], v[240:243], v[0:3], v[162:165]
	v_mfma_f32_16x16x32_bf16 v[166:169], v[244:247], v[0:3], v[166:169]
	v_mfma_f32_16x16x32_bf16 v[170:173], v[232:235], v[4:7], v[170:173]
	v_mfma_f32_16x16x32_bf16 v[174:177], v[236:239], v[4:7], v[174:177]
	v_mfma_f32_16x16x32_bf16 v[192:195], v[240:243], v[4:7], v[192:195]
	v_mfma_f32_16x16x32_bf16 v[196:199], v[244:247], v[4:7], v[196:199]
	global_load_dwordx4 v[216:219], v145, s[12:13] offset:128
	global_load_dwordx4 v[220:223], v145, s[16:17] offset:128
	global_load_dwordx4 v[224:227], v145, s[12:13] offset:192
	global_load_dwordx4 v[228:231], v145, s[16:17] offset:192
	s_waitcnt vmcnt(8) lgkmcnt(0)
	v_mfma_f32_16x16x32_bf16 v[154:157], v[248:251], v[8:11], v[154:157]
	v_mfma_f32_16x16x32_bf16 v[158:161], v[64:67], v[8:11], v[158:161]
	v_mfma_f32_16x16x32_bf16 v[162:165], v[178:181], v[8:11], v[162:165]
	v_mfma_f32_16x16x32_bf16 v[166:169], v[16:19], v[8:11], v[166:169]
	v_mfma_f32_16x16x32_bf16 v[170:173], v[248:251], v[12:15], v[170:173]
	v_mfma_f32_16x16x32_bf16 v[174:177], v[64:67], v[12:15], v[174:177]
	v_mfma_f32_16x16x32_bf16 v[192:195], v[178:181], v[12:15], v[192:195]
	v_mfma_f32_16x16x32_bf16 v[196:199], v[16:19], v[12:15], v[196:199]
	s_mov_b64 s[12:13], 0
	s_nop 7
	s_nop 1
	v_mbcnt_lo_u32_b32 v4, -1, 0
	v_mbcnt_hi_u32_b32 v4, -1, v4
	v_mov_b32_e32 v1, s23
	v_or_b32_e32 v0, s22, v28
	v_mov_b32_e32 v3, s23
	v_or_b32_e32 v2, s22, v34
	v_lshrrev_b32_e32 v4, 1, v4
	v_lshlrev_b64 v[0:1], 11, v[0:1]
	v_lshlrev_b64 v[2:3], 11, v[2:3]
	v_and_b32_e32 v4, 24, v4
	v_mov_b32_e32 v5, 0
	v_lshl_add_u64 v[0:1], v[30:31], 0, v[0:1]
	v_lshl_add_u64 v[2:3], v[30:31], 0, v[2:3]
	v_lshl_add_u64 v[0:1], v[0:1], 0, v[4:5]
	v_lshl_add_u64 v[2:3], v[2:3], 0, v[4:5]
	s_waitcnt vmcnt(6)
	v_pk_add_f32 v[154:155], v[154:155], v[200:201]
	v_pk_add_f32 v[156:157], v[156:157], v[202:203]
	v_pk_add_f32 v[170:171], v[170:171], v[200:201]
	v_pk_add_f32 v[172:173], v[172:173], v[202:203]
	v_pk_mul_f32 v[154:155], v[204:205], v[154:155]
	v_pk_mul_f32 v[156:157], v[206:207], v[156:157]
	v_pk_mul_f32 v[170:171], v[204:205], v[170:171]
	v_pk_mul_f32 v[172:173], v[206:207], v[172:173]
	v_cvt_pk_bf16_f32 v232, v154, v155
	v_cvt_pk_bf16_f32 v233, v156, v157
	v_cvt_pk_bf16_f32 v240, v170, v171
	v_cvt_pk_bf16_f32 v241, v172, v173
	s_waitcnt vmcnt(4)
	v_pk_add_f32 v[158:159], v[158:159], v[208:209]
	v_pk_add_f32 v[160:161], v[160:161], v[210:211]
	v_pk_add_f32 v[174:175], v[174:175], v[208:209]
	v_pk_add_f32 v[176:177], v[176:177], v[210:211]
	v_pk_mul_f32 v[158:159], v[212:213], v[158:159]
	v_pk_mul_f32 v[160:161], v[214:215], v[160:161]
	v_pk_mul_f32 v[174:175], v[212:213], v[174:175]
	v_pk_mul_f32 v[176:177], v[214:215], v[176:177]
	v_cvt_pk_bf16_f32 v234, v158, v159
	v_cvt_pk_bf16_f32 v235, v160, v161
	v_cvt_pk_bf16_f32 v242, v174, v175
	v_cvt_pk_bf16_f32 v243, v176, v177
	s_waitcnt vmcnt(2)
	v_pk_add_f32 v[162:163], v[162:163], v[216:217]
	v_pk_add_f32 v[164:165], v[164:165], v[218:219]
	v_pk_add_f32 v[192:193], v[192:193], v[216:217]
	v_pk_add_f32 v[194:195], v[194:195], v[218:219]
	v_pk_mul_f32 v[162:163], v[220:221], v[162:163]
	v_pk_mul_f32 v[164:165], v[222:223], v[164:165]
	v_pk_mul_f32 v[192:193], v[220:221], v[192:193]
	v_pk_mul_f32 v[194:195], v[222:223], v[194:195]
	v_cvt_pk_bf16_f32 v236, v162, v163
	v_cvt_pk_bf16_f32 v237, v164, v165
	v_cvt_pk_bf16_f32 v244, v192, v193
	v_cvt_pk_bf16_f32 v245, v194, v195
	s_waitcnt vmcnt(0)
	v_pk_add_f32 v[166:167], v[166:167], v[224:225]
	v_pk_add_f32 v[168:169], v[168:169], v[226:227]
	v_pk_add_f32 v[196:197], v[196:197], v[224:225]
	v_pk_add_f32 v[198:199], v[198:199], v[226:227]
	v_pk_mul_f32 v[166:167], v[228:229], v[166:167]
	v_pk_mul_f32 v[168:169], v[230:231], v[168:169]
	v_pk_mul_f32 v[196:197], v[228:229], v[196:197]
	v_pk_mul_f32 v[198:199], v[230:231], v[198:199]
	v_cvt_pk_bf16_f32 v238, v166, v167
	v_cvt_pk_bf16_f32 v239, v168, v169
	v_cvt_pk_bf16_f32 v246, v196, v197
	v_cvt_pk_bf16_f32 v247, v198, v199
	s_nop 1
	v_permlane32_swap_b32_e32 v232, v234
	v_permlane32_swap_b32_e32 v233, v235
	v_permlane32_swap_b32_e32 v240, v242
	v_permlane32_swap_b32_e32 v241, v243
	v_permlane32_swap_b32_e32 v236, v238
	v_permlane32_swap_b32_e32 v237, v239
	v_permlane32_swap_b32_e32 v244, v246
	v_permlane32_swap_b32_e32 v245, v247
	v_permlane16_swap_b32_e32 v232, v234
	v_permlane16_swap_b32_e32 v233, v235
	v_permlane16_swap_b32_e32 v240, v242
	v_permlane16_swap_b32_e32 v241, v243
	v_permlane16_swap_b32_e32 v236, v238
	v_permlane16_swap_b32_e32 v237, v239
	v_permlane16_swap_b32_e32 v244, v246
	v_permlane16_swap_b32_e32 v245, v247
	s_nop 1
	global_store_dwordx4 v[0:1], v[232:235], off
	global_store_dwordx4 v[0:1], v[236:239], off offset:64
	global_store_dwordx4 v[2:3], v[240:243], off
	global_store_dwordx4 v[2:3], v[244:247], off offset:64
	s_barrier
	s_cbranch_vccz .LBB0_489

; #define LAS __attribute__((address_space(3)))
; __device__ __forceinline__ unsigned pk2(float lo, float hi) { unsigned r; asm("v_cvt_pk_bf16_f32 %0, %1, %2" : "=v"(r) : "v"(lo), "v"(hi)); return r; }
; __device__ __forceinline__ float sigmoidf_(float x) { return __builtin_amdgcn_rcpf(1.0f + __builtin_amdgcn_exp2f(x * -1.44269504089f)); }
; __device__ __forceinline__ void phase_even_mix(CArgs a, LAS unsigned char* lds, int i2, int wv, int xw  ) {
;     ...
;         for (int it = 0; it < 8; ++it) { const int item = it * NTHR + tid, tt = item >> 6, cg = item & 63, p = t0 - 32 + tt;
;             u32x4 o = (u32x4){0u, 0u, 0u, 0u};
;             if (p >= 0) { const bf16* hp = HB + ((size_t)b * SEQ + p) * EVEN_IN + cg * 8; const u32x4 ra = *(const u32x4*)(hp + 512), rg = *(const u32x4*)(hp + 1024);
;                 o.x = pk2(bflo(ra.x) * sigmoidf_(bflo(rg.x)), bfhi(ra.x) * sigmoidf_(bfhi(rg.x))); o.y = pk2(bflo(ra.y) * sigmoidf_(bflo(rg.y)), bfhi(ra.y) * sigmoidf_(bfhi(rg.y)));
;                 o.z = pk2(bflo(ra.z) * sigmoidf_(bflo(rg.z)), bfhi(ra.z) * sigmoidf_(bfhi(rg.z))); o.w = pk2(bflo(ra.w) * sigmoidf_(bflo(rg.w)), bfhi(ra.w) * sigmoidf_(bfhi(rg.w))); }
;             *(LAS u32x4*)(glu + tt * 512 + cg * 8) = o; }
.Le2st_skip7:
	s_or_b64 exec, exec, s[16:17]
	s_waitcnt vmcnt(8)
	v_lshlrev_b32_e32 v1, 16, v232
	v_lshlrev_b32_e32 v10, 16, v236
	v_and_b32_e32 v236, 0xffff0000, v236
	v_lshlrev_b32_e32 v12, 16, v237
	v_and_b32_e32 v237, 0xffff0000, v237
	v_lshlrev_b32_e32 v14, 16, v238
	v_and_b32_e32 v238, 0xffff0000, v238
	v_lshlrev_b32_e32 v16, 16, v239
	v_and_b32_e32 v239, 0xffff0000, v239
	v_mul_f32_e32 v236, 0xbfb8aa3b, v236
	v_mul_f32_e32 v237, 0xbfb8aa3b, v237
	v_mul_f32_e32 v238, 0xbfb8aa3b, v238
	v_mul_f32_e32 v239, 0xbfb8aa3b, v239
	v_mul_f32_e32 v10, 0xbfb8aa3b, v10
	v_mul_f32_e32 v12, 0xbfb8aa3b, v12
	v_mul_f32_e32 v14, 0xbfb8aa3b, v14
	v_mul_f32_e32 v16, 0xbfb8aa3b, v16
	v_exp_f32_e32 v236, v236
	v_exp_f32_e32 v237, v237
	v_exp_f32_e32 v238, v238
	v_exp_f32_e32 v239, v239
	v_exp_f32_e32 v10, v10
	v_exp_f32_e32 v12, v12
	v_exp_f32_e32 v14, v14
	v_exp_f32_e32 v16, v16
	v_add_f32_e32 v236, 1.0, v236
	v_add_f32_e32 v237, 1.0, v237
	v_add_f32_e32 v238, 1.0, v238
	v_add_f32_e32 v239, 1.0, v239
	v_add_f32_e32 v10, 1.0, v10
	v_add_f32_e32 v12, 1.0, v12
	v_add_f32_e32 v14, 1.0, v14
	v_add_f32_e32 v16, 1.0, v16
	v_rcp_f32_e32 v236, v236
	v_rcp_f32_e32 v237, v237
	v_rcp_f32_e32 v238, v238
	v_rcp_f32_e32 v239, v239
	v_rcp_f32_e32 v10, v10
	v_rcp_f32_e32 v12, v12
	v_rcp_f32_e32 v14, v14
	v_rcp_f32_e32 v16, v16
	v_and_b32_e32 v232, 0xffff0000, v232
	v_lshlrev_b32_e32 v11, 16, v233
	v_and_b32_e32 v233, 0xffff0000, v233
	v_lshlrev_b32_e32 v13, 16, v234
	v_and_b32_e32 v234, 0xffff0000, v234
	v_lshlrev_b32_e32 v15, 16, v235
	v_and_b32_e32 v235, 0xffff0000, v235
	v_mul_f32_e32 v232, v236, v232
	v_mul_f32_e32 v233, v237, v233
	v_mul_f32_e32 v234, v238, v234
	v_mul_f32_e32 v235, v239, v235
	v_mul_f32_e32 v1, v10, v1
	v_mul_f32_e32 v236, v12, v11
	v_mul_f32_e32 v237, v14, v13
	v_mul_f32_e32 v238, v16, v15
	v_cvt_pk_bf16_f32 v232, v1, v232
	v_cvt_pk_bf16_f32 v233, v236, v233
	v_cvt_pk_bf16_f32 v234, v237, v234
	v_cvt_pk_bf16_f32 v235, v238, v235
	ds_write_b128 v149, v[232:235]
	s_waitcnt vmcnt(6)
	v_lshlrev_b32_e32 v1, 16, v240
	v_lshlrev_b32_e32 v10, 16, v244
	v_and_b32_e32 v244, 0xffff0000, v244
	v_lshlrev_b32_e32 v12, 16, v245
	v_and_b32_e32 v245, 0xffff0000, v245
	v_lshlrev_b32_e32 v14, 16, v246
	v_and_b32_e32 v246, 0xffff0000, v246
	v_lshlrev_b32_e32 v16, 16, v247
	v_and_b32_e32 v247, 0xffff0000, v247
	v_mul_f32_e32 v244, 0xbfb8aa3b, v244
	v_mul_f32_e32 v245, 0xbfb8aa3b, v245
	v_mul_f32_e32 v246, 0xbfb8aa3b, v246
	v_mul_f32_e32 v247, 0xbfb8aa3b, v247
	v_mul_f32_e32 v10, 0xbfb8aa3b, v10
	v_mul_f32_e32 v12, 0xbfb8aa3b, v12
	v_mul_f32_e32 v14, 0xbfb8aa3b, v14
	v_mul_f32_e32 v16, 0xbfb8aa3b, v16
	v_exp_f32_e32 v244, v244
	v_exp_f32_e32 v245, v245
	v_exp_f32_e32 v246, v246
	v_exp_f32_e32 v247, v247
	v_exp_f32_e32 v10, v10
	v_exp_f32_e32 v12, v12
	v_exp_f32_e32 v14, v14
	v_exp_f32_e32 v16, v16
	v_add_f32_e32 v244, 1.0, v244
	v_add_f32_e32 v245, 1.0, v245
	v_add_f32_e32 v246, 1.0, v246
	v_add_f32_e32 v247, 1.0, v247
	v_add_f32_e32 v10, 1.0, v10
	v_add_f32_e32 v12, 1.0, v12
	v_add_f32_e32 v14, 1.0, v14
	v_add_f32_e32 v16, 1.0, v16
	v_rcp_f32_e32 v244, v244
	v_rcp_f32_e32 v245, v245
	v_rcp_f32_e32 v246, v246
	v_rcp_f32_e32 v247, v247
	v_rcp_f32_e32 v10, v10
	v_rcp_f32_e32 v12, v12
	v_rcp_f32_e32 v14, v14
	v_rcp_f32_e32 v16, v16
	v_and_b32_e32 v240, 0xffff0000, v240
	v_lshlrev_b32_e32 v11, 16, v241
	v_and_b32_e32 v241, 0xffff0000, v241
	v_lshlrev_b32_e32 v13, 16, v242
	v_and_b32_e32 v242, 0xffff0000, v242
	v_lshlrev_b32_e32 v15, 16, v243
	v_and_b32_e32 v243, 0xffff0000, v243
	v_mul_f32_e32 v240, v244, v240
	v_mul_f32_e32 v241, v245, v241
	v_mul_f32_e32 v242, v246, v242
	v_mul_f32_e32 v243, v247, v243
	v_mul_f32_e32 v1, v10, v1
	v_mul_f32_e32 v244, v12, v11
	v_mul_f32_e32 v245, v14, v13
	v_mul_f32_e32 v246, v16, v15
	v_cvt_pk_bf16_f32 v240, v1, v240
	v_cvt_pk_bf16_f32 v241, v244, v241
	v_cvt_pk_bf16_f32 v242, v245, v242
	v_cvt_pk_bf16_f32 v243, v246, v243
	ds_write_b128 v150, v[240:243]
	s_waitcnt vmcnt(4)
	v_lshlrev_b32_e32 v1, 16, v208
	v_lshlrev_b32_e32 v10, 16, v212
	v_and_b32_e32 v212, 0xffff0000, v212
	v_lshlrev_b32_e32 v12, 16, v213
	v_and_b32_e32 v213, 0xffff0000, v213
	v_lshlrev_b32_e32 v14, 16, v214
	v_and_b32_e32 v214, 0xffff0000, v214
	v_lshlrev_b32_e32 v16, 16, v215
	v_and_b32_e32 v215, 0xffff0000, v215
	v_mul_f32_e32 v212, 0xbfb8aa3b, v212
	v_mul_f32_e32 v213, 0xbfb8aa3b, v213
	v_mul_f32_e32 v214, 0xbfb8aa3b, v214
	v_mul_f32_e32 v215, 0xbfb8aa3b, v215
	v_mul_f32_e32 v10, 0xbfb8aa3b, v10
	v_mul_f32_e32 v12, 0xbfb8aa3b, v12
	v_mul_f32_e32 v14, 0xbfb8aa3b, v14
	v_mul_f32_e32 v16, 0xbfb8aa3b, v16
	v_exp_f32_e32 v212, v212
	v_exp_f32_e32 v213, v213
	v_exp_f32_e32 v214, v214
	v_exp_f32_e32 v215, v215
	v_exp_f32_e32 v10, v10
	v_exp_f32_e32 v12, v12
	v_exp_f32_e32 v14, v14
	v_exp_f32_e32 v16, v16
	v_add_f32_e32 v212, 1.0, v212
	v_add_f32_e32 v213, 1.0, v213
	v_add_f32_e32 v214, 1.0, v214
	v_add_f32_e32 v215, 1.0, v215
	v_add_f32_e32 v10, 1.0, v10
	v_add_f32_e32 v12, 1.0, v12
	v_add_f32_e32 v14, 1.0, v14
	v_add_f32_e32 v16, 1.0, v16
	v_rcp_f32_e32 v212, v212
	v_rcp_f32_e32 v213, v213
	v_rcp_f32_e32 v214, v214
	v_rcp_f32_e32 v215, v215
	v_rcp_f32_e32 v10, v10
	v_rcp_f32_e32 v12, v12
	v_rcp_f32_e32 v14, v14
	v_rcp_f32_e32 v16, v16
	v_and_b32_e32 v208, 0xffff0000, v208
	v_lshlrev_b32_e32 v11, 16, v209
	v_and_b32_e32 v209, 0xffff0000, v209
	v_lshlrev_b32_e32 v13, 16, v210
	v_and_b32_e32 v210, 0xffff0000, v210
	v_lshlrev_b32_e32 v15, 16, v211
	v_and_b32_e32 v211, 0xffff0000, v211
	v_mul_f32_e32 v208, v212, v208
	v_mul_f32_e32 v209, v213, v209
	v_mul_f32_e32 v210, v214, v210
	v_mul_f32_e32 v211, v215, v211
	v_mul_f32_e32 v1, v10, v1
	v_mul_f32_e32 v212, v12, v11
	v_mul_f32_e32 v213, v14, v13
	v_mul_f32_e32 v214, v16, v15
	v_cvt_pk_bf16_f32 v208, v1, v208
	v_cvt_pk_bf16_f32 v209, v212, v209
	v_cvt_pk_bf16_f32 v210, v213, v210
	v_cvt_pk_bf16_f32 v211, v214, v211
	ds_write_b128 v151, v[208:211]
	s_waitcnt vmcnt(2)
; #define LAS __attribute__((address_space(3)))
; __device__ __forceinline__ unsigned pk2(float lo, float hi) { unsigned r; asm("v_cvt_pk_bf16_f32 %0, %1, %2" : "=v"(r) : "v"(lo), "v"(hi)); return r; }
; __device__ __forceinline__ float sigmoidf_(float x) { return __builtin_amdgcn_rcpf(1.0f + __builtin_amdgcn_exp2f(x * -1.44269504089f)); }
; __device__ __forceinline__ void phase_even_mix(CArgs a, LAS unsigned char* lds, int i2, int wv, int xw  ) {
;     ...
;             if (p >= 0) { const bf16* hp = HB + ((size_t)b * SEQ + p) * EVEN_IN + cg * 8; const u32x4 ra = *(const u32x4*)(hp + 512), rg = *(const u32x4*)(hp + 1024);
;                 o.x = pk2(bflo(ra.x) * sigmoidf_(bflo(rg.x)), bfhi(ra.x) * sigmoidf_(bfhi(rg.x))); o.y = pk2(bflo(ra.y) * sigmoidf_(bflo(rg.y)), bfhi(ra.y) * sigmoidf_(bfhi(rg.y)));
;                 o.z = pk2(bflo(ra.z) * sigmoidf_(bflo(rg.z)), bfhi(ra.z) * sigmoidf_(bfhi(rg.z))); o.w = pk2(bflo(ra.w) * sigmoidf_(bflo(rg.w)), bfhi(ra.w) * sigmoidf_(bfhi(rg.w))); }
;             *(LAS u32x4*)(glu + tt * 512 + cg * 8) = o; }
;         __syncthreads();
;         {
;             float w[31];
; #pragma unroll
;             for (int k = 0; k < 31; ++k) { unsigned off = (unsigned)c * 4u; asm volatile("" : "+v"(off)); w[k] = *(const float*)((const char*)(cw + k * 512) + off); }
;             const float cb = a->in[I_CONVB][i2 * 512 + c];
	v_lshlrev_b32_e32 v1, 16, v216
	v_lshlrev_b32_e32 v10, 16, v220
	v_and_b32_e32 v220, 0xffff0000, v220
	v_lshlrev_b32_e32 v12, 16, v221
	v_and_b32_e32 v221, 0xffff0000, v221
	v_lshlrev_b32_e32 v14, 16, v222
	v_and_b32_e32 v222, 0xffff0000, v222
	v_lshlrev_b32_e32 v16, 16, v223
	v_and_b32_e32 v223, 0xffff0000, v223
	v_mul_f32_e32 v220, 0xbfb8aa3b, v220
	v_mul_f32_e32 v221, 0xbfb8aa3b, v221
	v_mul_f32_e32 v222, 0xbfb8aa3b, v222
	v_mul_f32_e32 v223, 0xbfb8aa3b, v223
	v_mul_f32_e32 v10, 0xbfb8aa3b, v10
	v_mul_f32_e32 v12, 0xbfb8aa3b, v12
	v_mul_f32_e32 v14, 0xbfb8aa3b, v14
	v_mul_f32_e32 v16, 0xbfb8aa3b, v16
	v_exp_f32_e32 v220, v220
	v_exp_f32_e32 v221, v221
	v_exp_f32_e32 v222, v222
	v_exp_f32_e32 v223, v223
	v_exp_f32_e32 v10, v10
	v_exp_f32_e32 v12, v12
	v_exp_f32_e32 v14, v14
	v_exp_f32_e32 v16, v16
	v_add_f32_e32 v220, 1.0, v220
	v_add_f32_e32 v221, 1.0, v221
	v_add_f32_e32 v222, 1.0, v222
	v_add_f32_e32 v223, 1.0, v223
	v_add_f32_e32 v10, 1.0, v10
	v_add_f32_e32 v12, 1.0, v12
	v_add_f32_e32 v14, 1.0, v14
	v_add_f32_e32 v16, 1.0, v16
	v_rcp_f32_e32 v220, v220
	v_rcp_f32_e32 v221, v221
	v_rcp_f32_e32 v222, v222
	v_rcp_f32_e32 v223, v223
	v_rcp_f32_e32 v10, v10
	v_rcp_f32_e32 v12, v12
	v_rcp_f32_e32 v14, v14
	v_rcp_f32_e32 v16, v16
	v_and_b32_e32 v216, 0xffff0000, v216
	v_lshlrev_b32_e32 v11, 16, v217
	v_and_b32_e32 v217, 0xffff0000, v217
	v_lshlrev_b32_e32 v13, 16, v218
	v_and_b32_e32 v218, 0xffff0000, v218
	v_lshlrev_b32_e32 v15, 16, v219
	v_and_b32_e32 v219, 0xffff0000, v219
	v_mul_f32_e32 v216, v220, v216
	v_mul_f32_e32 v217, v221, v217
	v_mul_f32_e32 v218, v222, v218
	v_mul_f32_e32 v219, v223, v219
	v_mul_f32_e32 v1, v10, v1
	v_mul_f32_e32 v220, v12, v11
	v_mul_f32_e32 v221, v14, v13
	v_mul_f32_e32 v222, v16, v15
	v_cvt_pk_bf16_f32 v216, v1, v216
	v_cvt_pk_bf16_f32 v217, v220, v217
	v_cvt_pk_bf16_f32 v218, v221, v218
	v_cvt_pk_bf16_f32 v219, v222, v219
	ds_write_b128 v141, v[216:219]
	s_waitcnt vmcnt(0)
	v_lshlrev_b32_e32 v1, 16, v224
	v_lshlrev_b32_e32 v10, 16, v228
	v_and_b32_e32 v228, 0xffff0000, v228
	v_lshlrev_b32_e32 v12, 16, v229
	v_and_b32_e32 v229, 0xffff0000, v229
	v_lshlrev_b32_e32 v14, 16, v230
	v_and_b32_e32 v230, 0xffff0000, v230
	v_lshlrev_b32_e32 v16, 16, v231
	v_and_b32_e32 v231, 0xffff0000, v231
	v_mul_f32_e32 v228, 0xbfb8aa3b, v228
	v_mul_f32_e32 v229, 0xbfb8aa3b, v229
	v_mul_f32_e32 v230, 0xbfb8aa3b, v230
	v_mul_f32_e32 v231, 0xbfb8aa3b, v231
	v_mul_f32_e32 v10, 0xbfb8aa3b, v10
	v_mul_f32_e32 v12, 0xbfb8aa3b, v12
	v_mul_f32_e32 v14, 0xbfb8aa3b, v14
	v_mul_f32_e32 v16, 0xbfb8aa3b, v16
	v_exp_f32_e32 v228, v228
	v_exp_f32_e32 v229, v229
	v_exp_f32_e32 v230, v230
	v_exp_f32_e32 v231, v231
	v_exp_f32_e32 v10, v10
	v_exp_f32_e32 v12, v12
	v_exp_f32_e32 v14, v14
	v_exp_f32_e32 v16, v16
	v_add_f32_e32 v228, 1.0, v228
	v_add_f32_e32 v229, 1.0, v229
	v_add_f32_e32 v230, 1.0, v230
	v_add_f32_e32 v231, 1.0, v231
	v_add_f32_e32 v10, 1.0, v10
	v_add_f32_e32 v12, 1.0, v12
	v_add_f32_e32 v14, 1.0, v14
	v_add_f32_e32 v16, 1.0, v16
	v_rcp_f32_e32 v228, v228
	v_rcp_f32_e32 v229, v229
	v_rcp_f32_e32 v230, v230
	v_rcp_f32_e32 v231, v231
	v_rcp_f32_e32 v10, v10
	v_rcp_f32_e32 v12, v12
	v_rcp_f32_e32 v14, v14
	v_rcp_f32_e32 v16, v16
	v_and_b32_e32 v224, 0xffff0000, v224
	v_lshlrev_b32_e32 v11, 16, v225
	v_and_b32_e32 v225, 0xffff0000, v225
	v_lshlrev_b32_e32 v13, 16, v226
	v_and_b32_e32 v226, 0xffff0000, v226
	v_lshlrev_b32_e32 v15, 16, v227
	v_and_b32_e32 v227, 0xffff0000, v227
	v_mul_f32_e32 v224, v228, v224
	v_mul_f32_e32 v225, v229, v225
	v_mul_f32_e32 v226, v230, v226
	v_mul_f32_e32 v227, v231, v227
	v_mul_f32_e32 v1, v10, v1
	v_mul_f32_e32 v228, v12, v11
	v_mul_f32_e32 v229, v14, v13
	v_mul_f32_e32 v230, v16, v15
	v_cvt_pk_bf16_f32 v224, v1, v224
	v_cvt_pk_bf16_f32 v225, v228, v225
	v_cvt_pk_bf16_f32 v226, v229, v226
	v_cvt_pk_bf16_f32 v227, v230, v227
	ds_write_b128 v142, v[224:227]
	v_mov_b32_e32 v0, v29
	s_waitcnt vmcnt(0) lgkmcnt(0)
	s_barrier
	v_mov_b32_e32 v1, v29
	global_load_dword v0, v0, s[90:91]
	v_mov_b32_e32 v2, v29
	v_readlane_b32 s16, v254, 33
	global_load_dword v1, v1, s[90:91] offset:2048
	v_readlane_b32 s17, v254, 34
	v_mov_b32_e32 v3, v29
	v_mov_b32_e32 v4, v29
	v_mov_b32_e32 v5, v29
	v_mov_b32_e32 v6, v29
	v_mov_b32_e32 v7, v29
	global_load_dword v2, v2, s[16:17]
	v_readlane_b32 s16, v254, 35
	v_readlane_b32 s17, v254, 36
	v_mov_b32_e32 v8, v29
	v_mov_b32_e32 v9, v29
	v_mov_b32_e32 v10, v29
	v_mov_b32_e32 v11, v29
	v_mov_b32_e32 v12, v29
	global_load_dword v3, v3, s[16:17]
	v_readlane_b32 s16, v254, 37
	v_readlane_b32 s17, v254, 38
	v_mov_b32_e32 v13, v29
	v_mov_b32_e32 v14, v29
	v_mov_b32_e32 v15, v29
	v_mov_b32_e32 v16, v29
	v_mov_b32_e32 v17, v29
	global_load_dword v4, v4, s[16:17]
	v_readlane_b32 s16, v254, 39
	v_readlane_b32 s17, v254, 40
	v_mov_b32_e32 v18, v29
	v_mov_b32_e32 v19, v29
	v_mov_b32_e32 v20, v29
	v_mov_b32_e32 v21, v29
	v_mov_b32_e32 v22, v29
	global_load_dword v5, v5, s[16:17]
	v_readlane_b32 s16, v254, 41
	v_readlane_b32 s17, v254, 42
	v_mov_b32_e32 v23, v29
	v_mov_b32_e32 v152, v29
	v_mov_b32_e32 v154, v29
	v_mov_b32_e32 v155, v29
	v_mov_b32_e32 v156, v29
	global_load_dword v6, v6, s[16:17]
	v_readlane_b32 s16, v254, 43
	v_readlane_b32 s17, v254, 44
	v_mov_b32_e32 v157, v29
	v_mov_b32_e32 v158, v29
	v_mov_b32_e32 v159, v29
	s_add_i32 s19, s15, -16
	s_nop 0
	global_load_dword v7, v7, s[16:17]
	v_readlane_b32 s16, v254, 45
	v_readlane_b32 s17, v254, 46
	s_nop 4
	global_load_dword v8, v8, s[16:17]
	v_readlane_b32 s16, v254, 47
	v_readlane_b32 s17, v254, 48
	s_nop 4
	global_load_dword v9, v9, s[16:17]
	v_readlane_b32 s16, v254, 49
	v_readlane_b32 s17, v254, 50
	s_nop 4
	global_load_dword v10, v10, s[16:17]
; __device__ __forceinline__ void phase_even_mix(CArgs a, LAS unsigned char* lds, int i2, int wv, int xw  ) {
;     ...
;             for (int k = 0; k < 31; ++k) { unsigned off = (unsigned)c * 4u; asm volatile("" : "+v"(off)); w[k] = *(const float*)((const char*)(cw + k * 512) + off); }
;             const float cb = a->in[I_CONVB][i2 * 512 + c];
;             float win[34];
; #pragma clang loop unroll(full)
;             for (int r = 0; r < 64; ++r) {
;                 win[r % 34] = bf2f(glu[r * 512 + c]);
;                 if (r >= 32) { float y = cb;
; #pragma unroll
;                     for (int k = 0; k < 31; ++k) y += w[k] * win[(r - 30 + k) % 34];
;                     ybuf[(r - 32) * 512 + c] = y; }
	v_readlane_b32 s16, v254, 51
	v_readlane_b32 s17, v254, 52
	s_nop 4
	global_load_dword v11, v11, s[16:17]
	v_readlane_b32 s16, v254, 53
	v_readlane_b32 s17, v254, 54
	s_nop 4
	global_load_dword v12, v12, s[16:17]
	v_readlane_b32 s16, v254, 55
	v_readlane_b32 s17, v254, 56
	s_nop 4
	global_load_dword v13, v13, s[16:17]
	v_readlane_b32 s16, v254, 57
	v_readlane_b32 s17, v254, 58
	s_nop 4
	global_load_dword v14, v14, s[16:17]
	v_readlane_b32 s16, v254, 59
	v_readlane_b32 s17, v254, 60
	s_nop 4
	global_load_dword v15, v15, s[16:17]
	v_readlane_b32 s16, v254, 61
	v_readlane_b32 s17, v254, 62
	s_nop 4
	global_load_dword v16, v16, s[16:17]
	v_readlane_b32 s16, v254, 63
	v_readlane_b32 s17, v255, 0
	s_nop 4
	global_load_dword v17, v17, s[16:17]
	v_readlane_b32 s16, v255, 1
	v_readlane_b32 s17, v255, 2
	s_nop 4
	global_load_dword v18, v18, s[16:17]
	global_load_dword v19, v19, s[40:41]
	global_load_dword v20, v20, s[84:85]
	global_load_dword v21, v21, s[26:27]
	global_load_dword v22, v22, s[20:21]
	global_load_dword v23, v23, s[4:5]
	global_load_dword v152, v152, s[2:3]
	global_load_dword v154, v154, s[24:25]
	global_load_dword v155, v155, s[30:31]
	global_load_dword v156, v156, s[0:1]
	global_load_dword v157, v157, s[72:73]
	global_load_dword v158, v158, s[74:75]
	s_load_dwordx2 s[16:17], s[88:89], 0x38
	ds_read_u16 v162, v35 offset:3072
	ds_read_u16 v163, v35 offset:4096
	ds_read_u16 v164, v35 offset:5120
	ds_read_u16 v165, v35 offset:6144
	ds_read_u16 v166, v35 offset:7168
	s_waitcnt lgkmcnt(0)
	v_lshl_add_u64 v[160:161], v[26:27], 2, s[16:17]
	global_load_dword v160, v[160:161], off
	ds_read_u16 v161, v35 offset:2048
	global_load_dword v159, v159, s[76:77]
	v_lshlrev_b32_e32 v167, 16, v166
	ds_read_u16 v166, v35 offset:8192
	v_lshlrev_b32_e32 v162, 16, v162
	v_lshlrev_b32_e32 v163, 16, v163
	v_lshlrev_b32_e32 v164, 16, v164
	v_lshlrev_b32_e32 v165, 16, v165
	s_waitcnt lgkmcnt(0)
	v_lshlrev_b32_e32 v174, 16, v166
	ds_read_u16 v166, v35 offset:9216
	s_waitcnt lgkmcnt(0)
	v_lshlrev_b32_e32 v176, 16, v166
	ds_read_u16 v166, v35 offset:10240
	s_waitcnt lgkmcnt(0)
	v_lshlrev_b32_e32 v177, 16, v166
	ds_read_u16 v166, v35 offset:11264
	s_waitcnt lgkmcnt(0)
	v_lshlrev_b32_e32 v192, 16, v166
	ds_read_u16 v166, v35 offset:12288
	s_waitcnt lgkmcnt(0)
	v_lshlrev_b32_e32 v193, 16, v166
	ds_read_u16 v166, v35 offset:13312
	s_waitcnt lgkmcnt(0)
	v_lshlrev_b32_e32 v194, 16, v166
	ds_read_u16 v166, v35 offset:14336
	s_waitcnt lgkmcnt(0)
	v_lshlrev_b32_e32 v196, 16, v166
	ds_read_u16 v166, v35 offset:15360
	s_waitcnt lgkmcnt(0)
	v_lshlrev_b32_e32 v198, 16, v166
	ds_read_u16 v166, v35 offset:16384
	s_waitcnt lgkmcnt(0)
	v_lshlrev_b32_e32 v205, 16, v166
	ds_read_u16 v166, v35 offset:17408
	s_waitcnt lgkmcnt(0)
	v_lshlrev_b32_e32 v204, 16, v166
	ds_read_u16 v166, v35 offset:18432
	s_waitcnt lgkmcnt(0)
	v_lshlrev_b32_e32 v203, 16, v166
	ds_read_u16 v166, v35 offset:19456
	s_waitcnt lgkmcnt(0)
	v_lshlrev_b32_e32 v202, 16, v166
	ds_read_u16 v166, v35 offset:20480
	s_waitcnt vmcnt(1)
	v_fma_f32 v178, v0, v192, v160
	s_waitcnt lgkmcnt(0)
	v_lshlrev_b32_e32 v201, 16, v166
	ds_read_u16 v166, v35 offset:21504
	v_fmac_f32_e32 v178, v1, v193
	v_fmac_f32_e32 v178, v2, v194
	v_fmac_f32_e32 v178, v3, v196
	v_fmac_f32_e32 v178, v4, v198
	s_waitcnt lgkmcnt(0)
	v_lshlrev_b32_e32 v200, 16, v166
	ds_read_u16 v166, v35 offset:22528
	v_fmac_f32_e32 v178, v5, v205
	v_fmac_f32_e32 v178, v6, v204
	v_fmac_f32_e32 v178, v7, v203
	v_fmac_f32_e32 v178, v8, v202
	s_waitcnt lgkmcnt(0)
	v_lshlrev_b32_e32 v199, 16, v166
	ds_read_u16 v166, v35 offset:23552
	v_fmac_f32_e32 v178, v9, v201
	v_fmac_f32_e32 v178, v10, v200
	v_fmac_f32_e32 v178, v11, v199
	s_waitcnt lgkmcnt(0)
	v_lshlrev_b32_e32 v197, 16, v166
	ds_read_u16 v166, v35 offset:24576
	v_fmac_f32_e32 v178, v12, v197
	s_waitcnt lgkmcnt(0)
	v_lshlrev_b32_e32 v195, 16, v166
	ds_read_u16 v166, v35 offset:25600
	v_fmac_f32_e32 v178, v13, v195
	s_waitcnt lgkmcnt(0)
	v_lshlrev_b32_e32 v175, 16, v166
	ds_read_u16 v166, v35 offset:26624
	v_fmac_f32_e32 v178, v14, v175
	s_waitcnt lgkmcnt(0)
	v_lshlrev_b32_e32 v173, 16, v166
	ds_read_u16 v166, v35 offset:27648
	v_fmac_f32_e32 v178, v15, v173
	s_waitcnt lgkmcnt(0)
	v_lshlrev_b32_e32 v172, 16, v166
	ds_read_u16 v166, v35 offset:28672
	v_fmac_f32_e32 v178, v16, v172
	s_waitcnt lgkmcnt(0)
	v_lshlrev_b32_e32 v171, 16, v166
	ds_read_u16 v166, v35 offset:29696
	v_fmac_f32_e32 v178, v17, v171
	s_waitcnt lgkmcnt(0)
	v_lshlrev_b32_e32 v170, 16, v166
	ds_read_u16 v166, v35 offset:30720
	v_fmac_f32_e32 v178, v18, v170
	s_waitcnt lgkmcnt(0)
	v_lshlrev_b32_e32 v169, 16, v166
	ds_read_u16 v166, v35 offset:31744
	v_fmac_f32_e32 v178, v19, v169
	s_waitcnt lgkmcnt(0)
; __device__ __forceinline__ void phase_even_mix(CArgs a, LAS unsigned char* lds, int i2, int wv, int xw  ) {
;     ...
; #pragma clang loop unroll(full)
;             for (int r = 0; r < 64; ++r) {
;                 win[r % 34] = bf2f(glu[r * 512 + c]);
;                 if (r >= 32) { float y = cb;
; #pragma unroll
;                     for (int k = 0; k < 31; ++k) y += w[k] * win[(r - 30 + k) % 34];
;                     ybuf[(r - 32) * 512 + c] = y; }
;             }
	v_lshlrev_b32_e32 v168, 16, v166
	ds_read_u16 v166, v35 offset:32768
	v_lshlrev_b32_e32 v161, 16, v161
	v_fma_f32 v161, v0, v161, v160
	v_fmac_f32_e32 v161, v1, v162
	v_fmac_f32_e32 v161, v2, v163
	v_fmac_f32_e32 v161, v3, v164
	v_fmac_f32_e32 v161, v4, v165
	v_fmac_f32_e32 v161, v5, v167
	v_fmac_f32_e32 v161, v6, v174
	v_fmac_f32_e32 v161, v7, v176
	v_fma_f32 v162, v0, v162, v160
	v_fmac_f32_e32 v161, v8, v177
	v_fmac_f32_e32 v162, v1, v163
	v_fmac_f32_e32 v161, v9, v192
	v_fmac_f32_e32 v162, v2, v164
	v_fmac_f32_e32 v161, v10, v193
	v_fmac_f32_e32 v162, v3, v165
	v_fmac_f32_e32 v161, v11, v194
	v_fmac_f32_e32 v162, v4, v167
	v_fmac_f32_e32 v161, v12, v196
	v_fmac_f32_e32 v162, v5, v174
	v_fmac_f32_e32 v161, v13, v198
	v_fmac_f32_e32 v162, v6, v176
	v_fmac_f32_e32 v161, v14, v205
	v_fmac_f32_e32 v162, v7, v177
	v_fma_f32 v163, v0, v163, v160
	v_fmac_f32_e32 v161, v15, v204
	v_fmac_f32_e32 v162, v8, v192
	v_fmac_f32_e32 v163, v1, v164
	v_fmac_f32_e32 v161, v16, v203
	v_fmac_f32_e32 v162, v9, v193
	v_fmac_f32_e32 v163, v2, v165
	v_fmac_f32_e32 v161, v17, v202
	v_fmac_f32_e32 v162, v10, v194
	v_fmac_f32_e32 v163, v3, v167
	v_fmac_f32_e32 v161, v18, v201
	v_fmac_f32_e32 v162, v11, v196
	v_fmac_f32_e32 v163, v4, v174
	v_fmac_f32_e32 v161, v19, v200
	v_fmac_f32_e32 v162, v12, v198
	v_fmac_f32_e32 v163, v5, v176
	v_fmac_f32_e32 v161, v20, v199
	v_fmac_f32_e32 v162, v13, v205
	v_fmac_f32_e32 v163, v6, v177
	v_fmac_f32_e32 v161, v21, v197
	v_fmac_f32_e32 v162, v14, v204
	v_fmac_f32_e32 v163, v7, v192
	v_fma_f32 v164, v0, v164, v160
	v_fmac_f32_e32 v161, v22, v195
	v_fmac_f32_e32 v162, v15, v203
	v_fmac_f32_e32 v163, v8, v193
	v_fmac_f32_e32 v164, v1, v165
	v_fmac_f32_e32 v161, v23, v175
	v_fmac_f32_e32 v162, v16, v202
	v_fmac_f32_e32 v163, v9, v194
	v_fmac_f32_e32 v164, v2, v167
	v_fmac_f32_e32 v161, v152, v173
	v_fmac_f32_e32 v162, v17, v201
	v_fmac_f32_e32 v163, v10, v196
	v_fmac_f32_e32 v164, v3, v174
	v_fmac_f32_e32 v161, v154, v172
	v_fmac_f32_e32 v162, v18, v200
	v_fmac_f32_e32 v163, v11, v198
	v_fmac_f32_e32 v164, v4, v176
	v_fmac_f32_e32 v161, v155, v171
	v_fmac_f32_e32 v162, v19, v199
	v_fmac_f32_e32 v163, v12, v205
	v_fmac_f32_e32 v164, v5, v177
	v_fmac_f32_e32 v161, v156, v170
	v_fmac_f32_e32 v162, v20, v197
	v_fmac_f32_e32 v163, v13, v204
	v_fmac_f32_e32 v164, v6, v192
	v_fmac_f32_e32 v161, v157, v169
	v_fmac_f32_e32 v162, v21, v195
	v_fmac_f32_e32 v163, v14, v203
	v_fmac_f32_e32 v164, v7, v193
	v_fma_f32 v165, v0, v165, v160
	s_waitcnt lgkmcnt(0)
	v_lshlrev_b32_e32 v166, 16, v166
	v_fmac_f32_e32 v161, v158, v168
	v_fmac_f32_e32 v162, v22, v175
	v_fmac_f32_e32 v163, v15, v202
	v_fmac_f32_e32 v164, v8, v194
	v_fmac_f32_e32 v165, v1, v167
	s_waitcnt vmcnt(0)
	v_fmac_f32_e32 v161, v159, v166
	v_fmac_f32_e32 v162, v23, v173
	v_fmac_f32_e32 v163, v16, v201
	v_fmac_f32_e32 v164, v9, v196
	v_fmac_f32_e32 v165, v2, v174
	ds_write_b32 v78, v161
	ds_read_u16 v161, v35 offset:33792
	v_fmac_f32_e32 v162, v152, v172
	v_fmac_f32_e32 v163, v17, v200
	v_fmac_f32_e32 v164, v10, v198
	v_fmac_f32_e32 v165, v3, v176
	v_fmac_f32_e32 v162, v154, v171
	v_fmac_f32_e32 v163, v18, v199
	v_fmac_f32_e32 v164, v11, v205
	v_fmac_f32_e32 v165, v4, v177
	v_fmac_f32_e32 v162, v155, v170
	v_fmac_f32_e32 v163, v19, v197
	v_fmac_f32_e32 v164, v12, v204
	v_fmac_f32_e32 v165, v5, v192
	v_fmac_f32_e32 v162, v156, v169
	v_fmac_f32_e32 v163, v20, v195
	v_fmac_f32_e32 v164, v13, v203
	v_fmac_f32_e32 v165, v6, v193
	v_fmac_f32_e32 v162, v157, v168
	v_fmac_f32_e32 v163, v21, v175
	v_fmac_f32_e32 v164, v14, v202
	v_fmac_f32_e32 v165, v7, v194
	v_fma_f32 v167, v0, v167, v160
	s_waitcnt lgkmcnt(0)
	v_lshlrev_b32_e32 v161, 16, v161
	v_fmac_f32_e32 v162, v158, v166
	v_fmac_f32_e32 v163, v22, v173
	v_fmac_f32_e32 v164, v15, v201
	v_fmac_f32_e32 v165, v8, v196
	v_fmac_f32_e32 v167, v1, v174
	v_fmac_f32_e32 v162, v159, v161
	v_fmac_f32_e32 v163, v23, v172
	v_fmac_f32_e32 v164, v16, v200
	v_fmac_f32_e32 v165, v9, v198
	v_fmac_f32_e32 v167, v2, v176
	ds_write_b32 v79, v162
	ds_read_u16 v162, v35 offset:34816
	v_fmac_f32_e32 v163, v152, v171
	v_fmac_f32_e32 v164, v17, v199
	v_fmac_f32_e32 v165, v10, v205
	v_fmac_f32_e32 v167, v3, v177
	v_fmac_f32_e32 v163, v154, v170
	v_fmac_f32_e32 v164, v18, v197
	v_fmac_f32_e32 v165, v11, v204
	v_fmac_f32_e32 v167, v4, v192
	v_fmac_f32_e32 v163, v155, v169
	v_fmac_f32_e32 v164, v19, v195
	v_fmac_f32_e32 v165, v12, v203
	v_fmac_f32_e32 v167, v5, v193
	v_fmac_f32_e32 v163, v156, v168
	v_fmac_f32_e32 v164, v20, v175
	v_fmac_f32_e32 v165, v13, v202
	v_fmac_f32_e32 v167, v6, v194
	v_fmac_f32_e32 v163, v157, v166
	v_fmac_f32_e32 v164, v21, v173
	v_fmac_f32_e32 v165, v14, v201
	v_fmac_f32_e32 v167, v7, v196
	v_fma_f32 v174, v0, v174, v160
	s_waitcnt lgkmcnt(0)
	v_lshlrev_b32_e32 v162, 16, v162
	v_fmac_f32_e32 v163, v158, v161
	v_fmac_f32_e32 v164, v22, v172
	v_fmac_f32_e32 v165, v15, v200
	v_fmac_f32_e32 v167, v8, v198
	v_fmac_f32_e32 v174, v1, v176
	v_fmac_f32_e32 v163, v159, v162
	v_fmac_f32_e32 v164, v23, v171
	v_fmac_f32_e32 v165, v16, v199
	v_fmac_f32_e32 v167, v9, v205
	v_fmac_f32_e32 v174, v2, v177
	ds_write_b32 v80, v163
	ds_read_u16 v163, v35 offset:35840
	v_fmac_f32_e32 v164, v152, v170
	v_fmac_f32_e32 v165, v17, v197
	v_fmac_f32_e32 v167, v10, v204
	v_fmac_f32_e32 v174, v3, v192
	v_fmac_f32_e32 v164, v154, v169
	v_fmac_f32_e32 v165, v18, v195
	v_fmac_f32_e32 v167, v11, v203
	v_fmac_f32_e32 v174, v4, v193
	v_fmac_f32_e32 v164, v155, v168
	v_fmac_f32_e32 v165, v19, v175
	v_fmac_f32_e32 v167, v12, v202
	v_fmac_f32_e32 v174, v5, v194
	v_fmac_f32_e32 v164, v156, v166
	v_fmac_f32_e32 v165, v20, v173
	v_fmac_f32_e32 v167, v13, v201
	v_fmac_f32_e32 v174, v6, v196
	v_fmac_f32_e32 v164, v157, v161
	v_fmac_f32_e32 v165, v21, v172
	v_fmac_f32_e32 v167, v14, v200
	v_fmac_f32_e32 v174, v7, v198
	v_fma_f32 v176, v0, v176, v160
	s_waitcnt lgkmcnt(0)
; __device__ __forceinline__ void phase_even_mix(CArgs a, LAS unsigned char* lds, int i2, int wv, int xw  ) {
;     ...
; #pragma clang loop unroll(full)
;             for (int r = 0; r < 64; ++r) {
;                 win[r % 34] = bf2f(glu[r * 512 + c]);
;                 if (r >= 32) { float y = cb;
; #pragma unroll
;                     for (int k = 0; k < 31; ++k) y += w[k] * win[(r - 30 + k) % 34];
;                     ybuf[(r - 32) * 512 + c] = y; }
;             }
	v_lshlrev_b32_e32 v163, 16, v163
	v_fmac_f32_e32 v164, v158, v162
	v_fmac_f32_e32 v165, v22, v171
	v_fmac_f32_e32 v167, v15, v199
	v_fmac_f32_e32 v174, v8, v205
	v_fmac_f32_e32 v176, v1, v177
	v_fmac_f32_e32 v164, v159, v163
	v_fmac_f32_e32 v165, v23, v170
	v_fmac_f32_e32 v167, v16, v197
	v_fmac_f32_e32 v174, v9, v204
	v_fmac_f32_e32 v176, v2, v192
	ds_write_b32 v81, v164
	ds_read_u16 v164, v35 offset:36864
	v_fmac_f32_e32 v165, v152, v169
	v_fmac_f32_e32 v167, v17, v195
	v_fmac_f32_e32 v174, v10, v203
	v_fmac_f32_e32 v176, v3, v193
	v_fmac_f32_e32 v165, v154, v168
	v_fmac_f32_e32 v167, v18, v175
	v_fmac_f32_e32 v174, v11, v202
	v_fmac_f32_e32 v176, v4, v194
	v_fmac_f32_e32 v165, v155, v166
	v_fmac_f32_e32 v167, v19, v173
	v_fmac_f32_e32 v174, v12, v201
	v_fmac_f32_e32 v176, v5, v196
	v_fmac_f32_e32 v165, v156, v161
	v_fmac_f32_e32 v167, v20, v172
	v_fmac_f32_e32 v174, v13, v200
	v_fmac_f32_e32 v176, v6, v198
	v_fmac_f32_e32 v165, v157, v162
	v_fmac_f32_e32 v167, v21, v171
	v_fmac_f32_e32 v174, v14, v199
	v_fmac_f32_e32 v176, v7, v205
	v_fma_f32 v177, v0, v177, v160
	s_waitcnt lgkmcnt(0)
	v_lshlrev_b32_e32 v164, 16, v164
	v_fmac_f32_e32 v165, v158, v163
	v_fmac_f32_e32 v167, v22, v170
	v_fmac_f32_e32 v174, v15, v197
	v_fmac_f32_e32 v176, v8, v204
	v_fmac_f32_e32 v177, v1, v192
	v_fmac_f32_e32 v165, v159, v164
	v_fmac_f32_e32 v167, v23, v169
	v_fmac_f32_e32 v174, v16, v195
	v_fmac_f32_e32 v176, v9, v203
	v_fmac_f32_e32 v177, v2, v193
	ds_write_b32 v82, v165
	ds_read_u16 v165, v35 offset:37888
	v_fmac_f32_e32 v167, v152, v168
	v_fmac_f32_e32 v174, v17, v175
	v_fmac_f32_e32 v176, v10, v202
	v_fmac_f32_e32 v177, v3, v194
	v_fmac_f32_e32 v167, v154, v166
	v_fmac_f32_e32 v174, v18, v173
	v_fmac_f32_e32 v176, v11, v201
	v_fmac_f32_e32 v177, v4, v196
	v_fmac_f32_e32 v167, v155, v161
	v_fmac_f32_e32 v174, v19, v172
	v_fmac_f32_e32 v176, v12, v200
	v_fmac_f32_e32 v177, v5, v198
	v_fmac_f32_e32 v167, v156, v162
	v_fmac_f32_e32 v174, v20, v171
	v_fmac_f32_e32 v176, v13, v199
	v_fmac_f32_e32 v177, v6, v205
	v_fmac_f32_e32 v167, v157, v163
	v_fmac_f32_e32 v174, v21, v170
	v_fmac_f32_e32 v176, v14, v197
	v_fmac_f32_e32 v177, v7, v204
	s_waitcnt lgkmcnt(0)
	v_lshlrev_b32_e32 v165, 16, v165
	v_fmac_f32_e32 v167, v158, v164
	v_fmac_f32_e32 v174, v22, v169
	v_fmac_f32_e32 v176, v15, v195
	v_fmac_f32_e32 v177, v8, v203
	v_fmac_f32_e32 v167, v159, v165
	v_fmac_f32_e32 v174, v23, v168
	v_fmac_f32_e32 v176, v16, v175
	v_fmac_f32_e32 v177, v9, v202
	ds_write_b32 v83, v167
	ds_read_u16 v167, v35 offset:38912
	v_fmac_f32_e32 v174, v152, v166
	v_fmac_f32_e32 v176, v17, v173
	v_fmac_f32_e32 v177, v10, v201
	v_fmac_f32_e32 v174, v154, v161
	v_fmac_f32_e32 v176, v18, v172
	v_fmac_f32_e32 v177, v11, v200
	v_fmac_f32_e32 v174, v155, v162
	v_fmac_f32_e32 v176, v19, v171
	v_fmac_f32_e32 v177, v12, v199
	v_fmac_f32_e32 v174, v156, v163
	v_fmac_f32_e32 v176, v20, v170
	v_fmac_f32_e32 v177, v13, v197
	v_fmac_f32_e32 v174, v157, v164
	v_fmac_f32_e32 v176, v21, v169
	v_fmac_f32_e32 v177, v14, v195
	s_waitcnt lgkmcnt(0)
	v_lshlrev_b32_e32 v167, 16, v167
	v_fmac_f32_e32 v174, v158, v165
	v_fmac_f32_e32 v176, v22, v168
	v_fmac_f32_e32 v177, v15, v175
	v_fmac_f32_e32 v174, v159, v167
	v_fmac_f32_e32 v176, v23, v166
	v_fmac_f32_e32 v177, v16, v173
	ds_write_b32 v84, v174
	ds_read_u16 v174, v35 offset:39936
	v_fmac_f32_e32 v176, v152, v161
	v_fmac_f32_e32 v177, v17, v172
	v_fmac_f32_e32 v176, v154, v162
	v_fmac_f32_e32 v177, v18, v171
	v_fmac_f32_e32 v176, v155, v163
	v_fmac_f32_e32 v177, v19, v170
	v_fmac_f32_e32 v176, v156, v164
	v_fmac_f32_e32 v177, v20, v169
	v_fmac_f32_e32 v176, v157, v165
	v_fmac_f32_e32 v177, v21, v168
	s_waitcnt lgkmcnt(0)
	v_lshlrev_b32_e32 v174, 16, v174
	v_fmac_f32_e32 v176, v158, v167
	v_fmac_f32_e32 v177, v22, v166
	v_fmac_f32_e32 v176, v159, v174
	v_fmac_f32_e32 v177, v23, v161
	ds_write_b32 v85, v176
	ds_read_u16 v176, v35 offset:40960
	v_fmac_f32_e32 v177, v152, v162
	v_fmac_f32_e32 v177, v154, v163
	v_fmac_f32_e32 v177, v155, v164
	v_fmac_f32_e32 v177, v156, v165
	v_fmac_f32_e32 v178, v20, v168
	v_fmac_f32_e32 v177, v157, v167
	v_fmac_f32_e32 v178, v21, v166
	s_waitcnt lgkmcnt(0)
	v_lshlrev_b32_e32 v176, 16, v176
	v_fmac_f32_e32 v177, v158, v174
	v_fmac_f32_e32 v178, v22, v161
	v_fmac_f32_e32 v177, v159, v176
	v_fmac_f32_e32 v178, v23, v162
	ds_write_b32 v86, v177
	ds_read_u16 v177, v35 offset:41984
	v_fmac_f32_e32 v178, v152, v163
	v_fmac_f32_e32 v178, v154, v164
	v_fmac_f32_e32 v178, v155, v165
	v_fmac_f32_e32 v178, v156, v167
	v_fmac_f32_e32 v178, v157, v174
	s_waitcnt lgkmcnt(0)
	v_lshlrev_b32_e32 v177, 16, v177
	v_fmac_f32_e32 v178, v158, v176
	v_fmac_f32_e32 v178, v159, v177
	ds_write_b32 v87, v178
	ds_read_u16 v178, v35 offset:43008
	s_waitcnt lgkmcnt(0)
	v_lshlrev_b32_e32 v192, 16, v178
	v_fma_f32 v178, v0, v193, v160
	v_fmac_f32_e32 v178, v1, v194
	v_fmac_f32_e32 v178, v2, v196
	v_fmac_f32_e32 v178, v3, v198
	v_fmac_f32_e32 v178, v4, v205
	v_fmac_f32_e32 v178, v5, v204
	v_fmac_f32_e32 v178, v6, v203
	v_fmac_f32_e32 v178, v7, v202
	v_fmac_f32_e32 v178, v8, v201
	v_fmac_f32_e32 v178, v9, v200
	v_fmac_f32_e32 v178, v10, v199
	v_fmac_f32_e32 v178, v11, v197
	v_fmac_f32_e32 v178, v12, v195
	v_fmac_f32_e32 v178, v13, v175
	v_fmac_f32_e32 v178, v14, v173
	v_fmac_f32_e32 v178, v15, v172
	v_fmac_f32_e32 v178, v16, v171
	v_fmac_f32_e32 v178, v17, v170
	v_fmac_f32_e32 v178, v18, v169
	v_fmac_f32_e32 v178, v19, v168
	v_fmac_f32_e32 v178, v20, v166
	v_fmac_f32_e32 v178, v21, v161
	v_fmac_f32_e32 v178, v22, v162
	v_fmac_f32_e32 v178, v23, v163
	v_fmac_f32_e32 v178, v152, v164
	v_fmac_f32_e32 v178, v154, v165
	v_fmac_f32_e32 v178, v155, v167
	v_fmac_f32_e32 v178, v156, v174
	v_fmac_f32_e32 v178, v157, v176
	v_fmac_f32_e32 v178, v158, v177
	v_fmac_f32_e32 v178, v159, v192
	ds_write_b32 v88, v178
	ds_read_u16 v178, v35 offset:44032
	s_waitcnt lgkmcnt(0)
; __device__ __forceinline__ void phase_even_mix(CArgs a, LAS unsigned char* lds, int i2, int wv, int xw  ) {
;     ...
; #pragma clang loop unroll(full)
;             for (int r = 0; r < 64; ++r) {
;                 win[r % 34] = bf2f(glu[r * 512 + c]);
;                 if (r >= 32) { float y = cb;
; #pragma unroll
;                     for (int k = 0; k < 31; ++k) y += w[k] * win[(r - 30 + k) % 34];
;                     ybuf[(r - 32) * 512 + c] = y; }
;             }
	v_lshlrev_b32_e32 v193, 16, v178
	v_fma_f32 v178, v0, v194, v160
	v_fmac_f32_e32 v178, v1, v196
	v_fmac_f32_e32 v178, v2, v198
	v_fmac_f32_e32 v178, v3, v205
	v_fmac_f32_e32 v178, v4, v204
	v_fmac_f32_e32 v178, v5, v203
	v_fmac_f32_e32 v178, v6, v202
	v_fmac_f32_e32 v178, v7, v201
	v_fmac_f32_e32 v178, v8, v200
	v_fmac_f32_e32 v178, v9, v199
	v_fmac_f32_e32 v178, v10, v197
	v_fmac_f32_e32 v178, v11, v195
	v_fmac_f32_e32 v178, v12, v175
	v_fmac_f32_e32 v178, v13, v173
	v_fmac_f32_e32 v178, v14, v172
	v_fmac_f32_e32 v178, v15, v171
	v_fmac_f32_e32 v178, v16, v170
	v_fmac_f32_e32 v178, v17, v169
	v_fmac_f32_e32 v178, v18, v168
	v_fmac_f32_e32 v178, v19, v166
	v_fmac_f32_e32 v178, v20, v161
	v_fmac_f32_e32 v178, v21, v162
	v_fmac_f32_e32 v178, v22, v163
	v_fmac_f32_e32 v178, v23, v164
	v_fmac_f32_e32 v178, v152, v165
	v_fmac_f32_e32 v178, v154, v167
	v_fmac_f32_e32 v178, v155, v174
	v_fmac_f32_e32 v178, v156, v176
	v_fmac_f32_e32 v178, v157, v177
	v_fmac_f32_e32 v178, v158, v192
	v_fmac_f32_e32 v178, v159, v193
	ds_write_b32 v89, v178
	ds_read_u16 v178, v35 offset:45056
	s_waitcnt lgkmcnt(0)
	v_lshlrev_b32_e32 v194, 16, v178
	v_fma_f32 v178, v0, v196, v160
	v_fmac_f32_e32 v178, v1, v198
	v_fmac_f32_e32 v178, v2, v205
	v_fmac_f32_e32 v178, v3, v204
	v_fmac_f32_e32 v178, v4, v203
	v_fmac_f32_e32 v178, v5, v202
	v_fmac_f32_e32 v178, v6, v201
	v_fmac_f32_e32 v178, v7, v200
	v_fmac_f32_e32 v178, v8, v199
	v_fmac_f32_e32 v178, v9, v197
	v_fmac_f32_e32 v178, v10, v195
	v_fmac_f32_e32 v178, v11, v175
	v_fmac_f32_e32 v178, v12, v173
	v_fmac_f32_e32 v178, v13, v172
	v_fmac_f32_e32 v178, v14, v171
	v_fmac_f32_e32 v178, v15, v170
	v_fmac_f32_e32 v178, v16, v169
	v_fmac_f32_e32 v178, v17, v168
	v_fmac_f32_e32 v178, v18, v166
	v_fmac_f32_e32 v178, v19, v161
	v_fmac_f32_e32 v178, v20, v162
	v_fmac_f32_e32 v178, v21, v163
	v_fmac_f32_e32 v178, v22, v164
	v_fmac_f32_e32 v178, v23, v165
	v_fmac_f32_e32 v178, v152, v167
	v_fmac_f32_e32 v178, v154, v174
	v_fmac_f32_e32 v178, v155, v176
	v_fmac_f32_e32 v178, v156, v177
	v_fmac_f32_e32 v178, v157, v192
	v_fmac_f32_e32 v178, v158, v193
	v_fmac_f32_e32 v178, v159, v194
	ds_write_b32 v90, v178
	ds_read_u16 v178, v35 offset:46080
	s_waitcnt lgkmcnt(0)
	v_lshlrev_b32_e32 v196, 16, v178
	v_fma_f32 v178, v0, v198, v160
	v_fmac_f32_e32 v178, v1, v205
	v_fmac_f32_e32 v178, v2, v204
	v_fmac_f32_e32 v178, v3, v203
	v_fmac_f32_e32 v178, v4, v202
	v_fmac_f32_e32 v178, v5, v201
	v_fmac_f32_e32 v178, v6, v200
	v_fmac_f32_e32 v178, v7, v199
	v_fmac_f32_e32 v178, v8, v197
	v_fmac_f32_e32 v178, v9, v195
	v_fmac_f32_e32 v178, v10, v175
	v_fmac_f32_e32 v178, v11, v173
	v_fmac_f32_e32 v178, v12, v172
	v_fmac_f32_e32 v178, v13, v171
	v_fmac_f32_e32 v178, v14, v170
	v_fmac_f32_e32 v178, v15, v169
	v_fmac_f32_e32 v178, v16, v168
	v_fmac_f32_e32 v178, v17, v166
	v_fmac_f32_e32 v178, v18, v161
	v_fmac_f32_e32 v178, v19, v162
	v_fmac_f32_e32 v178, v20, v163
	v_fmac_f32_e32 v178, v21, v164
	v_fmac_f32_e32 v178, v22, v165
	v_fmac_f32_e32 v178, v23, v167
	v_fmac_f32_e32 v178, v152, v174
	v_fmac_f32_e32 v178, v154, v176
	v_fmac_f32_e32 v178, v155, v177
	v_fmac_f32_e32 v178, v156, v192
	v_fmac_f32_e32 v178, v157, v193
	v_fmac_f32_e32 v178, v158, v194
	v_fmac_f32_e32 v178, v159, v196
	ds_write_b32 v91, v178
	ds_read_u16 v178, v35 offset:47104
	s_waitcnt lgkmcnt(0)
	v_lshlrev_b32_e32 v198, 16, v178
	v_fma_f32 v178, v0, v205, v160
	v_fmac_f32_e32 v178, v1, v204
	v_fmac_f32_e32 v178, v2, v203
	v_fmac_f32_e32 v178, v3, v202
	v_fmac_f32_e32 v178, v4, v201
	v_fmac_f32_e32 v178, v5, v200
	v_fmac_f32_e32 v178, v6, v199
	v_fmac_f32_e32 v178, v7, v197
	v_fmac_f32_e32 v178, v8, v195
	v_fmac_f32_e32 v178, v9, v175
	v_fmac_f32_e32 v178, v10, v173
	v_fmac_f32_e32 v178, v11, v172
	v_fmac_f32_e32 v178, v12, v171
	v_fmac_f32_e32 v178, v13, v170
	v_fmac_f32_e32 v178, v14, v169
	v_fmac_f32_e32 v178, v15, v168
	v_fmac_f32_e32 v178, v16, v166
	v_fmac_f32_e32 v178, v17, v161
	v_fmac_f32_e32 v178, v18, v162
	v_fmac_f32_e32 v178, v19, v163
	v_fmac_f32_e32 v178, v20, v164
	v_fmac_f32_e32 v178, v21, v165
	v_fmac_f32_e32 v178, v22, v167
	v_fmac_f32_e32 v178, v23, v174
	v_fmac_f32_e32 v178, v152, v176
	v_fmac_f32_e32 v178, v154, v177
	v_fmac_f32_e32 v178, v155, v192
	v_fmac_f32_e32 v178, v156, v193
	v_fmac_f32_e32 v178, v157, v194
	v_fmac_f32_e32 v178, v158, v196
	v_fmac_f32_e32 v178, v159, v198
	ds_write_b32 v92, v178
	v_fma_f32 v178, v0, v204, v160
	v_fmac_f32_e32 v178, v1, v203
	v_fmac_f32_e32 v178, v2, v202
	v_fmac_f32_e32 v178, v3, v201
	v_fmac_f32_e32 v178, v4, v200
	v_fmac_f32_e32 v178, v5, v199
	v_fmac_f32_e32 v178, v6, v197
	v_fmac_f32_e32 v178, v7, v195
	v_fmac_f32_e32 v178, v8, v175
	v_fmac_f32_e32 v178, v9, v173
	v_fmac_f32_e32 v178, v10, v172
	v_fmac_f32_e32 v178, v11, v171
	v_fmac_f32_e32 v178, v12, v170
	v_fmac_f32_e32 v178, v13, v169
	v_fmac_f32_e32 v178, v14, v168
	v_fmac_f32_e32 v178, v15, v166
	v_fmac_f32_e32 v178, v16, v161
	v_fmac_f32_e32 v178, v17, v162
	v_fmac_f32_e32 v178, v18, v163
	v_fmac_f32_e32 v178, v19, v164
	v_fmac_f32_e32 v178, v20, v165
	v_fmac_f32_e32 v178, v21, v167
	v_fmac_f32_e32 v178, v22, v174
	v_fmac_f32_e32 v178, v23, v176
	ds_read_u16 v205, v35 offset:48128
	v_fmac_f32_e32 v178, v152, v177
	v_fmac_f32_e32 v178, v154, v192
	v_fmac_f32_e32 v178, v155, v193
	v_fmac_f32_e32 v178, v156, v194
	v_fmac_f32_e32 v178, v157, v196
	s_waitcnt lgkmcnt(0)
	v_lshlrev_b32_e32 v205, 16, v205
	v_fmac_f32_e32 v178, v158, v198
	v_fmac_f32_e32 v178, v159, v205
	ds_write_b32 v93, v178
	ds_read_u16 v178, v35 offset:49152
	s_waitcnt lgkmcnt(0)
; __device__ __forceinline__ void phase_even_mix(CArgs a, LAS unsigned char* lds, int i2, int wv, int xw  ) {
;     ...
; #pragma clang loop unroll(full)
;             for (int r = 0; r < 64; ++r) {
;                 win[r % 34] = bf2f(glu[r * 512 + c]);
;                 if (r >= 32) { float y = cb;
; #pragma unroll
;                     for (int k = 0; k < 31; ++k) y += w[k] * win[(r - 30 + k) % 34];
;                     ybuf[(r - 32) * 512 + c] = y; }
;             }
	v_lshlrev_b32_e32 v204, 16, v178
	v_fma_f32 v178, v0, v203, v160
	v_fmac_f32_e32 v178, v1, v202
	v_fmac_f32_e32 v178, v2, v201
	v_fmac_f32_e32 v178, v3, v200
	v_fmac_f32_e32 v178, v4, v199
	v_fmac_f32_e32 v178, v5, v197
	v_fmac_f32_e32 v178, v6, v195
	v_fmac_f32_e32 v178, v7, v175
	v_fmac_f32_e32 v178, v8, v173
	v_fmac_f32_e32 v178, v9, v172
	v_fmac_f32_e32 v178, v10, v171
	v_fmac_f32_e32 v178, v11, v170
	v_fmac_f32_e32 v178, v12, v169
	v_fmac_f32_e32 v178, v13, v168
	v_fmac_f32_e32 v178, v14, v166
	v_fmac_f32_e32 v178, v15, v161
	v_fmac_f32_e32 v178, v16, v162
	v_fmac_f32_e32 v178, v17, v163
	v_fmac_f32_e32 v178, v18, v164
	v_fmac_f32_e32 v178, v19, v165
	v_fmac_f32_e32 v178, v20, v167
	v_fmac_f32_e32 v178, v21, v174
	v_fmac_f32_e32 v178, v22, v176
	v_fmac_f32_e32 v178, v23, v177
	v_fmac_f32_e32 v178, v152, v192
	v_fmac_f32_e32 v178, v154, v193
	v_fmac_f32_e32 v178, v155, v194
	v_fmac_f32_e32 v178, v156, v196
	v_fmac_f32_e32 v178, v157, v198
	v_fmac_f32_e32 v178, v158, v205
	v_fmac_f32_e32 v178, v159, v204
	ds_write_b32 v94, v178
	ds_read_u16 v178, v35 offset:50176
	s_waitcnt lgkmcnt(0)
	v_lshlrev_b32_e32 v203, 16, v178
	v_fma_f32 v178, v0, v202, v160
	v_fmac_f32_e32 v178, v1, v201
	v_fmac_f32_e32 v178, v2, v200
	v_fmac_f32_e32 v178, v3, v199
	v_fmac_f32_e32 v178, v4, v197
	v_fmac_f32_e32 v178, v5, v195
	v_fmac_f32_e32 v178, v6, v175
	v_fmac_f32_e32 v178, v7, v173
	v_fmac_f32_e32 v178, v8, v172
	v_fmac_f32_e32 v178, v9, v171
	v_fmac_f32_e32 v178, v10, v170
	v_fmac_f32_e32 v178, v11, v169
	v_fmac_f32_e32 v178, v12, v168
	v_fmac_f32_e32 v178, v13, v166
	v_fmac_f32_e32 v178, v14, v161
	v_fmac_f32_e32 v178, v15, v162
	v_fmac_f32_e32 v178, v16, v163
	v_fmac_f32_e32 v178, v17, v164
	v_fmac_f32_e32 v178, v18, v165
	v_fmac_f32_e32 v178, v19, v167
	v_fmac_f32_e32 v178, v20, v174
	v_fmac_f32_e32 v178, v21, v176
	v_fmac_f32_e32 v178, v22, v177
	v_fmac_f32_e32 v178, v23, v192
	v_fmac_f32_e32 v178, v152, v193
	v_fmac_f32_e32 v178, v154, v194
	v_fmac_f32_e32 v178, v155, v196
	v_fmac_f32_e32 v178, v156, v198
	v_fmac_f32_e32 v178, v157, v205
	v_fmac_f32_e32 v178, v158, v204
	v_fmac_f32_e32 v178, v159, v203
	ds_write_b32 v95, v178
	ds_read_u16 v178, v35 offset:51200
	s_waitcnt lgkmcnt(0)
	v_lshlrev_b32_e32 v202, 16, v178
	v_fma_f32 v178, v0, v201, v160
	v_fmac_f32_e32 v178, v1, v200
	v_fmac_f32_e32 v178, v2, v199
	v_fmac_f32_e32 v178, v3, v197
	v_fmac_f32_e32 v178, v4, v195
	v_fmac_f32_e32 v178, v5, v175
	v_fmac_f32_e32 v178, v6, v173
	v_fmac_f32_e32 v178, v7, v172
	v_fmac_f32_e32 v178, v8, v171
	v_fmac_f32_e32 v178, v9, v170
	v_fmac_f32_e32 v178, v10, v169
	v_fmac_f32_e32 v178, v11, v168
	v_fmac_f32_e32 v178, v12, v166
	v_fmac_f32_e32 v178, v13, v161
	v_fmac_f32_e32 v178, v14, v162
	v_fmac_f32_e32 v178, v15, v163
	v_fmac_f32_e32 v178, v16, v164
	v_fmac_f32_e32 v178, v17, v165
	v_fmac_f32_e32 v178, v18, v167
	v_fmac_f32_e32 v178, v19, v174
	v_fmac_f32_e32 v178, v20, v176
	v_fmac_f32_e32 v178, v21, v177
	v_fmac_f32_e32 v178, v22, v192
	v_fmac_f32_e32 v178, v23, v193
	v_fmac_f32_e32 v178, v152, v194
	v_fmac_f32_e32 v178, v154, v196
	v_fmac_f32_e32 v178, v155, v198
	v_fmac_f32_e32 v178, v156, v205
	v_fmac_f32_e32 v178, v157, v204
	v_fmac_f32_e32 v178, v158, v203
	v_fmac_f32_e32 v178, v159, v202
	ds_write_b32 v96, v178
	ds_read_u16 v178, v35 offset:52224
	s_waitcnt lgkmcnt(0)
	v_lshlrev_b32_e32 v201, 16, v178
	v_fma_f32 v178, v0, v200, v160
	v_fmac_f32_e32 v178, v1, v199
	v_fmac_f32_e32 v178, v2, v197
	v_fmac_f32_e32 v178, v3, v195
	v_fmac_f32_e32 v178, v4, v175
	v_fmac_f32_e32 v178, v5, v173
	v_fmac_f32_e32 v178, v6, v172
	v_fmac_f32_e32 v178, v7, v171
	v_fmac_f32_e32 v178, v8, v170
	v_fmac_f32_e32 v178, v9, v169
	v_fmac_f32_e32 v178, v10, v168
	v_fmac_f32_e32 v178, v11, v166
	v_fmac_f32_e32 v178, v12, v161
	v_fmac_f32_e32 v178, v13, v162
	v_fmac_f32_e32 v178, v14, v163
	v_fmac_f32_e32 v178, v15, v164
	v_fmac_f32_e32 v178, v16, v165
	v_fmac_f32_e32 v178, v17, v167
	v_fmac_f32_e32 v178, v18, v174
	v_fmac_f32_e32 v178, v19, v176
	v_fmac_f32_e32 v178, v20, v177
	v_fmac_f32_e32 v178, v21, v192
	v_fmac_f32_e32 v178, v22, v193
	v_fmac_f32_e32 v178, v23, v194
	v_fmac_f32_e32 v178, v152, v196
	v_fmac_f32_e32 v178, v154, v198
	v_fmac_f32_e32 v178, v155, v205
	v_fmac_f32_e32 v178, v156, v204
	v_fmac_f32_e32 v178, v157, v203
	v_fmac_f32_e32 v178, v158, v202
	v_fmac_f32_e32 v178, v159, v201
	ds_write_b32 v97, v178
	ds_read_u16 v178, v35 offset:53248
	s_waitcnt lgkmcnt(0)
	v_lshlrev_b32_e32 v200, 16, v178
	v_fma_f32 v178, v0, v199, v160
	v_fmac_f32_e32 v178, v1, v197
	v_fmac_f32_e32 v178, v2, v195
	v_fmac_f32_e32 v178, v3, v175
	v_fmac_f32_e32 v178, v4, v173
	v_fmac_f32_e32 v178, v5, v172
	v_fmac_f32_e32 v178, v6, v171
	v_fmac_f32_e32 v178, v7, v170
	v_fmac_f32_e32 v178, v8, v169
	v_fmac_f32_e32 v178, v9, v168
	v_fmac_f32_e32 v178, v10, v166
	v_fmac_f32_e32 v178, v11, v161
	v_fmac_f32_e32 v178, v12, v162
	v_fmac_f32_e32 v178, v13, v163
	v_fmac_f32_e32 v178, v14, v164
	v_fmac_f32_e32 v178, v15, v165
	v_fmac_f32_e32 v178, v16, v167
	v_fmac_f32_e32 v178, v17, v174
	v_fmac_f32_e32 v178, v18, v176
	v_fmac_f32_e32 v178, v19, v177
	v_fmac_f32_e32 v178, v20, v192
	v_fmac_f32_e32 v178, v21, v193
	v_fmac_f32_e32 v178, v22, v194
	v_fmac_f32_e32 v178, v23, v196
	v_fmac_f32_e32 v178, v152, v198
	v_fmac_f32_e32 v178, v154, v205
	v_fmac_f32_e32 v178, v155, v204
	v_fmac_f32_e32 v178, v156, v203
	v_fmac_f32_e32 v178, v157, v202
	v_fmac_f32_e32 v178, v158, v201
	v_fmac_f32_e32 v178, v159, v200
	ds_write_b32 v98, v178
	ds_read_u16 v178, v35 offset:54272
	s_waitcnt lgkmcnt(0)
; __device__ __forceinline__ void phase_even_mix(CArgs a, LAS unsigned char* lds, int i2, int wv, int xw  ) {
;     ...
; #pragma clang loop unroll(full)
;             for (int r = 0; r < 64; ++r) {
;                 win[r % 34] = bf2f(glu[r * 512 + c]);
;                 if (r >= 32) { float y = cb;
; #pragma unroll
;                     for (int k = 0; k < 31; ++k) y += w[k] * win[(r - 30 + k) % 34];
;                     ybuf[(r - 32) * 512 + c] = y; }
;             }
	v_lshlrev_b32_e32 v199, 16, v178
	v_fma_f32 v178, v0, v197, v160
	v_fmac_f32_e32 v178, v1, v195
	v_fmac_f32_e32 v178, v2, v175
	v_fmac_f32_e32 v178, v3, v173
	v_fmac_f32_e32 v178, v4, v172
	v_fmac_f32_e32 v178, v5, v171
	v_fmac_f32_e32 v178, v6, v170
	v_fmac_f32_e32 v178, v7, v169
	v_fmac_f32_e32 v178, v8, v168
	v_fmac_f32_e32 v178, v9, v166
	v_fmac_f32_e32 v178, v10, v161
	v_fmac_f32_e32 v178, v11, v162
	v_fmac_f32_e32 v178, v12, v163
	v_fmac_f32_e32 v178, v13, v164
	v_fmac_f32_e32 v178, v14, v165
	v_fmac_f32_e32 v178, v15, v167
	v_fmac_f32_e32 v178, v16, v174
	v_fmac_f32_e32 v178, v17, v176
	v_fmac_f32_e32 v178, v18, v177
	v_fmac_f32_e32 v178, v19, v192
	v_fmac_f32_e32 v178, v20, v193
	v_fmac_f32_e32 v178, v21, v194
	v_fmac_f32_e32 v178, v22, v196
	v_fmac_f32_e32 v178, v23, v198
	v_fmac_f32_e32 v178, v152, v205
	v_fmac_f32_e32 v178, v154, v204
	v_fmac_f32_e32 v178, v155, v203
	v_fmac_f32_e32 v178, v156, v202
	v_fmac_f32_e32 v178, v157, v201
	v_fmac_f32_e32 v178, v158, v200
	v_fmac_f32_e32 v178, v159, v199
	ds_write_b32 v99, v178
	ds_read_u16 v178, v35 offset:55296
	s_waitcnt lgkmcnt(0)
	v_lshlrev_b32_e32 v197, 16, v178
	v_fma_f32 v178, v0, v195, v160
	v_fmac_f32_e32 v178, v1, v175
	v_fma_f32 v175, v0, v175, v160
	v_fmac_f32_e32 v175, v1, v173
	v_fmac_f32_e32 v175, v2, v172
	v_fmac_f32_e32 v175, v3, v171
	v_fmac_f32_e32 v175, v4, v170
	v_fmac_f32_e32 v175, v5, v169
	v_fmac_f32_e32 v175, v6, v168
	v_fmac_f32_e32 v178, v2, v173
	v_fmac_f32_e32 v175, v7, v166
	v_fma_f32 v173, v0, v173, v160
	v_fmac_f32_e32 v175, v8, v161
	v_fmac_f32_e32 v173, v1, v172
	v_fmac_f32_e32 v175, v9, v162
	v_fmac_f32_e32 v173, v2, v171
	v_fmac_f32_e32 v175, v10, v163
	v_fmac_f32_e32 v173, v3, v170
	v_fmac_f32_e32 v175, v11, v164
	v_fmac_f32_e32 v173, v4, v169
	v_fmac_f32_e32 v175, v12, v165
	v_fmac_f32_e32 v173, v5, v168
	v_fmac_f32_e32 v175, v13, v167
	v_fmac_f32_e32 v173, v6, v166
	v_fmac_f32_e32 v178, v3, v172
	v_fmac_f32_e32 v175, v14, v174
	v_fmac_f32_e32 v173, v7, v161
	v_fma_f32 v172, v0, v172, v160
	v_fmac_f32_e32 v175, v15, v176
	v_fmac_f32_e32 v173, v8, v162
	v_fmac_f32_e32 v172, v1, v171
	v_fmac_f32_e32 v175, v16, v177
	v_fmac_f32_e32 v173, v9, v163
	v_fmac_f32_e32 v172, v2, v170
	v_fmac_f32_e32 v175, v17, v192
	v_fmac_f32_e32 v173, v10, v164
	v_fmac_f32_e32 v172, v3, v169
	v_fmac_f32_e32 v175, v18, v193
	v_fmac_f32_e32 v173, v11, v165
	v_fmac_f32_e32 v172, v4, v168
	v_fmac_f32_e32 v175, v19, v194
	v_fmac_f32_e32 v173, v12, v167
	v_fmac_f32_e32 v172, v5, v166
	v_fmac_f32_e32 v175, v20, v196
	v_fmac_f32_e32 v173, v13, v174
	v_fmac_f32_e32 v172, v6, v161
	v_fmac_f32_e32 v178, v4, v171
	v_fmac_f32_e32 v175, v21, v198
	v_fmac_f32_e32 v173, v14, v176
	v_fmac_f32_e32 v172, v7, v162
	v_fma_f32 v171, v0, v171, v160
	v_fmac_f32_e32 v175, v22, v205
	v_fmac_f32_e32 v173, v15, v177
	v_fmac_f32_e32 v172, v8, v163
	v_fmac_f32_e32 v171, v1, v170
	v_fmac_f32_e32 v175, v23, v204
	v_fmac_f32_e32 v173, v16, v192
	v_fmac_f32_e32 v172, v9, v164
	v_fmac_f32_e32 v171, v2, v169
	ds_read_u16 v195, v35 offset:56320
	v_fmac_f32_e32 v175, v152, v203
	v_fmac_f32_e32 v173, v17, v193
	v_fmac_f32_e32 v172, v10, v165
	v_fmac_f32_e32 v171, v3, v168
	v_fmac_f32_e32 v175, v154, v202
	v_fmac_f32_e32 v173, v18, v194
	v_fmac_f32_e32 v172, v11, v167
	v_fmac_f32_e32 v171, v4, v166
	v_fmac_f32_e32 v175, v155, v201
	v_fmac_f32_e32 v173, v19, v196
	v_fmac_f32_e32 v172, v12, v174
	v_fmac_f32_e32 v171, v5, v161
	v_fmac_f32_e32 v175, v156, v200
	v_fmac_f32_e32 v173, v20, v198
	v_fmac_f32_e32 v172, v13, v176
	v_fmac_f32_e32 v171, v6, v162
	v_fmac_f32_e32 v178, v5, v170
	v_fmac_f32_e32 v175, v157, v199
	v_fmac_f32_e32 v173, v21, v205
	v_fmac_f32_e32 v172, v14, v177
	v_fmac_f32_e32 v171, v7, v163
	v_fma_f32 v170, v0, v170, v160
	s_waitcnt lgkmcnt(0)
	v_lshlrev_b32_e32 v195, 16, v195
	v_fmac_f32_e32 v175, v158, v197
	v_fmac_f32_e32 v173, v22, v204
	v_fmac_f32_e32 v172, v15, v192
	v_fmac_f32_e32 v171, v8, v164
	v_fmac_f32_e32 v170, v1, v169
	v_fmac_f32_e32 v175, v159, v195
	v_fmac_f32_e32 v173, v23, v203
	v_fmac_f32_e32 v172, v16, v193
	v_fmac_f32_e32 v171, v9, v165
	v_fmac_f32_e32 v170, v2, v168
	ds_write_b32 v101, v175
	ds_read_u16 v175, v35 offset:57344
	v_fmac_f32_e32 v173, v152, v202
	v_fmac_f32_e32 v172, v17, v194
	v_fmac_f32_e32 v171, v10, v167
	v_fmac_f32_e32 v170, v3, v166
	v_fmac_f32_e32 v173, v154, v201
	v_fmac_f32_e32 v172, v18, v196
	v_fmac_f32_e32 v171, v11, v174
	v_fmac_f32_e32 v170, v4, v161
	v_fmac_f32_e32 v173, v155, v200
	v_fmac_f32_e32 v172, v19, v198
	v_fmac_f32_e32 v171, v12, v176
	v_fmac_f32_e32 v170, v5, v162
	v_fmac_f32_e32 v173, v156, v199
	v_fmac_f32_e32 v172, v20, v205
	v_fmac_f32_e32 v171, v13, v177
	v_fmac_f32_e32 v170, v6, v163
	v_fmac_f32_e32 v178, v6, v169
	v_fmac_f32_e32 v173, v157, v197
	v_fmac_f32_e32 v172, v21, v204
	v_fmac_f32_e32 v171, v14, v192
	v_fmac_f32_e32 v170, v7, v164
	v_fma_f32 v169, v0, v169, v160
	s_waitcnt lgkmcnt(0)
	v_lshlrev_b32_e32 v175, 16, v175
	v_fmac_f32_e32 v173, v158, v195
	v_fmac_f32_e32 v172, v22, v203
	v_fmac_f32_e32 v171, v15, v193
	v_fmac_f32_e32 v170, v8, v165
	v_fmac_f32_e32 v169, v1, v168
	v_fmac_f32_e32 v173, v159, v175
	v_fmac_f32_e32 v172, v23, v202
	v_fmac_f32_e32 v171, v16, v194
	v_fmac_f32_e32 v170, v9, v167
	v_fmac_f32_e32 v169, v2, v166
	ds_write_b32 v102, v173
	ds_read_u16 v173, v35 offset:58368
	v_fmac_f32_e32 v172, v152, v201
	v_fmac_f32_e32 v171, v17, v196
	v_fmac_f32_e32 v170, v10, v174
	v_fmac_f32_e32 v169, v3, v161
	v_fmac_f32_e32 v172, v154, v200
	v_fmac_f32_e32 v171, v18, v198
	v_fmac_f32_e32 v170, v11, v176
	v_fmac_f32_e32 v169, v4, v162
	v_fmac_f32_e32 v172, v155, v199
	v_fmac_f32_e32 v171, v19, v205
	v_fmac_f32_e32 v170, v12, v177
	v_fmac_f32_e32 v169, v5, v163
	v_fmac_f32_e32 v172, v156, v197
	v_fmac_f32_e32 v171, v20, v204
	v_fmac_f32_e32 v170, v13, v192
	v_fmac_f32_e32 v169, v6, v164
	v_fmac_f32_e32 v178, v7, v168
	v_fmac_f32_e32 v172, v157, v195
	v_fmac_f32_e32 v171, v21, v203
	v_fmac_f32_e32 v170, v14, v193
	v_fmac_f32_e32 v169, v7, v165
	v_fma_f32 v168, v0, v168, v160
	s_waitcnt lgkmcnt(0)
; __device__ __forceinline__ void phase_even_mix(CArgs a, LAS unsigned char* lds, int i2, int wv, int xw  ) {
;     ...
;             for (int r = 0; r < 64; ++r) {
;                 win[r % 34] = bf2f(glu[r * 512 + c]);
;                 if (r >= 32) { float y = cb;
; #pragma unroll
;                     for (int k = 0; k < 31; ++k) y += w[k] * win[(r - 30 + k) % 34];
;                     ybuf[(r - 32) * 512 + c] = y; }
;             }
;         }
;         __syncthreads();
; #pragma unroll
;         for (int it = 0; it < 6; ++it) { const int item = it * NTHR + tid, tt = item >> 6, cg = item & 63, p = t0 - 16 + tt;
	v_lshlrev_b32_e32 v173, 16, v173
	v_fmac_f32_e32 v172, v158, v175
	v_fmac_f32_e32 v171, v22, v202
	v_fmac_f32_e32 v170, v15, v194
	v_fmac_f32_e32 v169, v8, v167
	v_fmac_f32_e32 v168, v1, v166
	v_fmac_f32_e32 v172, v159, v173
	v_fmac_f32_e32 v171, v23, v201
	v_fmac_f32_e32 v170, v16, v196
	v_fmac_f32_e32 v169, v9, v174
	v_fmac_f32_e32 v168, v2, v161
	ds_write_b32 v103, v172
	ds_read_u16 v172, v35 offset:59392
	v_fmac_f32_e32 v171, v152, v200
	v_fmac_f32_e32 v170, v17, v198
	v_fmac_f32_e32 v169, v10, v176
	v_fmac_f32_e32 v168, v3, v162
	v_fmac_f32_e32 v171, v154, v199
	v_fmac_f32_e32 v170, v18, v205
	v_fmac_f32_e32 v169, v11, v177
	v_fmac_f32_e32 v168, v4, v163
	v_fmac_f32_e32 v171, v155, v197
	v_fmac_f32_e32 v170, v19, v204
	v_fmac_f32_e32 v169, v12, v192
	v_fmac_f32_e32 v168, v5, v164
	v_fmac_f32_e32 v171, v156, v195
	v_fmac_f32_e32 v170, v20, v203
	v_fmac_f32_e32 v169, v13, v193
	v_fmac_f32_e32 v168, v6, v165
	v_fmac_f32_e32 v178, v8, v166
	v_fmac_f32_e32 v171, v157, v175
	v_fmac_f32_e32 v170, v21, v202
	v_fmac_f32_e32 v169, v14, v194
	v_fmac_f32_e32 v168, v7, v167
	v_fma_f32 v166, v0, v166, v160
	s_waitcnt lgkmcnt(0)
	v_lshlrev_b32_e32 v172, 16, v172
	v_fmac_f32_e32 v171, v158, v173
	v_fmac_f32_e32 v170, v22, v201
	v_fmac_f32_e32 v169, v15, v196
	v_fmac_f32_e32 v168, v8, v174
	v_fmac_f32_e32 v166, v1, v161
	v_fmac_f32_e32 v171, v159, v172
	v_fmac_f32_e32 v170, v23, v200
	v_fmac_f32_e32 v169, v16, v198
	v_fmac_f32_e32 v168, v9, v176
	v_fmac_f32_e32 v166, v2, v162
	ds_write_b32 v104, v171
	ds_read_u16 v171, v35 offset:60416
	v_fmac_f32_e32 v170, v152, v199
	v_fmac_f32_e32 v169, v17, v205
	v_fmac_f32_e32 v168, v10, v177
	v_fmac_f32_e32 v166, v3, v163
	v_fmac_f32_e32 v170, v154, v197
	v_fmac_f32_e32 v169, v18, v204
	v_fmac_f32_e32 v168, v11, v192
	v_fmac_f32_e32 v166, v4, v164
	v_fmac_f32_e32 v170, v155, v195
	v_fmac_f32_e32 v169, v19, v203
	v_fmac_f32_e32 v168, v12, v193
	v_fmac_f32_e32 v166, v5, v165
	v_fmac_f32_e32 v170, v156, v175
	v_fmac_f32_e32 v169, v20, v202
	v_fmac_f32_e32 v168, v13, v194
	v_fmac_f32_e32 v166, v6, v167
	v_fmac_f32_e32 v170, v157, v173
	v_fmac_f32_e32 v169, v21, v201
	v_fmac_f32_e32 v168, v14, v196
	v_fmac_f32_e32 v166, v7, v174
	v_fmac_f32_e32 v160, v0, v161
	s_waitcnt lgkmcnt(0)
	v_lshlrev_b32_e32 v171, 16, v171
	v_fmac_f32_e32 v170, v158, v172
	v_fmac_f32_e32 v169, v22, v200
	v_fmac_f32_e32 v168, v15, v198
	v_fmac_f32_e32 v166, v8, v176
	v_fmac_f32_e32 v160, v1, v162
	v_fmac_f32_e32 v170, v159, v171
	v_fmac_f32_e32 v169, v23, v199
	v_fmac_f32_e32 v168, v16, v205
	v_fmac_f32_e32 v166, v9, v177
	v_fmac_f32_e32 v160, v2, v163
	ds_write_b32 v105, v170
	ds_read_u16 v170, v35 offset:61440
	v_fmac_f32_e32 v169, v152, v197
	v_fmac_f32_e32 v168, v17, v204
	v_fmac_f32_e32 v166, v10, v192
	v_fmac_f32_e32 v160, v3, v164
	v_fmac_f32_e32 v169, v154, v195
	v_fmac_f32_e32 v168, v18, v203
	v_fmac_f32_e32 v166, v11, v193
	v_fmac_f32_e32 v160, v4, v165
	v_fmac_f32_e32 v169, v155, v175
	v_fmac_f32_e32 v168, v19, v202
	v_fmac_f32_e32 v166, v12, v194
	v_fmac_f32_e32 v160, v5, v167
	v_fmac_f32_e32 v169, v156, v173
	v_fmac_f32_e32 v168, v20, v201
	v_fmac_f32_e32 v166, v13, v196
	v_fmac_f32_e32 v160, v6, v174
	v_fmac_f32_e32 v169, v157, v172
	v_fmac_f32_e32 v168, v21, v200
	v_fmac_f32_e32 v166, v14, v198
	v_fmac_f32_e32 v160, v7, v176
	s_waitcnt lgkmcnt(0)
	v_lshlrev_b32_e32 v170, 16, v170
	v_fmac_f32_e32 v169, v158, v171
	v_fmac_f32_e32 v168, v22, v199
	v_fmac_f32_e32 v166, v15, v205
	v_fmac_f32_e32 v160, v8, v177
	v_fmac_f32_e32 v178, v9, v161
	v_fmac_f32_e32 v169, v159, v170
	v_fmac_f32_e32 v168, v23, v197
	v_fmac_f32_e32 v166, v16, v204
	v_fmac_f32_e32 v160, v9, v192
	v_fmac_f32_e32 v178, v10, v162
	ds_write_b32 v106, v169
	ds_read_u16 v169, v35 offset:62464
	v_fmac_f32_e32 v168, v152, v195
	v_fmac_f32_e32 v166, v17, v203
	v_fmac_f32_e32 v160, v10, v193
	v_fmac_f32_e32 v178, v11, v163
	v_fmac_f32_e32 v168, v154, v175
	v_fmac_f32_e32 v166, v18, v202
	v_fmac_f32_e32 v160, v11, v194
	v_fmac_f32_e32 v178, v12, v164
	v_fmac_f32_e32 v168, v155, v173
	v_fmac_f32_e32 v166, v19, v201
	v_fmac_f32_e32 v160, v12, v196
	v_fmac_f32_e32 v178, v13, v165
	v_fmac_f32_e32 v168, v156, v172
	v_fmac_f32_e32 v166, v20, v200
	v_fmac_f32_e32 v160, v13, v198
	v_fmac_f32_e32 v178, v14, v167
	v_fmac_f32_e32 v168, v157, v171
	v_fmac_f32_e32 v166, v21, v199
	v_fmac_f32_e32 v160, v14, v205
	v_fmac_f32_e32 v178, v15, v174
	s_waitcnt lgkmcnt(0)
	v_lshlrev_b32_e32 v169, 16, v169
	v_fmac_f32_e32 v168, v158, v170
	v_fmac_f32_e32 v166, v22, v197
	v_fmac_f32_e32 v160, v15, v204
	v_fmac_f32_e32 v178, v16, v176
	v_fmac_f32_e32 v168, v159, v169
	v_fmac_f32_e32 v166, v23, v195
	v_fmac_f32_e32 v160, v16, v203
	v_fmac_f32_e32 v178, v17, v177
	ds_write_b32 v107, v168
	ds_read_u16 v168, v35 offset:63488
	v_fmac_f32_e32 v166, v152, v175
	v_fmac_f32_e32 v160, v17, v202
	v_fmac_f32_e32 v178, v18, v192
	v_fmac_f32_e32 v166, v154, v173
	v_fmac_f32_e32 v160, v18, v201
	v_fmac_f32_e32 v178, v19, v193
	v_fmac_f32_e32 v166, v155, v172
	v_fmac_f32_e32 v160, v19, v200
	v_fmac_f32_e32 v178, v20, v194
	v_fmac_f32_e32 v166, v156, v171
	v_fmac_f32_e32 v160, v20, v199
	v_fmac_f32_e32 v178, v21, v196
	v_fmac_f32_e32 v166, v157, v170
	v_fmac_f32_e32 v160, v21, v197
	v_fmac_f32_e32 v178, v22, v198
	s_waitcnt lgkmcnt(0)
	v_lshlrev_b32_e32 v168, 16, v168
	v_fmac_f32_e32 v166, v158, v169
	v_fmac_f32_e32 v160, v22, v195
	v_fmac_f32_e32 v178, v23, v205
	v_fmac_f32_e32 v166, v159, v168
	v_fmac_f32_e32 v160, v23, v175
	v_fmac_f32_e32 v178, v152, v204
	ds_write_b32 v108, v166
	ds_read_u16 v166, v35 offset:64512
	v_fmac_f32_e32 v160, v152, v173
	v_fmac_f32_e32 v178, v154, v203
	v_fmac_f32_e32 v160, v154, v172
	v_fmac_f32_e32 v178, v155, v202
	v_fmac_f32_e32 v160, v155, v171
	v_fmac_f32_e32 v178, v156, v201
	v_fmac_f32_e32 v160, v156, v170
	v_fmac_f32_e32 v178, v157, v200
	v_fmac_f32_e32 v160, v157, v169
	v_fmac_f32_e32 v178, v158, v199
	s_waitcnt lgkmcnt(0)
	v_lshlrev_b32_e32 v166, 16, v166
	v_fmac_f32_e32 v160, v158, v168
	v_add_u32_e32 v152, s19, v69
	v_fmac_f32_e32 v178, v159, v197
	v_fmac_f32_e32 v160, v159, v166
	v_cmp_lt_i32_e32 vcc, -1, v152
	v_mov_b32_e32 v0, 0
	v_mov_b32_e32 v2, 0
	v_mov_b32_e32 v3, 0
	v_mov_b32_e32 v4, 0
	v_mov_b32_e32 v5, 0
	ds_write_b32 v100, v178
	ds_write_b32 v109, v160
	s_waitcnt lgkmcnt(0)
	s_barrier
; #define LAS __attribute__((address_space(3)))
; __device__ __forceinline__ void phase_even_mix(CArgs a, LAS unsigned char* lds, int i2, int wv, int xw  ) {
;     ...
;         for (int it = 0; it < 6; ++it) { const int item = it * NTHR + tid, tt = item >> 6, cg = item & 63, p = t0 - 16 + tt;
;             u32x4 o = (u32x4){0u, 0u, 0u, 0u};
;             if (p >= 0) o = *(const u32x4*)(HB + ((size_t)b * SEQ + p) * EVEN_IN + cg * 8);
;             *(LAS u32x4*)(glu + tt * 512 + cg * 8) = o; }
	v_add_u32_e32 v152, s19, v69
	v_mov_b32_e32 v200, 0
	v_cmp_lt_i32_e32 vcc, -1, v152
	v_mov_b32_e32 v201, 0
	v_mov_b32_e32 v202, 0
	v_mov_b32_e32 v203, 0
	s_nop 0
	s_and_saveexec_b64 s[16:17], vcc
	v_lshl_add_u64 v[0:1], s[92:93], 0, v[152:153]
	v_mad_u64_u32 v[2:3], s[22:23], v0, s53, v[24:25]
	v_mad_i32_i24 v3, v1, s53, v3
	global_load_dwordx4 v[200:203], v[2:3], off
	s_or_b64 exec, exec, s[16:17]
	v_add_u32_e32 v152, s19, v70
	v_mov_b32_e32 v204, 0
	v_cmp_lt_i32_e32 vcc, -1, v152
	v_mov_b32_e32 v205, 0
	v_mov_b32_e32 v206, 0
	v_mov_b32_e32 v207, 0
	s_nop 0
	s_and_saveexec_b64 s[16:17], vcc
	v_lshl_add_u64 v[0:1], s[92:93], 0, v[152:153]
	v_mad_u64_u32 v[2:3], s[22:23], v0, s53, v[24:25]
	v_mad_i32_i24 v3, v1, s53, v3
	global_load_dwordx4 v[204:207], v[2:3], off
	s_or_b64 exec, exec, s[16:17]
	v_add_u32_e32 v152, s19, v71
	v_mov_b32_e32 v208, 0
	v_cmp_lt_i32_e32 vcc, -1, v152
	v_mov_b32_e32 v209, 0
	v_mov_b32_e32 v210, 0
	v_mov_b32_e32 v211, 0
	s_nop 0
	s_and_saveexec_b64 s[16:17], vcc
	v_lshl_add_u64 v[0:1], s[92:93], 0, v[152:153]
	v_mad_u64_u32 v[2:3], s[22:23], v0, s53, v[24:25]
	v_mad_i32_i24 v3, v1, s53, v3
	global_load_dwordx4 v[208:211], v[2:3], off
	s_or_b64 exec, exec, s[16:17]
	v_add_u32_e32 v152, s19, v72
	v_mov_b32_e32 v212, 0
	v_cmp_lt_i32_e32 vcc, -1, v152
	v_mov_b32_e32 v213, 0
	v_mov_b32_e32 v214, 0
	v_mov_b32_e32 v215, 0
	s_nop 0
	s_and_saveexec_b64 s[16:17], vcc
	v_lshl_add_u64 v[0:1], s[92:93], 0, v[152:153]
	v_mad_u64_u32 v[2:3], s[22:23], v0, s53, v[24:25]
	v_mad_i32_i24 v3, v1, s53, v3
	global_load_dwordx4 v[212:215], v[2:3], off
	s_or_b64 exec, exec, s[16:17]
	v_add_u32_e32 v152, s19, v73
	v_mov_b32_e32 v216, 0
	v_cmp_lt_i32_e32 vcc, -1, v152
	v_mov_b32_e32 v217, 0
	v_mov_b32_e32 v218, 0
	v_mov_b32_e32 v219, 0
	s_nop 0
	s_and_saveexec_b64 s[16:17], vcc
	v_lshl_add_u64 v[0:1], s[92:93], 0, v[152:153]
	v_mad_u64_u32 v[2:3], s[22:23], v0, s53, v[24:25]
	v_mad_i32_i24 v3, v1, s53, v3
	global_load_dwordx4 v[216:219], v[2:3], off
	s_or_b64 exec, exec, s[16:17]
	v_add_u32_e32 v152, s19, v74
	v_mov_b32_e32 v220, 0
	v_cmp_lt_i32_e32 vcc, -1, v152
	v_mov_b32_e32 v221, 0
	v_mov_b32_e32 v222, 0
	v_mov_b32_e32 v223, 0
	s_nop 0
	s_and_saveexec_b64 s[16:17], vcc
	v_lshl_add_u64 v[0:1], s[92:93], 0, v[152:153]
	v_mad_u64_u32 v[2:3], s[22:23], v0, s53, v[24:25]
	v_mad_i32_i24 v3, v1, s53, v3
	global_load_dwordx4 v[220:223], v[2:3], off
	s_or_b64 exec, exec, s[16:17]
	s_waitcnt vmcnt(5)
	ds_write_b128 v146, v[200:203]
	s_waitcnt vmcnt(4)
	ds_write_b128 v147, v[204:207]
	s_waitcnt vmcnt(3)
	ds_write_b128 v148, v[208:211]
	s_waitcnt vmcnt(2)
	ds_write_b128 v149, v[212:215]
	s_waitcnt vmcnt(1)
	ds_write_b128 v150, v[216:219]
	s_waitcnt vmcnt(0)
	ds_write_b128 v151, v[220:223]
	s_branch .LBB0_460
